# quad-local handoff replaces grid barriers between out-proj, Q GEMM, attention, O GEMM; residual epilogues restructured
# speedup vs baseline: 1.0115x; 1.0109x over previous
.LBB0_883:
	s_add_u32 s0, s18, 0x4400
	s_addc_u32 s1, s19, 0
	v_mbcnt_hi_u32_b32 v0, -1, v217
	v_lshlrev_b32_e32 v1, 8, v0
	v_and_b32_e32 v1, 0x700, v1
	global_load_dword v2, v1, s[0:1] sc1
	v_mov_b32_e32 v3, 0x24a70
	ds_read_b32 v3, v3
	s_waitcnt vmcnt(0) lgkmcnt(0)
	s_getreg_b32 s0, hwreg(HW_REG_XCC_ID, 0, 4)
	v_cmp_eq_u32_e32 vcc, 32, v2
	s_nop 1
	s_cmp_eq_u64 vcc, exec
	s_cselect_b32 s100, 1, 0
	s_cmp_eq_u32 s38, 0x100
	s_cselect_b32 s100, s100, 0
	v_readfirstlane_b32 s1, v3
	s_nop 3
	s_lshl_b32 s98, s0, 3
	s_lshr_b32 s0, s1, 2
	s_add_i32 s98, s98, s0
	s_and_b32 s99, s1, 3
	s_cmp_lt_i32 s90, 6
	s_cselect_b64 s[0:1], -1, 0
	s_and_b64 s[4:5], s[0:1], s[2:3]
	s_andn2_b64 vcc, exec, s[4:5]
	s_cbranch_vccnz .LBB0_926
	s_and_b32 s0, s80, 0xffffffc0
	v_mbcnt_hi_u32_b32 v138, -1, v217
	v_add_u32_e32 v0, s0, v138
	s_cmpk_lt_i32 s6, 0x200
	v_mov_b32_e32 v1, v0
	s_mov_b64 s[0:1], s[86:87]
	s_mov_b64 s[2:3], s[18:19]
	s_waitcnt lgkmcnt(0)
	s_cselect_b64 s[8:9], -1, 0
	s_cmpk_gt_i32 s6, 0x1ff
	s_cbranch_scc1 .LBB0_890
	s_ashr_i32 s0, s6, 31
	s_lshr_b32 s0, s0, 29
	s_add_i32 s0, s6, s0
	s_and_b32 s1, s0, -8
	s_sub_i32 s1, s6, s1
	s_cmp_gt_i32 s1, -1
	s_cbranch_scc0 .LBB0_887
	s_lshl_b32 s7, s1, 6
	s_cbranch_execz .LBB0_888
	s_branch .LBB0_889

.LBB0_890:
	s_cmp_eq_u32 s100, 1
	s_cbranch_scc0 .Lqo_p3i
	s_lshl_b32 s59, s98, 1
	s_mov_b32 s58, s99

.LBB0_902:
	s_cmp_eq_u32 s100, 1
	s_cbranch_scc0 .Lqo_p3n
	s_lshl_b32 s1, s98, 1
	s_add_i32 s1, s1, s51
	s_mov_b32 s0, s99

.LBB0_906:
	s_lshl_b32 s14, s59, 8
	s_add_i32 s14, s14, s55
	s_lshl_b32 s15, s58, 8
	s_or_b32 s15, s15, s44
	v_and_b32_e32 v219, 15, v138
	v_or_b32_e32 v219, s14, v219
	v_and_b32_e32 v218, 48, v138
	v_add_u32_e32 v218, s15, v218
	v_lshl_add_u32 v235, v219, 10, v218
	v_lshlrev_b32_e32 v235, 1, v235
	v_lshlrev_b32_e32 v220, 2, v219
	v_add_lshl_u32 v137, v138, s14, 2
	v_add_u32_e32 v237, 0x8000, v235
	v_add_u32_e32 v239, 0x10000, v235
	v_add_u32_e32 v241, 0x18000, v235
	v_add_u32_e32 v243, 0x40000, v235
	v_add_u32_e32 v245, 0x48000, v235
	v_add_u32_e32 v247, 0x50000, v235
	v_add_u32_e32 v249, 0x58000, v235
	global_load_dwordx4 v[132:135], v235, s[28:29]
	global_load_dwordx4 v[148:151], v235, s[28:29] offset:16
	global_load_dword v234, v220, s[22:23]
	global_load_dwordx4 v[152:155], v237, s[28:29]
	global_load_dwordx4 v[156:159], v237, s[28:29] offset:16
	global_load_dword v236, v220, s[22:23] offset:64
	global_load_dwordx4 v[160:163], v239, s[28:29]
	global_load_dwordx4 v[164:167], v239, s[28:29] offset:16
	global_load_dword v238, v220, s[22:23] offset:128
	global_load_dwordx4 v[168:171], v241, s[28:29]
	global_load_dwordx4 v[172:175], v241, s[28:29] offset:16
	global_load_dword v240, v220, s[22:23] offset:192
	global_load_dwordx4 v[176:179], v243, s[28:29]
	global_load_dwordx4 v[180:183], v243, s[28:29] offset:16
	global_load_dword v242, v220, s[22:23] offset:512
	global_load_dwordx4 v[184:187], v245, s[28:29]
	global_load_dwordx4 v[188:191], v245, s[28:29] offset:16
	global_load_dword v244, v220, s[22:23] offset:576
	global_load_dwordx4 v[192:195], v247, s[28:29]
	global_load_dwordx4 v[196:199], v247, s[28:29] offset:16
	global_load_dword v246, v220, s[22:23] offset:640
	global_load_dwordx4 v[200:203], v249, s[28:29]
	global_load_dwordx4 v[204:207], v249, s[28:29] offset:16
	global_load_dword v248, v220, s[22:23] offset:704
	s_waitcnt vmcnt(21)
	v_lshlrev_b32_e32 v218, 16, v132
	v_and_b32_e32 v219, 0xffff0000, v132
	v_lshlrev_b32_e32 v220, 16, v133
	v_and_b32_e32 v221, 0xffff0000, v133
	v_lshlrev_b32_e32 v222, 16, v134
	v_and_b32_e32 v223, 0xffff0000, v134
	v_lshlrev_b32_e32 v224, 16, v135
	v_and_b32_e32 v225, 0xffff0000, v135
	v_lshlrev_b32_e32 v226, 16, v148
	v_and_b32_e32 v227, 0xffff0000, v148
	v_lshlrev_b32_e32 v228, 16, v149
	v_and_b32_e32 v229, 0xffff0000, v149
	v_lshlrev_b32_e32 v230, 16, v150
	v_and_b32_e32 v231, 0xffff0000, v150
	v_lshlrev_b32_e32 v232, 16, v151
	v_and_b32_e32 v233, 0xffff0000, v151
	v_pk_fma_f32 v[112:113], v[234:235], v[218:219], v[112:113] op_sel_hi:[0,1,1]
	v_pk_fma_f32 v[114:115], v[234:235], v[220:221], v[114:115] op_sel_hi:[0,1,1]
	v_pk_fma_f32 v[116:117], v[234:235], v[222:223], v[116:117] op_sel_hi:[0,1,1]
	v_pk_fma_f32 v[118:119], v[234:235], v[224:225], v[118:119] op_sel_hi:[0,1,1]
	v_pk_fma_f32 v[124:125], v[234:235], v[226:227], v[124:125] op_sel_hi:[0,1,1]
	v_pk_fma_f32 v[126:127], v[234:235], v[228:229], v[126:127] op_sel_hi:[0,1,1]
	v_pk_fma_f32 v[120:121], v[234:235], v[230:231], v[120:121] op_sel_hi:[0,1,1]
	v_pk_fma_f32 v[122:123], v[234:235], v[232:233], v[122:123] op_sel_hi:[0,1,1]
	v_mul_f32_e32 v132, v112, v112
	v_fmac_f32_e32 v132, v113, v113
	v_mul_f32_e32 v219, v114, v114
	v_fmac_f32_e32 v219, v115, v115
	v_mul_f32_e32 v220, v116, v116
	v_fmac_f32_e32 v220, v117, v117
	v_mul_f32_e32 v218, v118, v118
	v_fmac_f32_e32 v218, v119, v119
	v_fmac_f32_e32 v132, v124, v124
	v_fmac_f32_e32 v132, v125, v125
	v_fmac_f32_e32 v219, v126, v126
	v_fmac_f32_e32 v219, v127, v127
	v_fmac_f32_e32 v220, v120, v120
	v_fmac_f32_e32 v220, v121, v121
	v_fmac_f32_e32 v218, v122, v122
	v_fmac_f32_e32 v218, v123, v123
	v_add_f32_e32 v132, v132, v219
	v_add_f32_e32 v220, v220, v218
	v_add_f32_e32 v132, v132, v220
	v_cvt_pk_bf16_f32 v208, v112, v113
	v_cvt_pk_bf16_f32 v209, v114, v115
	v_cvt_pk_bf16_f32 v210, v116, v117
	v_cvt_pk_bf16_f32 v211, v118, v119
	v_cvt_pk_bf16_f32 v212, v124, v125
	v_cvt_pk_bf16_f32 v213, v126, v127
	v_cvt_pk_bf16_f32 v214, v120, v121
	v_cvt_pk_bf16_f32 v215, v122, v123
	global_store_dwordx4 v235, v[208:211], s[24:25]
	global_store_dwordx4 v235, v[212:215], s[24:25] offset:16
	s_waitcnt vmcnt(20)
	v_lshlrev_b32_e32 v218, 16, v152
	v_and_b32_e32 v219, 0xffff0000, v152
	v_lshlrev_b32_e32 v220, 16, v153
	v_and_b32_e32 v221, 0xffff0000, v153
	v_lshlrev_b32_e32 v222, 16, v154
	v_and_b32_e32 v223, 0xffff0000, v154
	v_lshlrev_b32_e32 v224, 16, v155
	v_and_b32_e32 v225, 0xffff0000, v155
	v_lshlrev_b32_e32 v226, 16, v156
	v_and_b32_e32 v227, 0xffff0000, v156
	v_lshlrev_b32_e32 v228, 16, v157
	v_and_b32_e32 v229, 0xffff0000, v157
	v_lshlrev_b32_e32 v230, 16, v158
	v_and_b32_e32 v231, 0xffff0000, v158
	v_lshlrev_b32_e32 v232, 16, v159
	v_and_b32_e32 v233, 0xffff0000, v159
	v_pk_fma_f32 v[96:97], v[236:237], v[218:219], v[96:97] op_sel_hi:[0,1,1]
	v_pk_fma_f32 v[98:99], v[236:237], v[220:221], v[98:99] op_sel_hi:[0,1,1]
	v_pk_fma_f32 v[100:101], v[236:237], v[222:223], v[100:101] op_sel_hi:[0,1,1]
	v_pk_fma_f32 v[102:103], v[236:237], v[224:225], v[102:103] op_sel_hi:[0,1,1]
	v_pk_fma_f32 v[108:109], v[236:237], v[226:227], v[108:109] op_sel_hi:[0,1,1]
	v_pk_fma_f32 v[110:111], v[236:237], v[228:229], v[110:111] op_sel_hi:[0,1,1]
	v_pk_fma_f32 v[104:105], v[236:237], v[230:231], v[104:105] op_sel_hi:[0,1,1]
	v_pk_fma_f32 v[106:107], v[236:237], v[232:233], v[106:107] op_sel_hi:[0,1,1]
	v_mul_f32_e32 v152, v96, v96
	v_fmac_f32_e32 v152, v97, v97
	v_mul_f32_e32 v219, v98, v98
	v_fmac_f32_e32 v219, v99, v99
	v_mul_f32_e32 v220, v100, v100
	v_fmac_f32_e32 v220, v101, v101
	v_mul_f32_e32 v218, v102, v102
	v_fmac_f32_e32 v218, v103, v103
	v_fmac_f32_e32 v152, v108, v108
	v_fmac_f32_e32 v152, v109, v109
	v_fmac_f32_e32 v219, v110, v110
	v_fmac_f32_e32 v219, v111, v111
	v_fmac_f32_e32 v220, v104, v104
	v_fmac_f32_e32 v220, v105, v105
	v_fmac_f32_e32 v218, v106, v106
	v_fmac_f32_e32 v218, v107, v107
	v_add_f32_e32 v152, v152, v219
	v_add_f32_e32 v220, v220, v218
	v_add_f32_e32 v152, v152, v220
	v_cvt_pk_bf16_f32 v208, v96, v97
	v_cvt_pk_bf16_f32 v209, v98, v99
	v_cvt_pk_bf16_f32 v210, v100, v101
	v_cvt_pk_bf16_f32 v211, v102, v103
	v_cvt_pk_bf16_f32 v212, v108, v109
	v_cvt_pk_bf16_f32 v213, v110, v111
	v_cvt_pk_bf16_f32 v214, v104, v105
	v_cvt_pk_bf16_f32 v215, v106, v107
	global_store_dwordx4 v237, v[208:211], s[24:25]
	global_store_dwordx4 v237, v[212:215], s[24:25] offset:16
	s_waitcnt vmcnt(19)
	v_lshlrev_b32_e32 v218, 16, v160
	v_and_b32_e32 v219, 0xffff0000, v160
	v_lshlrev_b32_e32 v220, 16, v161
	v_and_b32_e32 v221, 0xffff0000, v161
	v_lshlrev_b32_e32 v222, 16, v162
	v_and_b32_e32 v223, 0xffff0000, v162
	v_lshlrev_b32_e32 v224, 16, v163
	v_and_b32_e32 v225, 0xffff0000, v163
	v_lshlrev_b32_e32 v226, 16, v164
	v_and_b32_e32 v227, 0xffff0000, v164
	v_lshlrev_b32_e32 v228, 16, v165
	v_and_b32_e32 v229, 0xffff0000, v165
	v_lshlrev_b32_e32 v230, 16, v166
	v_and_b32_e32 v231, 0xffff0000, v166
	v_lshlrev_b32_e32 v232, 16, v167
	v_and_b32_e32 v233, 0xffff0000, v167
	v_pk_fma_f32 v[80:81], v[238:239], v[218:219], v[80:81] op_sel_hi:[0,1,1]
	v_pk_fma_f32 v[82:83], v[238:239], v[220:221], v[82:83] op_sel_hi:[0,1,1]
	v_pk_fma_f32 v[84:85], v[238:239], v[222:223], v[84:85] op_sel_hi:[0,1,1]
	v_pk_fma_f32 v[86:87], v[238:239], v[224:225], v[86:87] op_sel_hi:[0,1,1]
	v_pk_fma_f32 v[92:93], v[238:239], v[226:227], v[92:93] op_sel_hi:[0,1,1]
	v_pk_fma_f32 v[94:95], v[238:239], v[228:229], v[94:95] op_sel_hi:[0,1,1]
	v_pk_fma_f32 v[88:89], v[238:239], v[230:231], v[88:89] op_sel_hi:[0,1,1]
	v_pk_fma_f32 v[90:91], v[238:239], v[232:233], v[90:91] op_sel_hi:[0,1,1]
	v_mul_f32_e32 v160, v80, v80
	v_fmac_f32_e32 v160, v81, v81
	v_mul_f32_e32 v219, v82, v82
	v_fmac_f32_e32 v219, v83, v83
	v_mul_f32_e32 v220, v84, v84
	v_fmac_f32_e32 v220, v85, v85
	v_mul_f32_e32 v218, v86, v86
	v_fmac_f32_e32 v218, v87, v87
	v_fmac_f32_e32 v160, v92, v92
	v_fmac_f32_e32 v160, v93, v93
	v_fmac_f32_e32 v219, v94, v94
	v_fmac_f32_e32 v219, v95, v95
	v_fmac_f32_e32 v220, v88, v88
	v_fmac_f32_e32 v220, v89, v89
	v_fmac_f32_e32 v218, v90, v90
	v_fmac_f32_e32 v218, v91, v91
	v_add_f32_e32 v160, v160, v219
	v_add_f32_e32 v220, v220, v218
	v_add_f32_e32 v160, v160, v220
	v_cvt_pk_bf16_f32 v208, v80, v81
	v_cvt_pk_bf16_f32 v209, v82, v83
	v_cvt_pk_bf16_f32 v210, v84, v85
	v_cvt_pk_bf16_f32 v211, v86, v87
	v_cvt_pk_bf16_f32 v212, v92, v93
	v_cvt_pk_bf16_f32 v213, v94, v95
	v_cvt_pk_bf16_f32 v214, v88, v89
	v_cvt_pk_bf16_f32 v215, v90, v91
	global_store_dwordx4 v239, v[208:211], s[24:25]
	global_store_dwordx4 v239, v[212:215], s[24:25] offset:16
	s_waitcnt vmcnt(18)
	v_lshlrev_b32_e32 v218, 16, v168
	v_and_b32_e32 v219, 0xffff0000, v168
	v_lshlrev_b32_e32 v220, 16, v169
	v_and_b32_e32 v221, 0xffff0000, v169
	v_lshlrev_b32_e32 v222, 16, v170
	v_and_b32_e32 v223, 0xffff0000, v170
	v_lshlrev_b32_e32 v224, 16, v171
	v_and_b32_e32 v225, 0xffff0000, v171
	v_lshlrev_b32_e32 v226, 16, v172
	v_and_b32_e32 v227, 0xffff0000, v172
	v_lshlrev_b32_e32 v228, 16, v173
	v_and_b32_e32 v229, 0xffff0000, v173
	v_lshlrev_b32_e32 v230, 16, v174
	v_and_b32_e32 v231, 0xffff0000, v174
	v_lshlrev_b32_e32 v232, 16, v175
	v_and_b32_e32 v233, 0xffff0000, v175
	v_pk_fma_f32 v[64:65], v[240:241], v[218:219], v[64:65] op_sel_hi:[0,1,1]
	v_pk_fma_f32 v[66:67], v[240:241], v[220:221], v[66:67] op_sel_hi:[0,1,1]
	v_pk_fma_f32 v[68:69], v[240:241], v[222:223], v[68:69] op_sel_hi:[0,1,1]
	v_pk_fma_f32 v[70:71], v[240:241], v[224:225], v[70:71] op_sel_hi:[0,1,1]
	v_pk_fma_f32 v[76:77], v[240:241], v[226:227], v[76:77] op_sel_hi:[0,1,1]
	v_pk_fma_f32 v[78:79], v[240:241], v[228:229], v[78:79] op_sel_hi:[0,1,1]
	v_pk_fma_f32 v[72:73], v[240:241], v[230:231], v[72:73] op_sel_hi:[0,1,1]
	v_pk_fma_f32 v[74:75], v[240:241], v[232:233], v[74:75] op_sel_hi:[0,1,1]
	v_mul_f32_e32 v168, v64, v64
	v_fmac_f32_e32 v168, v65, v65
	v_mul_f32_e32 v219, v66, v66
	v_fmac_f32_e32 v219, v67, v67
	v_mul_f32_e32 v220, v68, v68
	v_fmac_f32_e32 v220, v69, v69
	v_mul_f32_e32 v218, v70, v70
	v_fmac_f32_e32 v218, v71, v71
	v_fmac_f32_e32 v168, v76, v76
	v_fmac_f32_e32 v168, v77, v77
	v_fmac_f32_e32 v219, v78, v78
	v_fmac_f32_e32 v219, v79, v79
	v_fmac_f32_e32 v220, v72, v72
	v_fmac_f32_e32 v220, v73, v73
	v_fmac_f32_e32 v218, v74, v74
	v_fmac_f32_e32 v218, v75, v75
	v_add_f32_e32 v168, v168, v219
	v_add_f32_e32 v220, v220, v218
	v_add_f32_e32 v168, v168, v220
	v_cvt_pk_bf16_f32 v208, v64, v65
	v_cvt_pk_bf16_f32 v209, v66, v67
	v_cvt_pk_bf16_f32 v210, v68, v69
	v_cvt_pk_bf16_f32 v211, v70, v71
	v_cvt_pk_bf16_f32 v212, v76, v77
	v_cvt_pk_bf16_f32 v213, v78, v79
	v_cvt_pk_bf16_f32 v214, v72, v73
	v_cvt_pk_bf16_f32 v215, v74, v75
	global_store_dwordx4 v241, v[208:211], s[24:25]
	global_store_dwordx4 v241, v[212:215], s[24:25] offset:16
	s_waitcnt vmcnt(17)
	v_lshlrev_b32_e32 v218, 16, v176
	v_and_b32_e32 v219, 0xffff0000, v176
	v_lshlrev_b32_e32 v220, 16, v177
	v_and_b32_e32 v221, 0xffff0000, v177
	v_lshlrev_b32_e32 v222, 16, v178
	v_and_b32_e32 v223, 0xffff0000, v178
	v_lshlrev_b32_e32 v224, 16, v179
	v_and_b32_e32 v225, 0xffff0000, v179
	v_lshlrev_b32_e32 v226, 16, v180
	v_and_b32_e32 v227, 0xffff0000, v180
	v_lshlrev_b32_e32 v228, 16, v181
	v_and_b32_e32 v229, 0xffff0000, v181
	v_lshlrev_b32_e32 v230, 16, v182
	v_and_b32_e32 v231, 0xffff0000, v182
	v_lshlrev_b32_e32 v232, 16, v183
	v_and_b32_e32 v233, 0xffff0000, v183
	v_pk_fma_f32 v[48:49], v[242:243], v[218:219], v[48:49] op_sel_hi:[0,1,1]
	v_pk_fma_f32 v[50:51], v[242:243], v[220:221], v[50:51] op_sel_hi:[0,1,1]
	v_pk_fma_f32 v[52:53], v[242:243], v[222:223], v[52:53] op_sel_hi:[0,1,1]
	v_pk_fma_f32 v[54:55], v[242:243], v[224:225], v[54:55] op_sel_hi:[0,1,1]
	v_pk_fma_f32 v[60:61], v[242:243], v[226:227], v[60:61] op_sel_hi:[0,1,1]
	v_pk_fma_f32 v[62:63], v[242:243], v[228:229], v[62:63] op_sel_hi:[0,1,1]
	v_pk_fma_f32 v[56:57], v[242:243], v[230:231], v[56:57] op_sel_hi:[0,1,1]
	v_pk_fma_f32 v[58:59], v[242:243], v[232:233], v[58:59] op_sel_hi:[0,1,1]
	v_mul_f32_e32 v176, v48, v48
	v_fmac_f32_e32 v176, v49, v49
	v_mul_f32_e32 v219, v50, v50
	v_fmac_f32_e32 v219, v51, v51
	v_mul_f32_e32 v220, v52, v52
	v_fmac_f32_e32 v220, v53, v53
	v_mul_f32_e32 v218, v54, v54
	v_fmac_f32_e32 v218, v55, v55
	v_fmac_f32_e32 v176, v60, v60
	v_fmac_f32_e32 v176, v61, v61
	v_fmac_f32_e32 v219, v62, v62
	v_fmac_f32_e32 v219, v63, v63
	v_fmac_f32_e32 v220, v56, v56
	v_fmac_f32_e32 v220, v57, v57
	v_fmac_f32_e32 v218, v58, v58
	v_fmac_f32_e32 v218, v59, v59
	v_add_f32_e32 v176, v176, v219
	v_add_f32_e32 v220, v220, v218
	v_add_f32_e32 v176, v176, v220
	v_cvt_pk_bf16_f32 v208, v48, v49
	v_cvt_pk_bf16_f32 v209, v50, v51
	v_cvt_pk_bf16_f32 v210, v52, v53
	v_cvt_pk_bf16_f32 v211, v54, v55
	v_cvt_pk_bf16_f32 v212, v60, v61
	v_cvt_pk_bf16_f32 v213, v62, v63
	v_cvt_pk_bf16_f32 v214, v56, v57
	v_cvt_pk_bf16_f32 v215, v58, v59
	global_store_dwordx4 v243, v[208:211], s[24:25]
	global_store_dwordx4 v243, v[212:215], s[24:25] offset:16
	s_waitcnt vmcnt(16)
	v_lshlrev_b32_e32 v218, 16, v184
	v_and_b32_e32 v219, 0xffff0000, v184
	v_lshlrev_b32_e32 v220, 16, v185
	v_and_b32_e32 v221, 0xffff0000, v185
	v_lshlrev_b32_e32 v222, 16, v186
	v_and_b32_e32 v223, 0xffff0000, v186
	v_lshlrev_b32_e32 v224, 16, v187
	v_and_b32_e32 v225, 0xffff0000, v187
	v_lshlrev_b32_e32 v226, 16, v188
	v_and_b32_e32 v227, 0xffff0000, v188
	v_lshlrev_b32_e32 v228, 16, v189
	v_and_b32_e32 v229, 0xffff0000, v189
	v_lshlrev_b32_e32 v230, 16, v190
	v_and_b32_e32 v231, 0xffff0000, v190
	v_lshlrev_b32_e32 v232, 16, v191
	v_and_b32_e32 v233, 0xffff0000, v191
	v_pk_fma_f32 v[32:33], v[244:245], v[218:219], v[32:33] op_sel_hi:[0,1,1]
	v_pk_fma_f32 v[34:35], v[244:245], v[220:221], v[34:35] op_sel_hi:[0,1,1]
	v_pk_fma_f32 v[36:37], v[244:245], v[222:223], v[36:37] op_sel_hi:[0,1,1]
	v_pk_fma_f32 v[38:39], v[244:245], v[224:225], v[38:39] op_sel_hi:[0,1,1]
	v_pk_fma_f32 v[44:45], v[244:245], v[226:227], v[44:45] op_sel_hi:[0,1,1]
	v_pk_fma_f32 v[46:47], v[244:245], v[228:229], v[46:47] op_sel_hi:[0,1,1]
	v_pk_fma_f32 v[40:41], v[244:245], v[230:231], v[40:41] op_sel_hi:[0,1,1]
	v_pk_fma_f32 v[42:43], v[244:245], v[232:233], v[42:43] op_sel_hi:[0,1,1]
	v_mul_f32_e32 v184, v32, v32
	v_fmac_f32_e32 v184, v33, v33
	v_mul_f32_e32 v219, v34, v34
	v_fmac_f32_e32 v219, v35, v35
	v_mul_f32_e32 v220, v36, v36
	v_fmac_f32_e32 v220, v37, v37
	v_mul_f32_e32 v218, v38, v38
	v_fmac_f32_e32 v218, v39, v39
	v_fmac_f32_e32 v184, v44, v44
	v_fmac_f32_e32 v184, v45, v45
	v_fmac_f32_e32 v219, v46, v46
	v_fmac_f32_e32 v219, v47, v47
	v_fmac_f32_e32 v220, v40, v40
	v_fmac_f32_e32 v220, v41, v41
	v_fmac_f32_e32 v218, v42, v42
	v_fmac_f32_e32 v218, v43, v43
	v_add_f32_e32 v184, v184, v219
	v_add_f32_e32 v220, v220, v218
	v_add_f32_e32 v184, v184, v220
	v_cvt_pk_bf16_f32 v208, v32, v33
	v_cvt_pk_bf16_f32 v209, v34, v35
	v_cvt_pk_bf16_f32 v210, v36, v37
	v_cvt_pk_bf16_f32 v211, v38, v39
	v_cvt_pk_bf16_f32 v212, v44, v45
	v_cvt_pk_bf16_f32 v213, v46, v47
	v_cvt_pk_bf16_f32 v214, v40, v41
	v_cvt_pk_bf16_f32 v215, v42, v43
	global_store_dwordx4 v245, v[208:211], s[24:25]
	global_store_dwordx4 v245, v[212:215], s[24:25] offset:16
	s_waitcnt vmcnt(15)
	v_lshlrev_b32_e32 v218, 16, v192
	v_and_b32_e32 v219, 0xffff0000, v192
	v_lshlrev_b32_e32 v220, 16, v193
	v_and_b32_e32 v221, 0xffff0000, v193
	v_lshlrev_b32_e32 v222, 16, v194
	v_and_b32_e32 v223, 0xffff0000, v194
	v_lshlrev_b32_e32 v224, 16, v195
	v_and_b32_e32 v225, 0xffff0000, v195
	v_lshlrev_b32_e32 v226, 16, v196
	v_and_b32_e32 v227, 0xffff0000, v196
	v_lshlrev_b32_e32 v228, 16, v197
	v_and_b32_e32 v229, 0xffff0000, v197
	v_lshlrev_b32_e32 v230, 16, v198
	v_and_b32_e32 v231, 0xffff0000, v198
	v_lshlrev_b32_e32 v232, 16, v199
	v_and_b32_e32 v233, 0xffff0000, v199
	v_pk_fma_f32 v[16:17], v[246:247], v[218:219], v[16:17] op_sel_hi:[0,1,1]
	v_pk_fma_f32 v[18:19], v[246:247], v[220:221], v[18:19] op_sel_hi:[0,1,1]
	v_pk_fma_f32 v[20:21], v[246:247], v[222:223], v[20:21] op_sel_hi:[0,1,1]
	v_pk_fma_f32 v[22:23], v[246:247], v[224:225], v[22:23] op_sel_hi:[0,1,1]
	v_pk_fma_f32 v[28:29], v[246:247], v[226:227], v[28:29] op_sel_hi:[0,1,1]
	v_pk_fma_f32 v[30:31], v[246:247], v[228:229], v[30:31] op_sel_hi:[0,1,1]
	v_pk_fma_f32 v[24:25], v[246:247], v[230:231], v[24:25] op_sel_hi:[0,1,1]
	v_pk_fma_f32 v[26:27], v[246:247], v[232:233], v[26:27] op_sel_hi:[0,1,1]
	v_mul_f32_e32 v192, v16, v16
	v_fmac_f32_e32 v192, v17, v17
	v_mul_f32_e32 v219, v18, v18
	v_fmac_f32_e32 v219, v19, v19
	v_mul_f32_e32 v220, v20, v20
	v_fmac_f32_e32 v220, v21, v21
	v_mul_f32_e32 v218, v22, v22
	v_fmac_f32_e32 v218, v23, v23
	v_fmac_f32_e32 v192, v28, v28
	v_fmac_f32_e32 v192, v29, v29
	v_fmac_f32_e32 v219, v30, v30
	v_fmac_f32_e32 v219, v31, v31
	v_fmac_f32_e32 v220, v24, v24
	v_fmac_f32_e32 v220, v25, v25
	v_fmac_f32_e32 v218, v26, v26
	v_fmac_f32_e32 v218, v27, v27
	v_add_f32_e32 v192, v192, v219
	v_add_f32_e32 v220, v220, v218
	v_add_f32_e32 v192, v192, v220
	v_cvt_pk_bf16_f32 v208, v16, v17
	v_cvt_pk_bf16_f32 v209, v18, v19
	v_cvt_pk_bf16_f32 v210, v20, v21
	v_cvt_pk_bf16_f32 v211, v22, v23
	v_cvt_pk_bf16_f32 v212, v28, v29
	v_cvt_pk_bf16_f32 v213, v30, v31
	v_cvt_pk_bf16_f32 v214, v24, v25
	v_cvt_pk_bf16_f32 v215, v26, v27
	global_store_dwordx4 v247, v[208:211], s[24:25]
	global_store_dwordx4 v247, v[212:215], s[24:25] offset:16
	s_waitcnt vmcnt(14)
	v_lshlrev_b32_e32 v218, 16, v200
	v_and_b32_e32 v219, 0xffff0000, v200
	v_lshlrev_b32_e32 v220, 16, v201
	v_and_b32_e32 v221, 0xffff0000, v201
	v_lshlrev_b32_e32 v222, 16, v202
	v_and_b32_e32 v223, 0xffff0000, v202
	v_lshlrev_b32_e32 v224, 16, v203
	v_and_b32_e32 v225, 0xffff0000, v203
	v_lshlrev_b32_e32 v226, 16, v204
	v_and_b32_e32 v227, 0xffff0000, v204
	v_lshlrev_b32_e32 v228, 16, v205
	v_and_b32_e32 v229, 0xffff0000, v205
	v_lshlrev_b32_e32 v230, 16, v206
	v_and_b32_e32 v231, 0xffff0000, v206
	v_lshlrev_b32_e32 v232, 16, v207
	v_and_b32_e32 v233, 0xffff0000, v207
	v_pk_fma_f32 v[0:1], v[248:249], v[218:219], v[0:1] op_sel_hi:[0,1,1]
	v_pk_fma_f32 v[2:3], v[248:249], v[220:221], v[2:3] op_sel_hi:[0,1,1]
	v_pk_fma_f32 v[4:5], v[248:249], v[222:223], v[4:5] op_sel_hi:[0,1,1]
	v_pk_fma_f32 v[6:7], v[248:249], v[224:225], v[6:7] op_sel_hi:[0,1,1]
	v_pk_fma_f32 v[12:13], v[248:249], v[226:227], v[12:13] op_sel_hi:[0,1,1]
	v_pk_fma_f32 v[14:15], v[248:249], v[228:229], v[14:15] op_sel_hi:[0,1,1]
	v_pk_fma_f32 v[8:9], v[248:249], v[230:231], v[8:9] op_sel_hi:[0,1,1]
	v_pk_fma_f32 v[10:11], v[248:249], v[232:233], v[10:11] op_sel_hi:[0,1,1]
	v_mul_f32_e32 v200, v0, v0
	v_fmac_f32_e32 v200, v1, v1
	v_mul_f32_e32 v219, v2, v2
	v_fmac_f32_e32 v219, v3, v3
	v_mul_f32_e32 v220, v4, v4
	v_fmac_f32_e32 v220, v5, v5
	v_mul_f32_e32 v218, v6, v6
	v_fmac_f32_e32 v218, v7, v7
	v_fmac_f32_e32 v200, v12, v12
	v_fmac_f32_e32 v200, v13, v13
	v_fmac_f32_e32 v219, v14, v14
	v_fmac_f32_e32 v219, v15, v15
	v_fmac_f32_e32 v220, v8, v8
	v_fmac_f32_e32 v220, v9, v9
	v_fmac_f32_e32 v218, v10, v10
	v_fmac_f32_e32 v218, v11, v11
	v_add_f32_e32 v200, v200, v219
	v_add_f32_e32 v220, v220, v218
	v_add_f32_e32 v200, v200, v220
	v_cvt_pk_bf16_f32 v208, v0, v1
	v_cvt_pk_bf16_f32 v209, v2, v3
	v_cvt_pk_bf16_f32 v210, v4, v5
	v_cvt_pk_bf16_f32 v211, v6, v7
	v_cvt_pk_bf16_f32 v212, v12, v13
	v_cvt_pk_bf16_f32 v213, v14, v15
	v_cvt_pk_bf16_f32 v214, v8, v9
	v_cvt_pk_bf16_f32 v215, v10, v11
	global_store_dwordx4 v249, v[208:211], s[24:25]
	global_store_dwordx4 v249, v[212:215], s[24:25] offset:16
	s_nop 1
	v_permlane32_swap_b32_e32 v132, v160
	v_permlane32_swap_b32_e32 v152, v168
	v_add_f32_e32 v132, v132, v160
	v_add_f32_e32 v152, v152, v168
	s_nop 1
	v_permlane16_swap_b32_e32 v132, v152
	v_add_f32_e32 v132, v132, v152
	global_atomic_add_f32 v137, v132, s[26:27]
	s_nop 1
	v_permlane32_swap_b32_e32 v176, v192
	v_permlane32_swap_b32_e32 v184, v200
	v_add_f32_e32 v176, v176, v192
	v_add_f32_e32 v184, v184, v200
	s_nop 1
	v_permlane16_swap_b32_e32 v176, v184
	v_add_f32_e32 v176, v176, v184
	global_atomic_add_f32 v137, v176, s[26:27] offset:512
	s_andn2_b64 vcc, exec, s[2:3]
	s_mov_b64 s[2:3], -1
	s_cbranch_vccnz .LBB0_895
	v_mov_b32_e32 v8, 0
	s_andn2_b64 vcc, exec, s[20:21]
	s_nop 0
	v_mfma_f32_4x4x1_16b_f32 v[112:115], v8, v8, 0
	s_nop 0
	v_mfma_f32_4x4x1_16b_f32 v[116:119], v8, v8, 0
	s_nop 0
	v_mfma_f32_4x4x1_16b_f32 v[96:99], v8, v8, 0
	s_nop 0
	v_mfma_f32_4x4x1_16b_f32 v[100:103], v8, v8, 0
	s_nop 0
	v_mfma_f32_4x4x1_16b_f32 v[80:83], v8, v8, 0
	s_nop 0
	v_mfma_f32_4x4x1_16b_f32 v[84:87], v8, v8, 0
	s_nop 0
	v_mfma_f32_4x4x1_16b_f32 v[64:67], v8, v8, 0
	s_nop 0
	v_mfma_f32_4x4x1_16b_f32 v[68:71], v8, v8, 0
	s_nop 0
	v_mfma_f32_4x4x1_16b_f32 v[124:127], v8, v8, 0
	s_nop 0
	v_mfma_f32_4x4x1_16b_f32 v[120:123], v8, v8, 0
	s_nop 0
	v_mfma_f32_4x4x1_16b_f32 v[108:111], v8, v8, 0
	s_nop 0
	v_mfma_f32_4x4x1_16b_f32 v[104:107], v8, v8, 0
	s_nop 0
	v_mfma_f32_4x4x1_16b_f32 v[92:95], v8, v8, 0
	s_nop 0
	v_mfma_f32_4x4x1_16b_f32 v[88:91], v8, v8, 0
	s_nop 0
	v_mfma_f32_4x4x1_16b_f32 v[76:79], v8, v8, 0
	s_nop 0
	v_mfma_f32_4x4x1_16b_f32 v[72:75], v8, v8, 0
	s_nop 0
	v_mfma_f32_4x4x1_16b_f32 v[48:51], v8, v8, 0
	s_nop 0
	v_mfma_f32_4x4x1_16b_f32 v[52:55], v8, v8, 0
	s_nop 0
	v_mfma_f32_4x4x1_16b_f32 v[32:35], v8, v8, 0
	s_nop 0
	v_mfma_f32_4x4x1_16b_f32 v[36:39], v8, v8, 0
	s_nop 0
	v_mfma_f32_4x4x1_16b_f32 v[16:19], v8, v8, 0
	s_nop 0
	v_mfma_f32_4x4x1_16b_f32 v[20:23], v8, v8, 0
	s_waitcnt lgkmcnt(0)
	v_mfma_f32_4x4x1_16b_f32 v[0:3], v8, v8, 0
	s_nop 0
	v_mfma_f32_4x4x1_16b_f32 v[4:7], v8, v8, 0
	s_nop 0
	v_mfma_f32_4x4x1_16b_f32 v[60:63], v8, v8, 0
	s_nop 0
	v_mfma_f32_4x4x1_16b_f32 v[56:59], v8, v8, 0
	s_nop 0
	v_mfma_f32_4x4x1_16b_f32 v[44:47], v8, v8, 0
	s_nop 0
	v_mfma_f32_4x4x1_16b_f32 v[40:43], v8, v8, 0
	s_nop 0
	v_mfma_f32_4x4x1_16b_f32 v[28:31], v8, v8, 0
	s_nop 0
	v_mfma_f32_4x4x1_16b_f32 v[24:27], v8, v8, 0
	s_nop 0
	v_mfma_f32_4x4x1_16b_f32 v[12:15], v8, v8, 0
	s_nop 0
	v_mfma_f32_4x4x1_16b_f32 v[8:11], v8, v8, 0
	s_cbranch_vccnz .LBB0_894
	s_barrier
	s_branch .LBB0_894

.LBB0_926:
	s_cmp_eq_u32 s100, 1
	s_cbranch_scc1 .Lqs5
	s_cmp_gt_i32 s91, 6
	s_cselect_b64 s[2:3], -1, 0
	s_and_b64 s[0:1], s[4:5], s[2:3]
	s_andn2_b64 vcc, exec, s[0:1]
	s_cbranch_vccnz .LBB0_982
	s_cmp_gt_u32 s80, 63
	s_waitcnt lgkmcnt(0)
	s_mov_b64 s[8:9], 0
	s_cbranch_scc1 .LBB0_929
	v_mbcnt_hi_u32_b32 v0, -1, v217
	v_cmp_eq_u32_e32 vcc, 0, v0
	s_and_b64 s[8:9], vcc, exec

.LBB0_988:
	v_bfe_i32 v3, v0, 27, 1
	v_lshlrev_b32_e32 v1, 4, v0
	v_lshrrev_b32_e32 v3, 22, v3
	v_add_u32_e32 v3, v1, v3
	v_and_b32_e32 v3, 0xfffffc00, v3
	v_sub_u32_e32 v3, v1, v3
	v_ashrrev_i32_e32 v2, 31, v0
	v_lshrrev_b32_e32 v4, 4, v3
	v_lshrrev_b32_e32 v2, 26, v2
	v_bitop3_b32 v3, v4, v3, 32 bitop3:0x6c
	v_add_u32_e32 v2, v0, v2
	v_ashrrev_i32_e32 v5, 31, v3
	v_ashrrev_i32_e32 v2, 6, v2
	v_lshrrev_b32_e32 v5, 26, v5
	v_lshlrev_b32_e32 v4, 3, v2
	v_add_u32_e32 v5, v3, v5
	v_and_b32_e32 v4, -16, v4
	v_ashrrev_i32_e32 v6, 6, v5
	v_and_b32_e32 v5, 0xc0, v5
	v_add_u32_e32 v4, v6, v4
	v_sub_u32_e32 v3, v3, v5
	v_mov_b32_e32 v5, 1
	s_ashr_i32 s4, s7, 3
	v_lshlrev_b32_e32 v2, 5, v2
	v_ashrrev_i16_sdwa v3, v5, sext(v3) dst_sel:DWORD dst_unused:UNUSED_PAD src0_sel:DWORD src1_sel:BYTE_0
	v_lshlrev_b32_e32 v7, 1, v4
	v_lshlrev_b32_e32 v8, 2, v4
	v_lshrrev_b32_e32 v9, 2, v4
	v_and_b32_e32 v6, 3, v6
	s_add_u32 s8, s2, 0xe400000
	v_and_b32_e32 v2, 32, v2
	v_bfe_i32 v3, v3, 0, 16
	v_and_b32_e32 v7, 0x1fffc0, v7
	v_and_b32_e32 v9, 4, v9
	v_and_or_b32 v6, v8, 48, v6
	s_addc_u32 s5, s3, 0
	v_or3_b32 v6, v6, v7, v9
	v_add_lshl_u32 v2, v2, v3, 1
	v_add_u32_e32 v1, 0x2000, v1
	s_add_u32 s12, s2, 0x1100000
	v_lshl_add_u32 v137, v4, 11, v2
	v_lshl_add_u32 v138, v6, 11, v2
	v_ashrrev_i32_e32 v2, 31, v1
	s_addc_u32 s7, s3, 0
	v_lshrrev_b32_e32 v2, 22, v2
	s_add_i32 s1, s1, s4
	v_add_u32_e32 v2, v1, v2
	s_ashr_i32 s4, s1, 31
	v_ashrrev_i32_e32 v2, 10, v2
	s_lshr_b32 s4, s4, 27
	v_mul_i32_i24_e32 v3, 0x400, v2
	s_add_i32 s4, s1, s4
	v_sub_u32_e32 v1, v1, v3
	s_and_b32 s13, s7, 0xffff
	s_ashr_i32 s7, s4, 5
	s_andn2_b32 s4, s4, 31
	v_lshrrev_b32_e32 v3, 4, v1
	s_sub_i32 s1, s1, s4
	v_bitop3_b32 v1, v3, v1, 32 bitop3:0x6c
	s_bfe_i32 s4, s1, 0x80000
	v_ashrrev_i32_e32 v4, 31, v1
	s_bfe_u32 s4, s4, 0x3000c
	v_lshrrev_b32_e32 v4, 26, v4
	s_add_i32 s4, s1, s4
	v_lshlrev_b32_e32 v3, 3, v2
	v_add_u32_e32 v4, v1, v4
	s_bfe_i32 s22, s4, 0x80000
	s_and_b32 s4, s4, 0xf8
	v_and_b32_e32 v3, -16, v3
	v_ashrrev_i32_e32 v6, 6, v4
	v_and_b32_e32 v4, 0xc0, v4
	s_sub_i32 s1, s1, s4
	v_add_u32_e32 v3, v6, v3
	v_sub_u32_e32 v1, v1, v4
	s_and_b32 s9, s5, 0xffff
	s_lshl_b32 s5, s88, 10
	s_lshl_b32 s7, s7, 3
	s_sext_i32_i8 s1, s1
	v_lshlrev_b32_e32 v2, 5, v2
	v_ashrrev_i16_sdwa v1, v5, sext(v1) dst_sel:DWORD dst_unused:UNUSED_PAD src0_sel:DWORD src1_sel:BYTE_0
	v_lshlrev_b32_e32 v4, 1, v3
	v_lshlrev_b32_e32 v5, 2, v3
	v_lshrrev_b32_e32 v7, 2, v3
	v_and_b32_e32 v6, 3, v6
	s_sext_i32_i16 s22, s22
	s_add_i32 s70, s7, s1
	s_add_i32 s1, s5, 0
	v_and_b32_e32 v2, 32, v2
	v_bfe_i32 v1, v1, 0, 16
	v_and_b32_e32 v4, 0x1fffc0, v4
	v_and_b32_e32 v7, 4, v7
	v_and_or_b32 v5, v5, 48, v6
	s_mov_b32 s11, 0x20000
	s_brev_b32 s10, -2
	s_ashr_i32 s69, s22, 3
	s_add_i32 s7, s1, 0x10000
	v_or3_b32 v4, v5, v4, v7
	v_add_lshl_u32 v1, v2, v1, 1
	s_mov_b32 s14, s10
	s_mov_b32 s15, s11
	s_cmp_eq_u32 s100, 1
	s_cbranch_scc0 .Lqo_p4ai
	s_lshl_b32 s70, s98, 1
	s_mov_b32 s69, s99
.Lqo_p4ai:
	s_lshl_b32 s71, s69, 19
	s_mov_b32 m0, s7
	s_add_i32 s33, s1, 0x12000
	v_lshl_add_u32 v140, v4, 11, v1
	buffer_load_dwordx4 v138, s[12:15], s71 offen lds
	s_mov_b32 m0, s33
	s_add_i32 s35, s1, 0x14000
	buffer_load_dwordx4 v140, s[12:15], s71 offen lds
	s_or_b32 s4, s71, 0x4000
	s_mov_b32 m0, s35
	s_add_i32 s37, s1, 0x16000
	buffer_load_dwordx4 v138, s[12:15], s4 offen lds
	s_mov_b32 m0, s37
	s_lshl_b32 s72, s70, 19
	buffer_load_dwordx4 v140, s[12:15], s4 offen lds
	s_mov_b32 m0, s1
	s_add_i32 s39, s1, 0x2000
	v_lshl_add_u32 v139, v3, 11, v1
	buffer_load_dwordx4 v137, s[8:11], s72 offen lds
	s_mov_b32 m0, s39
	s_add_i32 s40, s1, 0x4000
	buffer_load_dwordx4 v139, s[8:11], s72 offen lds
	s_or_b32 s4, s72, 0x40000
	s_mov_b32 m0, s40
	s_add_i32 s41, s1, 0x6000
	buffer_load_dwordx4 v137, s[8:11], s4 offen lds
	s_mov_b32 m0, s41
	s_mov_b32 s42, 0
	buffer_load_dwordx4 v139, s[8:11], s4 offen lds
	s_lshr_b32 s4, s80, 8
	s_cmp_eq_u32 s4, 1
	s_cselect_b64 s[22:23], -1, 0
	s_cmp_lg_u32 s4, 1
	s_mov_b32 s43, 0x40000
	s_cbranch_scc1 .LBB0_990
	s_barrier

.LBB0_999:
	s_cmp_eq_u32 s100, 1
	s_cbranch_scc0 .Lqo_p4an
	s_lshl_b32 s66, s98, 1
	s_add_i32 s66, s66, s42
	s_mov_b32 s65, s99

.LBB0_1007:
	s_cmp_eq_u32 s100, 1
	s_cbranch_scc1 .Lqs6
	s_cmp_gt_i32 s91, 7
	s_cselect_b64 s[2:3], -1, 0
	s_and_b64 s[0:1], s[20:21], s[2:3]
	s_andn2_b64 vcc, exec, s[0:1]
	s_cbranch_vccnz .LBB0_1063
	s_cmp_gt_u32 s80, 63
	s_waitcnt lgkmcnt(0)
	s_mov_b64 s[8:9], 0
	s_cbranch_scc1 .LBB0_1010
	v_mbcnt_hi_u32_b32 v0, -1, v217
	v_cmp_eq_u32_e32 vcc, 0, v0
	s_and_b64 s[8:9], vcc, exec

.LBB0_1063:
	s_cmp_lt_i32 s90, 8
	s_cselect_b64 s[0:1], -1, 0
	s_and_b64 s[4:5], s[0:1], s[2:3]
	s_andn2_b64 vcc, exec, s[4:5]
	s_cbranch_vccnz .LBB0_1072
	s_and_b32 s0, s80, 0xffffffc0
	s_waitcnt lgkmcnt(0)
	v_mbcnt_hi_u32_b32 v1, -1, v217
	s_mov_b32 s20, 0
	v_add_u32_e32 v0, s0, v1
	s_mov_b64 s[0:1], s[86:87]
	s_mov_b64 s[2:3], s[18:19]
	s_cmpk_gt_i32 s6, 0x1ff
	s_cbranch_scc1 .LBB0_1071
	s_ashr_i32 s0, s6, 31
	s_lshr_b32 s0, s0, 25
	s_add_i32 s0, s6, s0
	s_ashr_i32 s1, s0, 7
	s_and_b32 s0, s0, 0xff80
	s_sub_i32 s0, s6, s0
	s_cmp_eq_u32 s100, 1
	s_cbranch_scc0 .Lqo_p4b1
	s_mov_b32 s1, s99
	s_lshl_b32 s0, s98, 1
.Lqo_p4b1:
	s_bfe_i32 s7, s0, 0x80000
	s_bfe_u32 s7, s7, 0x5000a
	s_add_i32 s0, s0, s7
	s_bfe_i32 s0, s0, 0x80000
	s_sext_i32_i16 s0, s0
	v_bfe_u32 v2, v0, 5, 1
	s_ashr_i32 s0, s0, 5
	v_lshl_or_b32 v3, s88, 4, v2
	v_and_b32_e32 v4, 16, v0
	v_bitop3_b32 v2, v2, v0, 15 bitop3:0x78
	s_add_u32 s7, s2, 0x600000
	v_or_b32_e32 v2, v2, v4
	v_lshlrev_b32_e32 v5, 9, v3
	s_addc_u32 s28, s3, 0
	s_lshl_b32 s0, s0, 2
	v_lshl_or_b32 v140, v2, 4, v5
	v_or_b32_e32 v2, 2, v3
	v_bitop3_b32 v5, v3, v0, 2 bitop3:0x36
	s_add_i32 s0, s0, s1
	v_and_or_b32 v5, v5, 15, v4
	v_lshlrev_b32_e32 v2, 9, v2
	s_ashr_i32 s1, s0, 31
	v_lshl_or_b32 v141, v5, 4, v2
	v_or_b32_e32 v2, 4, v3
	v_bitop3_b32 v5, v3, v0, 4 bitop3:0x36
	s_lshl_b64 s[0:1], s[0:1], 17
	v_and_or_b32 v5, v5, 15, v4
	v_lshlrev_b32_e32 v2, 9, v2
	s_add_u32 s8, s7, s0
	v_lshl_or_b32 v142, v5, 4, v2
	v_or_b32_e32 v2, 6, v3
	v_bitop3_b32 v5, v3, v0, 6 bitop3:0x36
	s_addc_u32 s0, s28, s1
	v_and_or_b32 v5, v5, 15, v4
	v_lshlrev_b32_e32 v2, 9, v2
	s_and_b32 s9, s0, 0xffff
	s_lshl_b32 s0, s88, 13
	v_lshl_or_b32 v143, v5, 4, v2
	v_or_b32_e32 v2, 8, v3
	v_bitop3_b32 v5, v3, v0, 8 bitop3:0x36
	s_mov_b32 s10, 0x20000
	s_add_i32 s29, s0, 0
	v_and_or_b32 v5, v5, 15, v4
	v_lshlrev_b32_e32 v2, 9, v2
	s_mov_b32 s11, s10
	s_mov_b32 m0, s29
	s_add_i32 s30, s29, 0x400
	v_lshl_or_b32 v144, v5, 4, v2
	v_or_b32_e32 v2, 10, v3
	v_bitop3_b32 v5, v3, v0, 10 bitop3:0x36
	buffer_load_dwordx4 v140, s[8:11], 0 offen lds
	s_mov_b32 m0, s30
	s_add_i32 s31, s29, 0x800
	v_and_or_b32 v5, v5, 15, v4
	v_lshlrev_b32_e32 v2, 9, v2
	buffer_load_dwordx4 v141, s[8:11], 0 offen lds
	s_mov_b32 m0, s31
	s_add_i32 s35, s29, 0xc00
	v_lshl_or_b32 v145, v5, 4, v2
	v_or_b32_e32 v2, 12, v3
	v_bitop3_b32 v5, v3, v0, 12 bitop3:0x36
	buffer_load_dwordx4 v142, s[8:11], 0 offen lds
	s_mov_b32 m0, s35
	s_add_i32 s37, s29, 0x1000
	v_and_or_b32 v5, v5, 15, v4
	v_lshlrev_b32_e32 v2, 9, v2
	buffer_load_dwordx4 v143, s[8:11], 0 offen lds
	s_mov_b32 m0, s37
	s_add_i32 s39, s29, 0x1400
	v_lshl_or_b32 v146, v5, 4, v2
	v_or_b32_e32 v2, 14, v3
	v_bitop3_b32 v3, v3, v0, 14 bitop3:0x36
	buffer_load_dwordx4 v144, s[8:11], 0 offen lds
	s_mov_b32 m0, s39
	s_add_i32 s41, s29, 0x1800
	v_and_or_b32 v3, v3, 15, v4
	v_lshlrev_b32_e32 v2, 9, v2
	buffer_load_dwordx4 v145, s[8:11], 0 offen lds
	s_mov_b32 m0, s41
	s_add_i32 s48, s29, 0x1c00
	s_add_i32 s12, 0, 0x10000
	v_lshl_or_b32 v147, v3, 4, v2
	buffer_load_dwordx4 v146, s[8:11], 0 offen lds
	s_mov_b32 m0, s48
	s_add_i32 s50, s12, s0
	buffer_load_dwordx4 v147, s[8:11], 0 offen lds
	s_mov_b32 s49, 0x10000
	s_mov_b32 m0, s50
	s_add_i32 s51, s50, 0x400
	buffer_load_dwordx4 v140, s[8:11], s49 offen lds
	s_mov_b32 m0, s51
	s_add_i32 s52, s50, 0x800
	buffer_load_dwordx4 v141, s[8:11], s49 offen lds
	s_mov_b32 m0, s52
	s_add_i32 s53, s50, 0xc00
	buffer_load_dwordx4 v142, s[8:11], s49 offen lds
	s_mov_b32 m0, s53
	s_add_i32 s54, s50, 0x1000
	buffer_load_dwordx4 v143, s[8:11], s49 offen lds
	s_mov_b32 m0, s54
	s_add_i32 s55, s50, 0x1400
	buffer_load_dwordx4 v144, s[8:11], s49 offen lds
	s_mov_b32 m0, s55
	s_add_i32 s56, s50, 0x1800
	buffer_load_dwordx4 v145, s[8:11], s49 offen lds
	s_mov_b32 m0, s56
	s_add_i32 s57, s50, 0x1c00
	buffer_load_dwordx4 v146, s[8:11], s49 offen lds
	s_mov_b32 m0, s57
	v_mov_b32_e32 v130, 0
	buffer_load_dwordx4 v147, s[8:11], s49 offen lds
	v_and_b32_e32 v2, 48, v0
	v_mov_b32_e32 v3, v130
	v_lshl_add_u64 v[2:3], s[2:3], 0, v[2:3]
	s_mov_b64 s[0:1], 0x20400000
	v_lshl_add_u64 v[132:133], v[2:3], 0, s[0:1]
	v_and_b32_e32 v3, 64, v1
	v_xor_b32_e32 v2, 16, v1
	v_add_u32_e32 v3, 64, v3
	v_cmp_lt_i32_e32 vcc, v2, v3
	v_bfe_u32 v5, v0, 4, 2
	v_and_b32_e32 v4, 15, v0
	v_cndmask_b32_e32 v2, v1, v2, vcc
	v_lshlrev_b32_e32 v148, 2, v2
	v_xor_b32_e32 v2, 32, v1
	v_bitop3_b32 v0, v5, v0, 15 bitop3:0x78
	v_cmp_lt_i32_e32 vcc, v2, v3
	v_lshlrev_b32_e32 v151, 4, v0
	v_bitop3_b32 v0, v5, v4, 4 bitop3:0x36
	s_add_u32 s58, s2, 0x800000
	v_cndmask_b32_e32 v1, v1, v2, vcc
	v_lshlrev_b32_e32 v152, 4, v0
	v_bitop3_b32 v0, v5, v4, 8 bitop3:0x36
	s_addc_u32 s59, s3, 0
	v_lshlrev_b32_e32 v149, 2, v1
	v_lshlrev_b32_e32 v1, 9, v4
	v_lshlrev_b32_e32 v2, 2, v5
	v_lshlrev_b32_e32 v153, 4, v0
	v_bitop3_b32 v0, v5, v4, 12 bitop3:0x36
	s_mov_b32 s21, s20
	v_add_u32_e32 v150, 0, v1
	s_add_u32 s24, s2, 0x24400000
	v_lshlrev_b32_e32 v154, 4, v0
	v_or_b32_e32 v159, 0x2000, v1
	v_or_b32_e32 v160, 0x4000, v1
	v_or_b32_e32 v161, 0x6000, v1
	v_or_b32_e32 v162, 0x8000, v1
	v_or_b32_e32 v163, 0xa000, v1
	v_or_b32_e32 v164, 0xc000, v1
	v_or_b32_e32 v165, 0xe000, v1
	v_add_u32_e32 v166, s12, v1
	s_mov_b32 s22, s20
	s_mov_b32 s23, s20
	v_lshlrev_b32_e32 v134, 1, v2
	v_mov_b64_e32 v[0:1], s[20:21]
	v_lshl_or_b32 v128, s88, 5, v4
	v_mov_b32_e32 v129, v130
	s_addc_u32 s25, s3, 0
	v_or_b32_e32 v155, 0x100, v151
	v_or_b32_e32 v156, 0x100, v152
	v_or_b32_e32 v157, 0x100, v153
	v_or_b32_e32 v158, 0x100, v154
	s_mov_b32 s60, 0x8000
	v_add_u32_e32 v167, s12, v159
	v_add_u32_e32 v168, s12, v154
	v_add_u32_e32 v169, s12, v153
	v_add_u32_e32 v170, s12, v152
	v_add_u32_e32 v171, s12, v151
	v_add_u32_e32 v172, s12, v160
	v_add_u32_e32 v173, s12, v161
	v_add_u32_e32 v174, s12, v162
	v_add_u32_e32 v175, s12, v163
	v_add_u32_e32 v176, s12, v164
	v_add_u32_e32 v177, s12, v165
	v_add_u32_e32 v178, 0x10000, v150
	v_add_u32_e32 v179, 0x12000, v150
	v_add_u32_e32 v180, 0x14000, v150
	v_add_u32_e32 v181, 0x16000, v150
	v_add_u32_e32 v182, 0x18000, v150
	v_add_u32_e32 v183, 0x1a000, v150
	v_add_u32_e32 v184, 0x1c000, v150
	v_add_u32_e32 v185, 0x1e000, v150
	s_mov_b32 s61, 0xff61b1e6
	s_mov_b32 s14, 0x20000
	s_mov_b32 s15, s10
	s_mov_b64 s[26:27], 0x8000
	v_mov_b64_e32 v[2:3], s[22:23]
	s_mov_b32 s20, s6
	s_branch .LBB0_1067

.LBB0_1067:
	s_ashr_i32 s0, s20, 31
	s_lshr_b32 s0, s0, 25
	s_add_i32 s0, s20, s0
	s_ashr_i32 s12, s0, 7
	s_and_b32 s0, s0, 0xffffff80
	s_sub_i32 s0, s20, s0
	s_cmp_eq_u32 s100, 1
	s_cbranch_scc0 .Lqo_p4b2
	s_mov_b32 s12, s99
	s_lshr_b32 s0, s20, 8
	s_add_i32 s0, s0, s98
	s_add_i32 s0, s0, s98
.Lqo_p4b2:
	s_bfe_i32 s1, s0, 0x80000
	s_bfe_u32 s1, s1, 0x5000a
	s_add_i32 s1, s0, s1
	s_bfe_i32 s1, s1, 0x80000
	s_sext_i32_i16 s1, s1
	s_ashr_i32 s13, s1, 5
	s_lshl_b32 s1, s13, 2
	s_add_i32 s2, s1, s12
	s_ashr_i32 s3, s2, 31
	s_lshl_b64 s[2:3], s[2:3], 17
	s_add_u32 s8, s58, s2
	s_addc_u32 s1, s59, s3
	s_and_b32 s9, s1, 0xffff
	s_ashr_i32 s1, s0, 31
	s_lshl_b64 s[0:1], s[0:1], 8
	v_lshl_add_u64 v[96:97], s[0:1], 0, v[128:129]
	s_lshl_b32 s0, s12, 8
	s_ashr_i32 s1, s0, 31
	s_lshl_b64 s[2:3], s[0:1], 1
	s_waitcnt vmcnt(0)
	v_lshl_add_u64 v[98:99], v[132:133], 0, s[2:3]
	v_lshlrev_b64 v[138:139], 11, v[96:97]
	s_waitcnt lgkmcnt(0)
	s_barrier
	v_lshl_add_u64 v[4:5], v[98:99], 0, v[138:139]
	global_load_dwordx4 v[64:67], v[4:5], off
	global_load_dwordx4 v[68:71], v[4:5], off offset:64
	global_load_dwordx4 v[72:75], v[4:5], off offset:128
	global_load_dwordx4 v[76:79], v[4:5], off offset:192
	global_load_dwordx4 v[80:83], v[4:5], off offset:256
	global_load_dwordx4 v[84:87], v[4:5], off offset:320
	global_load_dwordx4 v[88:91], v[4:5], off offset:384
	global_load_dwordx4 v[92:95], v[4:5], off offset:448
	v_add_u32_e32 v188, v150, v151
	ds_read_b128 v[4:7], v188
	v_add_u32_e32 v187, v150, v152
	ds_read_b128 v[8:11], v187
	v_add_u32_e32 v186, v150, v153
	v_add_u32_e32 v137, v150, v154
	v_add_u32_e32 v102, v166, v152
	v_add_u32_e32 v100, v166, v154
	v_add_u32_e32 v101, v166, v153
	v_add_u32_e32 v103, v166, v151
	v_add_u32_e32 v219, v169, v159
	v_add_u32_e32 v220, v170, v159
	v_add_u32_e32 v216, v167, v151
	v_add_u32_e32 v218, v168, v159
	v_add_u32_e32 v214, v169, v160
	v_add_u32_e32 v215, v170, v160
	v_add_u32_e32 v212, v172, v151
	v_add_u32_e32 v213, v168, v160
	v_add_u32_e32 v210, v169, v161
	v_add_u32_e32 v211, v170, v161
	v_add_u32_e32 v208, v173, v151
	v_add_u32_e32 v209, v168, v161
	v_add_u32_e32 v206, v168, v162
	v_add_u32_e32 v207, v169, v162
	v_add_u32_e32 v204, v174, v152
	v_add_u32_e32 v205, v174, v151
	v_add_u32_e32 v202, v168, v163
	v_add_u32_e32 v203, v169, v163
	v_add_u32_e32 v189, v177, v154
	v_add_u32_e32 v135, v177, v152
	s_mov_b32 s11, s10
	s_mov_b32 m0, s29
	s_add_i32 s20, s20, s38
	s_ashr_i32 s0, s20, 31
	s_lshr_b32 s0, s0, 25
	s_add_i32 s0, s20, s0
	s_ashr_i32 s1, s0, 7
	s_and_b32 s0, s0, 0xff80
	s_sub_i32 s0, s20, s0
	s_cmp_eq_u32 s100, 1
	s_cbranch_scc0 .Lqo_p4b3
	s_mov_b32 s1, s99
	s_lshr_b32 s0, s20, 8
	s_add_i32 s0, s0, s98
	s_add_i32 s0, s0, s98
.Lqo_p4b3:
	s_waitcnt vmcnt(7) lgkmcnt(1)
	v_mfma_f32_16x16x32_bf16 v[4:7], v[4:7], v[64:67], 0
	ds_read_b128 v[24:27], v187 offset:32768
	ds_read_b128 v[12:15], v187 offset:8192
	ds_read_b128 v[16:19], v187 offset:16384
	s_waitcnt vmcnt(6) lgkmcnt(3)
	v_mfma_f32_16x16x32_bf16 v[4:7], v[8:11], v[68:71], v[4:7]
	ds_read_b128 v[8:11], v186
	ds_read_b128 v[20:23], v187 offset:24576
	ds_read_b128 v[44:47], v102 offset:256
	s_waitcnt vmcnt(5) lgkmcnt(2)
	v_mfma_f32_16x16x32_bf16 v[4:7], v[8:11], v[72:75], v[4:7]
	ds_read_b128 v[8:11], v137
	ds_read_b128 v[28:31], v187 offset:40960
	ds_read_b128 v[36:39], v187 offset:57344
	s_waitcnt vmcnt(4) lgkmcnt(2)
	v_mfma_f32_16x16x32_bf16 v[4:7], v[8:11], v[76:79], v[4:7]
	ds_read_b128 v[8:11], v188 offset:256
	ds_read_b128 v[40:43], v101 offset:256
	s_waitcnt vmcnt(3) lgkmcnt(1)
	v_mfma_f32_16x16x32_bf16 v[4:7], v[8:11], v[80:83], v[4:7]
	ds_read_b128 v[8:11], v187 offset:256
	s_waitcnt vmcnt(2) lgkmcnt(0)
	v_mfma_f32_16x16x32_bf16 v[4:7], v[8:11], v[84:87], v[4:7]
	ds_read_b128 v[8:11], v186 offset:256
	s_waitcnt vmcnt(1) lgkmcnt(0)
	v_mfma_f32_16x16x32_bf16 v[4:7], v[8:11], v[88:91], v[4:7]
	ds_read_b128 v[8:11], v137 offset:256
	s_waitcnt vmcnt(0) lgkmcnt(0)
	v_mfma_f32_16x16x32_bf16 v[4:7], v[8:11], v[92:95], v[4:7]
	ds_read_b128 v[8:11], v188 offset:8192
	s_waitcnt lgkmcnt(0)
	v_mfma_f32_16x16x32_bf16 v[8:11], v[8:11], v[64:67], 0
	v_mfma_f32_16x16x32_bf16 v[8:11], v[12:15], v[68:71], v[8:11]
	ds_read_b128 v[12:15], v186 offset:8192
	s_waitcnt lgkmcnt(0)
	v_mfma_f32_16x16x32_bf16 v[8:11], v[12:15], v[72:75], v[8:11]
	ds_read_b128 v[12:15], v137 offset:8192
	s_waitcnt lgkmcnt(0)
	v_mfma_f32_16x16x32_bf16 v[8:11], v[12:15], v[76:79], v[8:11]
	ds_read_b128 v[12:15], v188 offset:8448
	s_waitcnt lgkmcnt(0)
	v_mfma_f32_16x16x32_bf16 v[8:11], v[12:15], v[80:83], v[8:11]
	ds_read_b128 v[12:15], v187 offset:8448
	s_waitcnt lgkmcnt(0)
	v_mfma_f32_16x16x32_bf16 v[8:11], v[12:15], v[84:87], v[8:11]
	ds_read_b128 v[12:15], v186 offset:8448
	s_waitcnt lgkmcnt(0)
	v_mfma_f32_16x16x32_bf16 v[8:11], v[12:15], v[88:91], v[8:11]
	ds_read_b128 v[12:15], v137 offset:8448
	s_waitcnt lgkmcnt(0)
	v_mfma_f32_16x16x32_bf16 v[12:15], v[12:15], v[92:95], v[8:11]
	s_nop 4
	ds_read_b128 v[8:11], v188 offset:16384
	s_waitcnt lgkmcnt(0)
	v_mfma_f32_16x16x32_bf16 v[8:11], v[8:11], v[64:67], 0
	v_mfma_f32_16x16x32_bf16 v[8:11], v[16:19], v[68:71], v[8:11]
	ds_read_b128 v[16:19], v186 offset:16384
	s_waitcnt lgkmcnt(0)
	v_mfma_f32_16x16x32_bf16 v[8:11], v[16:19], v[72:75], v[8:11]
	ds_read_b128 v[16:19], v137 offset:16384
	s_waitcnt lgkmcnt(0)
	v_mfma_f32_16x16x32_bf16 v[8:11], v[16:19], v[76:79], v[8:11]
	ds_read_b128 v[16:19], v188 offset:16640
	s_waitcnt lgkmcnt(0)
	v_mfma_f32_16x16x32_bf16 v[8:11], v[16:19], v[80:83], v[8:11]
	ds_read_b128 v[16:19], v187 offset:16640
	s_waitcnt lgkmcnt(0)
	v_mfma_f32_16x16x32_bf16 v[8:11], v[16:19], v[84:87], v[8:11]
	ds_read_b128 v[16:19], v186 offset:16640
	s_waitcnt lgkmcnt(0)
	v_mfma_f32_16x16x32_bf16 v[8:11], v[16:19], v[88:91], v[8:11]
	ds_read_b128 v[16:19], v137 offset:16640
	s_waitcnt lgkmcnt(0)
	v_mfma_f32_16x16x32_bf16 v[8:11], v[16:19], v[92:95], v[8:11]
	ds_read_b128 v[16:19], v188 offset:24576
	s_waitcnt lgkmcnt(0)
	v_mfma_f32_16x16x32_bf16 v[16:19], v[16:19], v[64:67], 0
	v_mfma_f32_16x16x32_bf16 v[16:19], v[20:23], v[68:71], v[16:19]
	ds_read_b128 v[20:23], v186 offset:24576
	s_waitcnt lgkmcnt(0)
	v_mfma_f32_16x16x32_bf16 v[16:19], v[20:23], v[72:75], v[16:19]
	ds_read_b128 v[20:23], v137 offset:24576
	s_waitcnt lgkmcnt(0)
	v_mfma_f32_16x16x32_bf16 v[16:19], v[20:23], v[76:79], v[16:19]
	ds_read_b128 v[20:23], v188 offset:24832
	s_waitcnt lgkmcnt(0)
	v_mfma_f32_16x16x32_bf16 v[16:19], v[20:23], v[80:83], v[16:19]
	ds_read_b128 v[20:23], v187 offset:24832
	s_waitcnt lgkmcnt(0)
	v_mfma_f32_16x16x32_bf16 v[16:19], v[20:23], v[84:87], v[16:19]
	ds_read_b128 v[20:23], v186 offset:24832
	s_waitcnt lgkmcnt(0)
	v_mfma_f32_16x16x32_bf16 v[16:19], v[20:23], v[88:91], v[16:19]
	ds_read_b128 v[20:23], v137 offset:24832
	s_waitcnt lgkmcnt(0)
	v_mfma_f32_16x16x32_bf16 v[20:23], v[20:23], v[92:95], v[16:19]
	s_nop 4
	ds_read_b128 v[16:19], v188 offset:32768
	s_waitcnt lgkmcnt(0)
	v_mfma_f32_16x16x32_bf16 v[16:19], v[16:19], v[64:67], 0
	v_mfma_f32_16x16x32_bf16 v[16:19], v[24:27], v[68:71], v[16:19]
	ds_read_b128 v[24:27], v186 offset:32768
	s_waitcnt lgkmcnt(0)
	v_mfma_f32_16x16x32_bf16 v[16:19], v[24:27], v[72:75], v[16:19]
	ds_read_b128 v[24:27], v137 offset:32768
	s_waitcnt lgkmcnt(0)
	v_mfma_f32_16x16x32_bf16 v[16:19], v[24:27], v[76:79], v[16:19]
	ds_read_b128 v[24:27], v188 offset:33024
	s_waitcnt lgkmcnt(0)
	v_mfma_f32_16x16x32_bf16 v[16:19], v[24:27], v[80:83], v[16:19]
	ds_read_b128 v[24:27], v187 offset:33024
	s_waitcnt lgkmcnt(0)
	v_mfma_f32_16x16x32_bf16 v[16:19], v[24:27], v[84:87], v[16:19]
	ds_read_b128 v[24:27], v186 offset:33024
	s_waitcnt lgkmcnt(0)
	v_mfma_f32_16x16x32_bf16 v[16:19], v[24:27], v[88:91], v[16:19]
	ds_read_b128 v[24:27], v137 offset:33024
	s_waitcnt lgkmcnt(0)
	v_mfma_f32_16x16x32_bf16 v[16:19], v[24:27], v[92:95], v[16:19]
	ds_read_b128 v[24:27], v188 offset:40960
	s_waitcnt lgkmcnt(0)
	v_mfma_f32_16x16x32_bf16 v[24:27], v[24:27], v[64:67], 0
	v_mfma_f32_16x16x32_bf16 v[24:27], v[28:31], v[68:71], v[24:27]
	ds_read_b128 v[28:31], v186 offset:40960
	s_waitcnt lgkmcnt(0)
	v_mfma_f32_16x16x32_bf16 v[24:27], v[28:31], v[72:75], v[24:27]
	ds_read_b128 v[28:31], v137 offset:40960
	s_waitcnt lgkmcnt(0)
	v_mfma_f32_16x16x32_bf16 v[24:27], v[28:31], v[76:79], v[24:27]
	ds_read_b128 v[28:31], v188 offset:41216
	s_waitcnt lgkmcnt(0)
	v_mfma_f32_16x16x32_bf16 v[24:27], v[28:31], v[80:83], v[24:27]
	ds_read_b128 v[28:31], v187 offset:41216
	s_waitcnt lgkmcnt(0)
	v_mfma_f32_16x16x32_bf16 v[24:27], v[28:31], v[84:87], v[24:27]
	ds_read_b128 v[28:31], v186 offset:41216
	s_waitcnt lgkmcnt(0)
	v_mfma_f32_16x16x32_bf16 v[24:27], v[28:31], v[88:91], v[24:27]
	ds_read_b128 v[28:31], v137 offset:41216
	s_waitcnt lgkmcnt(0)
	v_mfma_f32_16x16x32_bf16 v[32:35], v[28:31], v[92:95], v[24:27]
	s_nop 4
	ds_read_b128 v[24:27], v188 offset:49152
	ds_read_b128 v[28:31], v187 offset:49152
	s_waitcnt lgkmcnt(1)
	v_mfma_f32_16x16x32_bf16 v[24:27], v[24:27], v[64:67], 0
	s_waitcnt lgkmcnt(0)
	v_mfma_f32_16x16x32_bf16 v[24:27], v[28:31], v[68:71], v[24:27]
	ds_read_b128 v[28:31], v186 offset:49152
	s_waitcnt lgkmcnt(0)
	v_mfma_f32_16x16x32_bf16 v[24:27], v[28:31], v[72:75], v[24:27]
	ds_read_b128 v[28:31], v137 offset:49152
	s_waitcnt lgkmcnt(0)
	v_mfma_f32_16x16x32_bf16 v[24:27], v[28:31], v[76:79], v[24:27]
	ds_read_b128 v[28:31], v188 offset:49408
	s_waitcnt lgkmcnt(0)
	v_mfma_f32_16x16x32_bf16 v[24:27], v[28:31], v[80:83], v[24:27]
	ds_read_b128 v[28:31], v187 offset:49408
	s_waitcnt lgkmcnt(0)
	v_mfma_f32_16x16x32_bf16 v[24:27], v[28:31], v[84:87], v[24:27]
	ds_read_b128 v[28:31], v186 offset:49408
	s_waitcnt lgkmcnt(0)
	v_mfma_f32_16x16x32_bf16 v[24:27], v[28:31], v[88:91], v[24:27]
	ds_read_b128 v[28:31], v137 offset:49408
	s_waitcnt lgkmcnt(0)
	v_mfma_f32_16x16x32_bf16 v[24:27], v[28:31], v[92:95], v[24:27]
	ds_read_b128 v[28:31], v188 offset:57344
	s_waitcnt lgkmcnt(0)
	v_mfma_f32_16x16x32_bf16 v[28:31], v[28:31], v[64:67], 0
	v_mfma_f32_16x16x32_bf16 v[28:31], v[36:39], v[68:71], v[28:31]
	ds_read_b128 v[36:39], v186 offset:57344
	s_waitcnt lgkmcnt(0)
	v_mfma_f32_16x16x32_bf16 v[28:31], v[36:39], v[72:75], v[28:31]
	ds_read_b128 v[36:39], v137 offset:57344
	s_waitcnt lgkmcnt(0)
	v_mfma_f32_16x16x32_bf16 v[28:31], v[36:39], v[76:79], v[28:31]
	ds_read_b128 v[36:39], v188 offset:57600
	s_waitcnt lgkmcnt(0)
	v_mfma_f32_16x16x32_bf16 v[28:31], v[36:39], v[80:83], v[28:31]
	ds_read_b128 v[36:39], v187 offset:57600
	s_waitcnt lgkmcnt(0)
	v_mfma_f32_16x16x32_bf16 v[28:31], v[36:39], v[84:87], v[28:31]
	ds_read_b128 v[36:39], v186 offset:57600
	s_waitcnt lgkmcnt(0)
	v_mfma_f32_16x16x32_bf16 v[28:31], v[36:39], v[88:91], v[28:31]
	ds_read_b128 v[36:39], v137 offset:57600
	s_waitcnt lgkmcnt(0)
	v_mfma_f32_16x16x32_bf16 v[36:39], v[36:39], v[92:95], v[28:31]
	s_nop 4
	ds_read_b128 v[28:31], v100 offset:256
	ds_read_b128 v[48:51], v103 offset:256
	ds_read_b128 v[52:55], v100
	ds_read_b128 v[56:59], v101
	ds_read_b128 v[60:63], v102
	ds_read_b128 v[104:107], v103
	ds_read_b128 v[108:111], v220
	s_waitcnt lgkmcnt(1)
	v_mfma_f32_16x16x32_bf16 v[104:107], v[104:107], v[64:67], 0
	ds_read_b128 v[116:119], v215
	ds_read_b128 v[124:127], v211
	ds_read_b128 v[222:225], v203
	v_mfma_f32_16x16x32_bf16 v[60:63], v[60:63], v[68:71], v[104:107]
	v_mfma_f32_16x16x32_bf16 v[56:59], v[56:59], v[72:75], v[60:63]
	s_nop 2
	v_add_u32_e32 v105, v167, v154
	v_add_u32_e32 v104, v171, v159
	ds_read_b128 v[112:115], v104
	v_mfma_f32_16x16x32_bf16 v[52:55], v[52:55], v[76:79], v[56:59]
	ds_read_b128 v[60:63], v219
	v_add_u32_e32 v106, v167, v153
	v_add_u32_e32 v107, v167, v152
	v_mfma_f32_16x16x32_bf16 v[48:51], v[48:51], v[80:83], v[52:55]
	ds_read_b128 v[56:59], v218
	s_nop 2
	ds_read_b128 v[52:55], v216 offset:256
	v_mfma_f32_16x16x32_bf16 v[44:47], v[44:47], v[84:87], v[48:51]
	v_mfma_f32_16x16x32_bf16 v[40:43], v[40:43], v[88:91], v[44:47]
	s_nop 1
	ds_read_b128 v[48:51], v107 offset:256
	s_nop 3
	ds_read_b128 v[44:47], v106 offset:256
	v_mfma_f32_16x16x32_bf16 v[28:31], v[28:31], v[92:95], v[40:43]
	s_nop 2
	ds_read_b128 v[40:43], v105 offset:256
	s_waitcnt lgkmcnt(6)
	v_mfma_f32_16x16x32_bf16 v[112:115], v[112:115], v[64:67], 0
	v_mfma_f32_16x16x32_bf16 v[108:111], v[108:111], v[68:71], v[112:115]
	s_waitcnt lgkmcnt(5)
	v_mfma_f32_16x16x32_bf16 v[60:63], v[60:63], v[72:75], v[108:111]
	s_nop 4
	ds_read_b128 v[112:115], v214
	s_waitcnt lgkmcnt(5)
	v_mfma_f32_16x16x32_bf16 v[56:59], v[56:59], v[76:79], v[60:63]
	v_add_u32_e32 v109, v172, v154
	v_add_u32_e32 v108, v171, v160
	ds_read_b128 v[120:123], v108
	s_waitcnt lgkmcnt(5)
	v_mfma_f32_16x16x32_bf16 v[52:55], v[52:55], v[80:83], v[56:59]
	ds_read_b128 v[60:63], v213
	v_add_u32_e32 v110, v172, v153
	v_add_u32_e32 v111, v172, v152
	s_waitcnt lgkmcnt(5)
	v_mfma_f32_16x16x32_bf16 v[48:51], v[48:51], v[84:87], v[52:55]
	ds_read_b128 v[56:59], v212 offset:256
	s_waitcnt lgkmcnt(5)
	v_mfma_f32_16x16x32_bf16 v[44:47], v[44:47], v[88:91], v[48:51]
	ds_read_b128 v[52:55], v111 offset:256
	s_nop 3
	ds_read_b128 v[48:51], v110 offset:256
	s_waitcnt lgkmcnt(6)
	v_mfma_f32_16x16x32_bf16 v[40:43], v[40:43], v[92:95], v[44:47]
	s_nop 2
	ds_read_b128 v[44:47], v109 offset:256
	s_waitcnt lgkmcnt(5)
	v_mfma_f32_16x16x32_bf16 v[120:123], v[120:123], v[64:67], 0
	v_mfma_f32_16x16x32_bf16 v[116:119], v[116:119], v[68:71], v[120:123]
	v_mfma_f32_16x16x32_bf16 v[112:115], v[112:115], v[72:75], v[116:119]
	s_nop 5
	ds_read_b128 v[120:123], v210
	s_waitcnt lgkmcnt(5)
	v_mfma_f32_16x16x32_bf16 v[60:63], v[60:63], v[76:79], v[112:115]
	ds_read_b128 v[116:119], v209
	s_waitcnt lgkmcnt(5)
	v_mfma_f32_16x16x32_bf16 v[56:59], v[56:59], v[80:83], v[60:63]
	v_add_u32_e32 v113, v173, v154
	v_add_u32_e32 v112, v171, v161
	ds_read_b128 v[190:193], v112
	s_waitcnt lgkmcnt(5)
	v_mfma_f32_16x16x32_bf16 v[52:55], v[52:55], v[84:87], v[56:59]
	ds_read_b128 v[60:63], v208 offset:256
	v_add_u32_e32 v114, v173, v153
	v_add_u32_e32 v115, v173, v152
	s_waitcnt lgkmcnt(5)
	v_mfma_f32_16x16x32_bf16 v[48:51], v[48:51], v[88:91], v[52:55]
	ds_read_b128 v[56:59], v115 offset:256
	s_nop 1
	ds_read_b128 v[52:55], v114 offset:256
	s_waitcnt lgkmcnt(6)
	v_mfma_f32_16x16x32_bf16 v[44:47], v[44:47], v[92:95], v[48:51]
	s_nop 2
	ds_read_b128 v[48:51], v113 offset:256
	s_waitcnt lgkmcnt(4)
	v_mfma_f32_16x16x32_bf16 v[190:193], v[190:193], v[64:67], 0
	v_mfma_f32_16x16x32_bf16 v[124:127], v[124:127], v[68:71], v[190:193]
	v_mfma_f32_16x16x32_bf16 v[120:123], v[120:123], v[72:75], v[124:127]
	s_nop 5
	ds_read_b128 v[190:193], v207
	ds_read_b128 v[124:127], v206
	v_mfma_f32_16x16x32_bf16 v[116:119], v[116:119], v[76:79], v[120:123]
	s_waitcnt lgkmcnt(5)
	v_mfma_f32_16x16x32_bf16 v[60:63], v[60:63], v[80:83], v[116:119]
	s_nop 0
	ds_read_b128 v[120:123], v205 offset:256
	s_nop 3
	v_add_u32_e32 v117, v170, v162
	v_add_u32_e32 v116, v171, v162
	ds_read_b128 v[194:197], v117
	ds_read_b128 v[198:201], v116
	s_waitcnt lgkmcnt(0)
	v_mfma_f32_16x16x32_bf16 v[198:201], v[198:201], v[64:67], 0
	v_add_u32_e32 v118, v174, v154
	v_add_u32_e32 v119, v174, v153
	v_mfma_f32_16x16x32_bf16 v[194:197], v[194:197], v[68:71], v[198:201]
	v_mfma_f32_16x16x32_bf16 v[56:59], v[56:59], v[84:87], v[60:63]
	s_nop 3
	v_add_u32_e32 v200, v175, v152
	v_add_u32_e32 v201, v175, v151
	v_add_u32_e32 v199, v169, v164
	ds_read_b128 v[60:63], v204 offset:256
	v_mfma_f32_16x16x32_bf16 v[190:193], v[190:193], v[72:75], v[194:197]
	v_add_u32_e32 v198, v171, v164
	ds_read_b128 v[234:237], v199
	ds_read_b128 v[242:245], v198
	v_mfma_f32_16x16x32_bf16 v[124:127], v[124:127], v[76:79], v[190:193]
	ds_read_b128 v[194:197], v202
	v_mfma_f32_16x16x32_bf16 v[120:123], v[120:123], v[80:83], v[124:127]
	s_nop 1
	ds_read_b128 v[190:193], v201 offset:256
	s_nop 2
	ds_read_b128 v[124:127], v200 offset:256
	s_waitcnt lgkmcnt(5)
	v_mfma_f32_16x16x32_bf16 v[60:63], v[60:63], v[84:87], v[120:123]
	s_nop 2
	v_add_u32_e32 v121, v170, v163
	v_add_u32_e32 v120, v171, v163
	ds_read_b128 v[226:229], v121
	ds_read_b128 v[230:233], v120
	s_waitcnt lgkmcnt(0)
	v_mfma_f32_16x16x32_bf16 v[230:233], v[230:233], v[64:67], 0
	v_add_u32_e32 v122, v175, v154
	v_add_u32_e32 v123, v175, v153
	v_mfma_f32_16x16x32_bf16 v[52:55], v[52:55], v[88:91], v[56:59]
	v_mfma_f32_16x16x32_bf16 v[226:229], v[226:229], v[68:71], v[230:233]
	s_nop 1
	ds_read_b128 v[56:59], v119 offset:256
	v_mfma_f32_16x16x32_bf16 v[48:51], v[48:51], v[92:95], v[52:55]
	s_nop 2
	ds_read_b128 v[52:55], v118 offset:256
	v_mfma_f32_16x16x32_bf16 v[222:225], v[222:225], v[72:75], v[226:229]
	v_mfma_f32_16x16x32_bf16 v[194:197], v[194:197], v[76:79], v[222:225]
	s_waitcnt lgkmcnt(1)
	v_mfma_f32_16x16x32_bf16 v[56:59], v[56:59], v[88:91], v[60:63]
	v_mfma_f32_16x16x32_bf16 v[190:193], v[190:193], v[80:83], v[194:197]
	s_nop 1
	ds_read_b128 v[60:63], v123 offset:256
	s_nop 1
	v_add_u32_e32 v196, v168, v164
	v_add_u32_e32 v197, v170, v164
	ds_read_b128 v[230:233], v196
	ds_read_b128 v[238:241], v197
	s_waitcnt lgkmcnt(3)
	v_mfma_f32_16x16x32_bf16 v[52:55], v[52:55], v[92:95], v[56:59]
	v_add_u32_e32 v194, v170, v165
	v_add_u32_e32 v195, v171, v165
	ds_read_b128 v[246:249], v194
	ds_read_b128 v[250:253], v195
	ds_read_b128 v[56:59], v122 offset:256
	v_mfma_f32_16x16x32_bf16 v[242:245], v[242:245], v[64:67], 0
	v_mfma_f32_16x16x32_bf16 v[124:127], v[124:127], v[84:87], v[190:193]
	s_waitcnt lgkmcnt(3)
	v_mfma_f32_16x16x32_bf16 v[238:241], v[238:241], v[68:71], v[242:245]
	v_mfma_f32_16x16x32_bf16 v[60:63], v[60:63], v[88:91], v[124:127]
	s_nop 4
	v_add_u32_e32 v126, v176, v153
	v_add_u32_e32 v127, v176, v151
	ds_read_b128 v[190:193], v126 offset:256
	ds_read_b128 v[226:229], v127 offset:256
	v_mfma_f32_16x16x32_bf16 v[234:237], v[234:237], v[72:75], v[238:241]
	v_add_u32_e32 v125, v176, v154
	v_add_u32_e32 v124, v176, v152
	ds_read_b128 v[222:225], v124 offset:256
	s_waitcnt lgkmcnt(3)
	v_mfma_f32_16x16x32_bf16 v[56:59], v[56:59], v[92:95], v[60:63]
	s_nop 2
	ds_read_b128 v[60:63], v125 offset:256
	v_mfma_f32_16x16x32_bf16 v[230:233], v[230:233], v[76:79], v[234:237]
	v_mfma_f32_16x16x32_bf16 v[64:67], v[250:253], v[64:67], 0
	s_waitcnt lgkmcnt(2)
	v_mfma_f32_16x16x32_bf16 v[226:229], v[226:229], v[80:83], v[230:233]
	v_mfma_f32_16x16x32_bf16 v[64:67], v[246:249], v[68:71], v[64:67]
	v_max_f32_e32 v68, v5, v5
	v_max_f32_e32 v69, v4, v4
	v_max_f32_e32 v68, v69, v68
	v_max_f32_e32 v69, v7, v7
	v_max_f32_e32 v70, v6, v6
	v_max_f32_e32 v69, v70, v69
	s_waitcnt lgkmcnt(1)
	v_mfma_f32_16x16x32_bf16 v[222:225], v[222:225], v[84:87], v[226:229]
	v_max3_f32 v68, v68, s61, v69
	v_max_f32_e32 v69, v13, v13
	v_max_f32_e32 v70, v12, v12
	v_max_f32_e32 v69, v70, v69
	v_max_f32_e32 v70, v15, v15
	v_max_f32_e32 v71, v14, v14
	v_max_f32_e32 v70, v71, v70
	v_max3_f32 v68, v68, v69, v70
	v_max_f32_e32 v69, v9, v9
	v_max_f32_e32 v70, v8, v8
	v_mfma_f32_16x16x32_bf16 v[190:193], v[190:193], v[88:91], v[222:225]
	v_max_f32_e32 v69, v70, v69
	v_max_f32_e32 v70, v11, v11
	v_max_f32_e32 v71, v10, v10
	v_max_f32_e32 v70, v71, v70
	v_max3_f32 v68, v68, v69, v70
	v_max_f32_e32 v69, v21, v21
	v_max_f32_e32 v70, v20, v20
	v_max_f32_e32 v69, v70, v69
	v_max_f32_e32 v70, v23, v23
	v_max_f32_e32 v71, v22, v22
	s_waitcnt lgkmcnt(0)
	v_mfma_f32_16x16x32_bf16 v[60:63], v[60:63], v[92:95], v[190:193]
	v_max_f32_e32 v70, v71, v70
	v_max3_f32 v68, v68, v69, v70
	v_max_f32_e32 v69, v17, v17
	v_add_u32_e32 v192, v168, v165
	v_add_u32_e32 v193, v169, v165
	ds_read_b128 v[238:241], v192
	ds_read_b128 v[242:245], v193
	v_max_f32_e32 v70, v16, v16
	v_max_f32_e32 v69, v70, v69
	v_max_f32_e32 v70, v19, v19
	v_max_f32_e32 v71, v18, v18
	v_max_f32_e32 v70, v71, v70
	v_max3_f32 v68, v68, v69, v70
	v_max_f32_e32 v69, v33, v33
	v_max_f32_e32 v70, v32, v32
	v_max_f32_e32 v69, v70, v69
	v_max_f32_e32 v70, v35, v35
	v_max_f32_e32 v71, v34, v34
	v_max_f32_e32 v70, v71, v70
	v_max3_f32 v68, v68, v69, v70
	v_max_f32_e32 v69, v25, v25
	v_max_f32_e32 v70, v24, v24
	v_add_u32_e32 v191, v177, v153
	v_add_u32_e32 v190, v177, v151
	v_max_f32_e32 v69, v70, v69
	v_max_f32_e32 v70, v27, v27
	v_max_f32_e32 v71, v26, v26
	ds_read_b128 v[226:229], v191 offset:256
	ds_read_b128 v[234:237], v190 offset:256
	v_max_f32_e32 v70, v71, v70
	s_waitcnt lgkmcnt(2)
	v_mfma_f32_16x16x32_bf16 v[64:67], v[242:245], v[72:75], v[64:67]
	v_max3_f32 v68, v68, v69, v70
	v_max_f32_e32 v69, v37, v37
	v_max_f32_e32 v70, v36, v36
	v_max_f32_e32 v69, v70, v69
	v_max_f32_e32 v70, v39, v39
	v_max_f32_e32 v71, v38, v38
	v_max_f32_e32 v70, v71, v70
	ds_read_b128 v[222:225], v189 offset:256
	ds_read_b128 v[230:233], v135 offset:256
	v_max3_f32 v68, v68, v69, v70
	v_max_f32_e32 v69, v29, v29
	v_max_f32_e32 v70, v28, v28
	v_mfma_f32_16x16x32_bf16 v[64:67], v[238:241], v[76:79], v[64:67]
	v_max_f32_e32 v69, v70, v69
	v_max_f32_e32 v70, v31, v31
	v_max_f32_e32 v71, v30, v30
	v_max_f32_e32 v70, v71, v70
	v_max3_f32 v68, v68, v69, v70
	v_max_f32_e32 v69, v41, v41
	v_max_f32_e32 v70, v40, v40
	v_max_f32_e32 v69, v70, v69
	v_max_f32_e32 v70, v43, v43
	v_max_f32_e32 v71, v42, v42
	s_waitcnt lgkmcnt(2)
	v_mfma_f32_16x16x32_bf16 v[64:67], v[234:237], v[80:83], v[64:67]
	v_max_f32_e32 v70, v71, v70
	v_max3_f32 v68, v68, v69, v70
	v_max_f32_e32 v69, v45, v45
	v_max_f32_e32 v70, v44, v44
	v_max_f32_e32 v69, v70, v69
	v_max_f32_e32 v70, v47, v47
	v_max_f32_e32 v71, v46, v46
	v_max_f32_e32 v70, v71, v70
	s_waitcnt lgkmcnt(0)
	v_mfma_f32_16x16x32_bf16 v[64:67], v[230:233], v[84:87], v[64:67]
	v_max3_f32 v68, v68, v69, v70
	v_max_f32_e32 v69, v49, v49
	v_max_f32_e32 v70, v48, v48
	v_max_f32_e32 v69, v70, v69
	v_max_f32_e32 v70, v51, v51
	v_max_f32_e32 v71, v50, v50
	v_max_f32_e32 v70, v71, v70
	v_max3_f32 v68, v68, v69, v70
	v_max_f32_e32 v69, v53, v53
	v_max_f32_e32 v70, v52, v52
	v_mfma_f32_16x16x32_bf16 v[64:67], v[226:229], v[88:91], v[64:67]
	v_max_f32_e32 v69, v70, v69
	v_max_f32_e32 v70, v55, v55
	v_max_f32_e32 v71, v54, v54
	v_max_f32_e32 v70, v71, v70
	v_max3_f32 v68, v68, v69, v70
	v_max_f32_e32 v69, v57, v57
	v_max_f32_e32 v70, v56, v56
	v_max_f32_e32 v69, v70, v69
	v_max_f32_e32 v70, v59, v59
	v_max_f32_e32 v71, v58, v58
	v_mfma_f32_16x16x32_bf16 v[64:67], v[222:225], v[92:95], v[64:67]
	v_max_f32_e32 v70, v71, v70
	v_max3_f32 v68, v68, v69, v70
	v_max_f32_e32 v69, v61, v61
	v_max_f32_e32 v70, v60, v60
	v_max_f32_e32 v69, v70, v69
	v_max_f32_e32 v70, v63, v63
	v_max_f32_e32 v71, v62, v62
	v_max_f32_e32 v70, v71, v70
	v_max3_f32 v68, v68, v69, v70
	v_max_f32_e32 v69, v65, v65
	v_max_f32_e32 v70, v64, v64
	v_max_f32_e32 v69, v70, v69
	v_max_f32_e32 v70, v67, v67
	v_max_f32_e32 v71, v66, v66
	v_max_f32_e32 v70, v71, v70
	v_max3_f32 v68, v68, v69, v70
	ds_bpermute_b32 v69, v148, v68
	s_waitcnt lgkmcnt(0)
	v_max_f32_e32 v69, v69, v69
	v_max_f32_e32 v68, v68, v69
	ds_bpermute_b32 v69, v149, v68
	s_waitcnt lgkmcnt(0)
	v_max_f32_e32 v69, v69, v69
	v_max_f32_e32 v74, v68, v69
	v_sub_f32_e32 v4, v4, v74
	v_exp_f32_e32 v68, v4
	v_sub_f32_e32 v4, v12, v74
	v_exp_f32_e32 v69, v4
	v_sub_f32_e32 v4, v5, v74
	v_exp_f32_e32 v12, v4
	v_sub_f32_e32 v4, v13, v74
	v_exp_f32_e32 v13, v4
	v_sub_f32_e32 v4, v6, v74
	v_exp_f32_e32 v70, v4
	v_sub_f32_e32 v4, v14, v74
	v_exp_f32_e32 v71, v4
	v_sub_f32_e32 v4, v7, v74
	v_exp_f32_e32 v6, v4
	v_sub_f32_e32 v4, v15, v74
	v_exp_f32_e32 v7, v4
	v_pk_add_f32 v[4:5], v[68:69], v[12:13]
	v_sub_f32_e32 v9, v9, v74
	v_sub_f32_e32 v8, v8, v74
	v_pk_add_f32 v[14:15], v[70:71], v[6:7]
	v_exp_f32_e32 v8, v8
	v_pk_add_f32 v[72:73], v[4:5], v[14:15]
	v_exp_f32_e32 v14, v9
	v_sub_f32_e32 v9, v21, v74
	v_cvt_pk_bf16_f32 v4, v68, v12
	v_sub_f32_e32 v12, v20, v74
	v_exp_f32_e32 v20, v9
	v_sub_f32_e32 v9, v10, v74
	v_sub_f32_e32 v10, v22, v74
	v_cvt_pk_bf16_f32 v5, v70, v6
	v_cvt_pk_bf16_f32 v6, v69, v13
	v_exp_f32_e32 v13, v10
	v_sub_f32_e32 v10, v11, v74
	v_exp_f32_e32 v15, v10
	v_sub_f32_e32 v10, v23, v74
	v_exp_f32_e32 v12, v12
	v_exp_f32_e32 v21, v10
	v_exp_f32_e32 v9, v9
	v_cvt_pk_bf16_f32 v7, v71, v7
	v_cvt_pk_bf16_f32 v10, v12, v20
	v_pk_add_f32 v[68:69], v[12:13], v[20:21]
	v_cvt_pk_bf16_f32 v11, v13, v21
	v_sub_f32_e32 v13, v32, v74
	v_pk_add_f32 v[22:23], v[8:9], v[14:15]
	v_cvt_pk_bf16_f32 v8, v8, v14
	v_sub_f32_e32 v12, v16, v74
	v_exp_f32_e32 v14, v13
	v_sub_f32_e32 v13, v17, v74
	v_sub_f32_e32 v16, v18, v74
	v_sub_f32_e32 v18, v19, v74
	v_exp_f32_e32 v12, v12
	v_exp_f32_e32 v13, v13
	v_exp_f32_e32 v16, v16
	v_exp_f32_e32 v19, v18
	v_cvt_pk_bf16_f32 v9, v9, v15
	v_sub_f32_e32 v15, v33, v74
	v_sub_f32_e32 v17, v34, v74
	v_sub_f32_e32 v18, v35, v74
	v_exp_f32_e32 v15, v15
	v_exp_f32_e32 v17, v17
	v_exp_f32_e32 v21, v18
	v_add_f32_e32 v18, v12, v13
	v_add_f32_e32 v20, v16, v19
	v_cvt_pk_bf16_f32 v12, v12, v13
	v_cvt_pk_bf16_f32 v13, v16, v19
	v_sub_f32_e32 v16, v24, v74
	v_exp_f32_e32 v70, v16
	v_sub_f32_e32 v16, v36, v74
	v_exp_f32_e32 v19, v16
	v_sub_f32_e32 v16, v25, v74
	v_exp_f32_e32 v131, v16
	v_sub_f32_e32 v16, v37, v74
	v_add_f32_e32 v32, v14, v15
	v_add_f32_e32 v34, v17, v21
	v_cvt_pk_bf16_f32 v14, v14, v15
	v_cvt_pk_bf16_f32 v15, v17, v21
	v_exp_f32_e32 v21, v16
	v_sub_f32_e32 v16, v26, v74
	v_exp_f32_e32 v26, v16
	v_sub_f32_e32 v16, v38, v74
	v_exp_f32_e32 v33, v16
	v_sub_f32_e32 v16, v27, v74
	v_exp_f32_e32 v27, v16
	v_sub_f32_e32 v16, v39, v74
	v_exp_f32_e32 v35, v16
	v_pk_add_f32 v[16:17], v[72:73], v[72:73] op_sel:[0,1] op_sel_hi:[1,0]
	v_pk_add_f32 v[22:23], v[22:23], v[22:23] op_sel:[0,1] op_sel_hi:[1,0]
	v_pk_add_f32 v[24:25], v[68:69], v[68:69] op_sel:[0,1] op_sel_hi:[1,0]
	v_mov_b32_e32 v17, v70
	v_mov_b32_e32 v23, v26
	v_mov_b32_e32 v25, v27
	v_pk_add_f32 v[16:17], v[16:17], v[130:131]
	v_pk_add_f32 v[22:23], v[22:23], v[24:25]
	v_pk_add_f32 v[24:25], v[32:33], v[34:35]
	v_pk_add_f32 v[16:17], v[16:17], v[22:23]
	v_pk_add_f32 v[22:23], v[18:19], v[20:21]
	v_sub_f32_e32 v20, v28, v74
	v_pk_add_f32 v[22:23], v[22:23], v[24:25]
	v_cvt_pk_bf16_f32 v18, v19, v21
	v_pk_add_f32 v[36:37], v[16:17], v[22:23]
	v_exp_f32_e32 v22, v20
	v_sub_f32_e32 v20, v40, v74
	v_exp_f32_e32 v23, v20
	v_sub_f32_e32 v20, v29, v74
	v_exp_f32_e32 v24, v20
	v_sub_f32_e32 v20, v41, v74
	v_exp_f32_e32 v25, v20
	v_sub_f32_e32 v20, v30, v74
	v_cvt_pk_bf16_f32 v17, v26, v27
	v_exp_f32_e32 v26, v20
	v_sub_f32_e32 v20, v42, v74
	v_exp_f32_e32 v27, v20
	v_sub_f32_e32 v20, v31, v74
	v_exp_f32_e32 v28, v20
	v_sub_f32_e32 v20, v43, v74
	v_exp_f32_e32 v29, v20
	v_pk_add_f32 v[20:21], v[22:23], v[24:25]
	v_cvt_pk_bf16_f32 v19, v33, v35
	v_sub_f32_e32 v40, v54, v74
	v_pk_add_f32 v[30:31], v[26:27], v[28:29]
	v_exp_f32_e32 v41, v40
	v_pk_add_f32 v[32:33], v[20:21], v[30:31]
	v_cvt_pk_bf16_f32 v20, v22, v24
	v_cvt_pk_bf16_f32 v22, v23, v25
	v_sub_f32_e32 v25, v48, v74
	v_cvt_pk_bf16_f32 v21, v26, v28
	v_exp_f32_e32 v26, v25
	v_sub_f32_e32 v25, v45, v74
	v_exp_f32_e32 v28, v25
	v_sub_f32_e32 v25, v49, v74
	v_cvt_pk_bf16_f32 v23, v27, v29
	v_sub_f32_e32 v24, v44, v74
	v_exp_f32_e32 v30, v25
	v_sub_f32_e32 v25, v46, v74
	v_sub_f32_e32 v29, v47, v74
	v_exp_f32_e32 v24, v24
	v_exp_f32_e32 v25, v25
	v_sub_f32_e32 v27, v50, v74
	v_exp_f32_e32 v29, v29
	v_sub_f32_e32 v31, v51, v74
	v_exp_f32_e32 v27, v27
	v_exp_f32_e32 v31, v31
	v_sub_f32_e32 v40, v58, v74
	v_pk_add_f32 v[34:35], v[24:25], v[28:29]
	v_cvt_pk_bf16_f32 v25, v25, v29
	v_sub_f32_e32 v29, v56, v74
	v_exp_f32_e32 v43, v40
	v_sub_f32_e32 v40, v55, v74
	v_pk_add_f32 v[38:39], v[26:27], v[30:31]
	v_cvt_pk_bf16_f32 v24, v24, v28
	v_cvt_pk_bf16_f32 v26, v26, v30
	v_cvt_pk_bf16_f32 v27, v27, v31
	v_sub_f32_e32 v28, v52, v74
	v_exp_f32_e32 v30, v29
	v_sub_f32_e32 v29, v53, v74
	v_sub_f32_e32 v31, v57, v74
	v_exp_f32_e32 v45, v40
	v_sub_f32_e32 v40, v59, v74
	v_exp_f32_e32 v28, v28
	v_exp_f32_e32 v29, v29
	v_exp_f32_e32 v31, v31
	v_exp_f32_e32 v47, v40
	v_add_f32_e32 v42, v41, v45
	v_add_f32_e32 v40, v28, v29
	v_add_f32_e32 v44, v30, v31
	v_add_f32_e32 v46, v43, v47
	v_cvt_pk_bf16_f32 v28, v28, v29
	v_cvt_pk_bf16_f32 v29, v41, v45
	v_cvt_pk_bf16_f32 v30, v30, v31
	v_cvt_pk_bf16_f32 v31, v43, v47
	v_sub_f32_e32 v41, v60, v74
	v_sub_f32_e32 v43, v61, v74
	v_exp_f32_e32 v48, v41
	v_exp_f32_e32 v49, v43
	v_sub_f32_e32 v45, v62, v74
	v_sub_f32_e32 v47, v63, v74
	v_exp_f32_e32 v50, v45
	v_exp_f32_e32 v51, v47
	v_sub_f32_e32 v41, v64, v74
	v_sub_f32_e32 v43, v65, v74
	v_sub_f32_e32 v45, v66, v74
	v_sub_f32_e32 v47, v67, v74
	v_pk_add_f32 v[36:37], v[36:37], v[36:37] op_sel:[0,1] op_sel_hi:[1,0]
	v_pk_add_f32 v[32:33], v[32:33], v[32:33] op_sel:[0,1] op_sel_hi:[1,0]
	v_exp_f32_e32 v41, v41
	v_exp_f32_e32 v43, v43
	v_exp_f32_e32 v45, v45
	v_exp_f32_e32 v47, v47
	v_mov_b32_e32 v37, v48
	v_mov_b32_e32 v33, v49
	v_pk_add_f32 v[32:33], v[36:37], v[32:33]
	v_pk_add_f32 v[34:35], v[34:35], v[34:35] op_sel:[0,1] op_sel_hi:[1,0]
	v_pk_add_f32 v[36:37], v[38:39], v[38:39] op_sel:[0,1] op_sel_hi:[1,0]
	v_mov_b32_e32 v35, v50
	v_mov_b32_e32 v37, v51
	v_pk_add_f32 v[34:35], v[34:35], v[36:37]
	v_pk_add_f32 v[36:37], v[44:45], v[46:47]
	v_pk_add_f32 v[32:33], v[32:33], v[34:35]
	v_pk_add_f32 v[34:35], v[40:41], v[42:43]
	v_cvt_pk_bf16_f32 v16, v70, v131
	v_pk_add_f32 v[34:35], v[34:35], v[36:37]
	s_nop 0
	v_pk_add_f32 v[32:33], v[32:33], v[34:35]
	v_cvt_pk_bf16_f32 v34, v41, v43
	v_add_f32_e32 v36, v32, v33
	ds_bpermute_b32 v37, v148, v36
	v_cvt_pk_bf16_f32 v32, v48, v49
	v_cvt_pk_bf16_f32 v33, v50, v51
	v_cvt_pk_bf16_f32 v35, v45, v47
	s_waitcnt lgkmcnt(0)
	v_add_f32_e32 v36, v36, v37
	ds_bpermute_b32 v37, v149, v36
	s_waitcnt lgkmcnt(0)
	v_add_f32_e32 v36, v36, v37
	v_rcp_f32_e32 v136, v36
	v_mov_b32_e32 v36, 16
	s_nop 0
	v_ashrrev_i32_e32 v37, 31, v36
	v_lshl_add_u64 v[36:37], v[96:97], 0, v[36:37]
	v_lshlrev_b64 v[36:37], 11, v[36:37]
	v_lshl_add_u64 v[36:37], v[98:99], 0, v[36:37]
	global_load_dwordx4 v[68:71], v[36:37], off
	global_load_dwordx4 v[72:75], v[36:37], off offset:64
	global_load_dwordx4 v[76:79], v[36:37], off offset:128
	global_load_dwordx4 v[80:83], v[36:37], off offset:192
	global_load_dwordx4 v[84:87], v[36:37], off offset:256
	global_load_dwordx4 v[88:91], v[36:37], off offset:320
	global_load_dwordx4 v[92:95], v[36:37], off offset:384
	global_load_dwordx4 v[96:99], v[36:37], off offset:448
	ds_read_b128 v[36:39], v137 offset:256
	ds_read_b128 v[40:43], v186 offset:256
	ds_read_b128 v[44:47], v187 offset:256
	ds_read_b128 v[48:51], v188 offset:256
	ds_read_b128 v[52:55], v137
	ds_read_b128 v[56:59], v186
	ds_read_b128 v[60:63], v187
	ds_read_b128 v[64:67], v188
	s_waitcnt vmcnt(7) lgkmcnt(0)
	v_mfma_f32_16x16x32_bf16 v[64:67], v[64:67], v[68:71], 0
	s_waitcnt vmcnt(6)
	v_mfma_f32_16x16x32_bf16 v[60:63], v[60:63], v[72:75], v[64:67]
	s_waitcnt vmcnt(5)
	v_mfma_f32_16x16x32_bf16 v[56:59], v[56:59], v[76:79], v[60:63]
	s_waitcnt vmcnt(4)
	v_mfma_f32_16x16x32_bf16 v[52:55], v[52:55], v[80:83], v[56:59]
	s_waitcnt vmcnt(3)
	v_mfma_f32_16x16x32_bf16 v[48:51], v[48:51], v[84:87], v[52:55]
	s_waitcnt vmcnt(2)
	v_mfma_f32_16x16x32_bf16 v[44:47], v[44:47], v[88:91], v[48:51]
	s_waitcnt vmcnt(1)
	v_mfma_f32_16x16x32_bf16 v[40:43], v[40:43], v[92:95], v[44:47]
	s_waitcnt vmcnt(0)
	v_mfma_f32_16x16x32_bf16 v[44:47], v[36:39], v[96:99], v[40:43]
	ds_read_b128 v[36:39], v137 offset:8448
	s_nop 4
	ds_read_b128 v[40:43], v186 offset:8448
	ds_read_b128 v[48:51], v187 offset:8448
	ds_read_b128 v[52:55], v188 offset:8448
	ds_read_b128 v[56:59], v137 offset:8192
	ds_read_b128 v[60:63], v186 offset:8192
	ds_read_b128 v[64:67], v187 offset:8192
	ds_read_b128 v[222:225], v188 offset:8192
	s_waitcnt lgkmcnt(0)
	v_mfma_f32_16x16x32_bf16 v[222:225], v[222:225], v[68:71], 0
	v_mfma_f32_16x16x32_bf16 v[64:67], v[64:67], v[72:75], v[222:225]
	v_mfma_f32_16x16x32_bf16 v[60:63], v[60:63], v[76:79], v[64:67]
	v_mfma_f32_16x16x32_bf16 v[56:59], v[56:59], v[80:83], v[60:63]
	v_mfma_f32_16x16x32_bf16 v[52:55], v[52:55], v[84:87], v[56:59]
	v_mfma_f32_16x16x32_bf16 v[48:51], v[48:51], v[88:91], v[52:55]
	v_mfma_f32_16x16x32_bf16 v[40:43], v[40:43], v[92:95], v[48:51]
	v_mfma_f32_16x16x32_bf16 v[60:63], v[36:39], v[96:99], v[40:43]
	ds_read_b128 v[36:39], v137 offset:16640
	s_nop 5
	ds_read_b128 v[40:43], v186 offset:16640
	ds_read_b128 v[48:51], v187 offset:16640
	ds_read_b128 v[52:55], v188 offset:16640
	ds_read_b128 v[56:59], v137 offset:16384
	ds_read_b128 v[64:67], v186 offset:16384
	ds_read_b128 v[222:225], v187 offset:16384
	ds_read_b128 v[226:229], v188 offset:16384
	s_waitcnt lgkmcnt(0)
	v_mfma_f32_16x16x32_bf16 v[226:229], v[226:229], v[68:71], 0
	v_mfma_f32_16x16x32_bf16 v[222:225], v[222:225], v[72:75], v[226:229]
	v_mfma_f32_16x16x32_bf16 v[64:67], v[64:67], v[76:79], v[222:225]
	v_mfma_f32_16x16x32_bf16 v[56:59], v[56:59], v[80:83], v[64:67]
	v_mfma_f32_16x16x32_bf16 v[52:55], v[52:55], v[84:87], v[56:59]
	v_mfma_f32_16x16x32_bf16 v[48:51], v[48:51], v[88:91], v[52:55]
	v_mfma_f32_16x16x32_bf16 v[40:43], v[40:43], v[92:95], v[48:51]
	v_mfma_f32_16x16x32_bf16 v[36:39], v[36:39], v[96:99], v[40:43]
	s_nop 6
	ds_read_b128 v[40:43], v137 offset:24832
	ds_read_b128 v[48:51], v186 offset:24832
	ds_read_b128 v[52:55], v187 offset:24832
	ds_read_b128 v[56:59], v188 offset:24832
	ds_read_b128 v[64:67], v137 offset:24576
	ds_read_b128 v[222:225], v186 offset:24576
	ds_read_b128 v[226:229], v187 offset:24576
	ds_read_b128 v[230:233], v188 offset:24576
	s_waitcnt lgkmcnt(0)
	v_mfma_f32_16x16x32_bf16 v[230:233], v[230:233], v[68:71], 0
	v_mfma_f32_16x16x32_bf16 v[226:229], v[226:229], v[72:75], v[230:233]
	v_mfma_f32_16x16x32_bf16 v[222:225], v[222:225], v[76:79], v[226:229]
	v_mfma_f32_16x16x32_bf16 v[64:67], v[64:67], v[80:83], v[222:225]
	v_mfma_f32_16x16x32_bf16 v[56:59], v[56:59], v[84:87], v[64:67]
	v_mfma_f32_16x16x32_bf16 v[52:55], v[52:55], v[88:91], v[56:59]
	v_mfma_f32_16x16x32_bf16 v[48:51], v[48:51], v[92:95], v[52:55]
	v_mfma_f32_16x16x32_bf16 v[52:55], v[40:43], v[96:99], v[48:51]
	ds_read_b128 v[40:43], v137 offset:33024
	s_nop 5
	ds_read_b128 v[48:51], v186 offset:33024
	ds_read_b128 v[56:59], v187 offset:33024
	ds_read_b128 v[64:67], v188 offset:33024
	ds_read_b128 v[222:225], v137 offset:32768
	ds_read_b128 v[226:229], v186 offset:32768
	ds_read_b128 v[230:233], v187 offset:32768
	ds_read_b128 v[234:237], v188 offset:32768
	s_waitcnt lgkmcnt(0)
	v_mfma_f32_16x16x32_bf16 v[234:237], v[234:237], v[68:71], 0
	v_mfma_f32_16x16x32_bf16 v[230:233], v[230:233], v[72:75], v[234:237]
	v_mfma_f32_16x16x32_bf16 v[226:229], v[226:229], v[76:79], v[230:233]
	v_mfma_f32_16x16x32_bf16 v[222:225], v[222:225], v[80:83], v[226:229]
	v_mfma_f32_16x16x32_bf16 v[64:67], v[64:67], v[84:87], v[222:225]
	v_mfma_f32_16x16x32_bf16 v[56:59], v[56:59], v[88:91], v[64:67]
	v_mfma_f32_16x16x32_bf16 v[48:51], v[48:51], v[92:95], v[56:59]
	v_mfma_f32_16x16x32_bf16 v[40:43], v[40:43], v[96:99], v[48:51]
	s_nop 6
	ds_read_b128 v[48:51], v137 offset:41216
	ds_read_b128 v[56:59], v186 offset:41216
	ds_read_b128 v[64:67], v187 offset:41216
	ds_read_b128 v[222:225], v188 offset:41216
	ds_read_b128 v[226:229], v137 offset:40960
	ds_read_b128 v[230:233], v186 offset:40960
	ds_read_b128 v[234:237], v187 offset:40960
	ds_read_b128 v[238:241], v188 offset:40960
	s_waitcnt lgkmcnt(0)
	v_mfma_f32_16x16x32_bf16 v[238:241], v[238:241], v[68:71], 0
	v_mfma_f32_16x16x32_bf16 v[234:237], v[234:237], v[72:75], v[238:241]
	v_mfma_f32_16x16x32_bf16 v[230:233], v[230:233], v[76:79], v[234:237]
	v_mfma_f32_16x16x32_bf16 v[226:229], v[226:229], v[80:83], v[230:233]
	v_mfma_f32_16x16x32_bf16 v[222:225], v[222:225], v[84:87], v[226:229]
	v_mfma_f32_16x16x32_bf16 v[64:67], v[64:67], v[88:91], v[222:225]
	v_mfma_f32_16x16x32_bf16 v[56:59], v[56:59], v[92:95], v[64:67]
	v_mfma_f32_16x16x32_bf16 v[56:59], v[48:51], v[96:99], v[56:59]
	ds_read_b128 v[48:51], v137 offset:49408
	s_nop 4
	ds_read_b128 v[64:67], v186 offset:49408
	ds_read_b128 v[222:225], v187 offset:49408
	ds_read_b128 v[226:229], v188 offset:49408
	ds_read_b128 v[230:233], v137 offset:49152
	ds_read_b128 v[234:237], v186 offset:49152
	ds_read_b128 v[238:241], v187 offset:49152
	ds_read_b128 v[242:245], v188 offset:49152
	s_waitcnt lgkmcnt(0)
	v_mfma_f32_16x16x32_bf16 v[242:245], v[242:245], v[68:71], 0
	v_mfma_f32_16x16x32_bf16 v[238:241], v[238:241], v[72:75], v[242:245]
	v_mfma_f32_16x16x32_bf16 v[234:237], v[234:237], v[76:79], v[238:241]
	v_mfma_f32_16x16x32_bf16 v[230:233], v[230:233], v[80:83], v[234:237]
	v_mfma_f32_16x16x32_bf16 v[226:229], v[226:229], v[84:87], v[230:233]
	v_mfma_f32_16x16x32_bf16 v[222:225], v[222:225], v[88:91], v[226:229]
	v_mfma_f32_16x16x32_bf16 v[64:67], v[64:67], v[92:95], v[222:225]
	v_mfma_f32_16x16x32_bf16 v[48:51], v[48:51], v[96:99], v[64:67]
	s_nop 6
	ds_read_b128 v[64:67], v137 offset:57600
	ds_read_b128 v[222:225], v186 offset:57600
	ds_read_b128 v[226:229], v187 offset:57600
	ds_read_b128 v[230:233], v188 offset:57600
	ds_read_b128 v[234:237], v137 offset:57344
	ds_read_b128 v[238:241], v186 offset:57344
	ds_read_b128 v[242:245], v187 offset:57344
	ds_read_b128 v[246:249], v188 offset:57344
	s_waitcnt lgkmcnt(0)
	s_barrier
	s_waitcnt lgkmcnt(0)
	v_mfma_f32_16x16x32_bf16 v[246:249], v[246:249], v[68:71], 0
	buffer_load_dwordx4 v140, s[8:11], 0 offen lds
	s_mov_b32 m0, s30
	v_mfma_f32_16x16x32_bf16 v[242:245], v[242:245], v[72:75], v[246:249]
	buffer_load_dwordx4 v141, s[8:11], 0 offen lds
	s_mov_b32 m0, s31
	v_mfma_f32_16x16x32_bf16 v[238:241], v[238:241], v[76:79], v[242:245]
	buffer_load_dwordx4 v142, s[8:11], 0 offen lds
	s_mov_b32 m0, s35
	v_mfma_f32_16x16x32_bf16 v[234:237], v[234:237], v[80:83], v[238:241]
	buffer_load_dwordx4 v143, s[8:11], 0 offen lds
	s_mov_b32 m0, s37
	v_mfma_f32_16x16x32_bf16 v[230:233], v[230:233], v[84:87], v[234:237]
	buffer_load_dwordx4 v144, s[8:11], 0 offen lds
	s_mov_b32 m0, s39
	v_mfma_f32_16x16x32_bf16 v[226:229], v[226:229], v[88:91], v[230:233]
	buffer_load_dwordx4 v145, s[8:11], 0 offen lds
	s_mov_b32 m0, s41
	v_mfma_f32_16x16x32_bf16 v[222:225], v[222:225], v[92:95], v[226:229]
	buffer_load_dwordx4 v146, s[8:11], 0 offen lds
	s_mov_b32 m0, s48
	s_nop 0
	buffer_load_dwordx4 v147, s[8:11], 0 offen lds
	v_mfma_f32_16x16x32_bf16 v[64:67], v[64:67], v[96:99], v[222:225]
	ds_read_b128 v[226:229], v102
	s_mov_b32 m0, s50
	s_nop 0
	ds_read_b128 v[222:225], v103
	s_waitcnt lgkmcnt(0)
	v_mfma_f32_16x16x32_bf16 v[222:225], v[222:225], v[68:71], 0
	v_mfma_f32_16x16x32_bf16 v[222:225], v[226:229], v[72:75], v[222:225]
	ds_read_b128 v[226:229], v101
	s_waitcnt lgkmcnt(0)
	v_mfma_f32_16x16x32_bf16 v[222:225], v[226:229], v[76:79], v[222:225]
	ds_read_b128 v[226:229], v100
	s_waitcnt lgkmcnt(0)
	v_mfma_f32_16x16x32_bf16 v[222:225], v[226:229], v[80:83], v[222:225]
	ds_read_b128 v[226:229], v103 offset:256
	s_waitcnt lgkmcnt(0)
	v_mfma_f32_16x16x32_bf16 v[222:225], v[226:229], v[84:87], v[222:225]
	ds_read_b128 v[226:229], v102 offset:256
	s_waitcnt lgkmcnt(0)
	v_mfma_f32_16x16x32_bf16 v[222:225], v[226:229], v[88:91], v[222:225]
	ds_read_b128 v[226:229], v101 offset:256
	ds_read_b128 v[100:103], v100 offset:256
	s_waitcnt lgkmcnt(1)
	v_mfma_f32_16x16x32_bf16 v[222:225], v[226:229], v[92:95], v[222:225]
	s_waitcnt lgkmcnt(0)
	v_mfma_f32_16x16x32_bf16 v[100:103], v[100:103], v[96:99], v[222:225]
	s_nop 5
	ds_read_b128 v[222:225], v105 offset:256
	ds_read_b128 v[226:229], v106 offset:256
	ds_read_b128 v[230:233], v107 offset:256
	ds_read_b128 v[234:237], v216 offset:256
	ds_read_b128 v[238:241], v218
	ds_read_b128 v[242:245], v219
	ds_read_b128 v[218:221], v220
	ds_read_b128 v[104:107], v104
	s_waitcnt lgkmcnt(0)
	v_mfma_f32_16x16x32_bf16 v[104:107], v[104:107], v[68:71], 0
	v_mfma_f32_16x16x32_bf16 v[104:107], v[218:221], v[72:75], v[104:107]
	v_mfma_f32_16x16x32_bf16 v[104:107], v[242:245], v[76:79], v[104:107]
	v_mfma_f32_16x16x32_bf16 v[104:107], v[238:241], v[80:83], v[104:107]
	v_mfma_f32_16x16x32_bf16 v[104:107], v[234:237], v[84:87], v[104:107]
	v_mfma_f32_16x16x32_bf16 v[104:107], v[230:233], v[88:91], v[104:107]
	v_mfma_f32_16x16x32_bf16 v[104:107], v[226:229], v[92:95], v[104:107]
	v_mfma_f32_16x16x32_bf16 v[104:107], v[222:225], v[96:99], v[104:107]
	ds_read_b128 v[218:221], v109 offset:256
	ds_read_b128 v[222:225], v110 offset:256
	ds_read_b128 v[226:229], v111 offset:256
	ds_read_b128 v[230:233], v212 offset:256
	ds_read_b128 v[234:237], v213
	ds_read_b128 v[238:241], v214
	ds_read_b128 v[212:215], v215
	ds_read_b128 v[108:111], v108
	s_waitcnt lgkmcnt(0)
	v_mfma_f32_16x16x32_bf16 v[108:111], v[108:111], v[68:71], 0
	v_mfma_f32_16x16x32_bf16 v[108:111], v[212:215], v[72:75], v[108:111]
	v_mfma_f32_16x16x32_bf16 v[108:111], v[238:241], v[76:79], v[108:111]
	v_mfma_f32_16x16x32_bf16 v[108:111], v[234:237], v[80:83], v[108:111]
	v_mfma_f32_16x16x32_bf16 v[108:111], v[230:233], v[84:87], v[108:111]
	v_mfma_f32_16x16x32_bf16 v[108:111], v[226:229], v[88:91], v[108:111]
	v_mfma_f32_16x16x32_bf16 v[108:111], v[222:225], v[92:95], v[108:111]
	v_mfma_f32_16x16x32_bf16 v[108:111], v[218:221], v[96:99], v[108:111]
	ds_read_b128 v[212:215], v113 offset:256
	ds_read_b128 v[218:221], v114 offset:256
	ds_read_b128 v[222:225], v115 offset:256
	ds_read_b128 v[226:229], v208 offset:256
	ds_read_b128 v[230:233], v209
	ds_read_b128 v[234:237], v210
	ds_read_b128 v[208:211], v211
	ds_read_b128 v[112:115], v112
	s_waitcnt lgkmcnt(0)
	v_mfma_f32_16x16x32_bf16 v[112:115], v[112:115], v[68:71], 0
	v_mfma_f32_16x16x32_bf16 v[112:115], v[208:211], v[72:75], v[112:115]
	v_mfma_f32_16x16x32_bf16 v[112:115], v[234:237], v[76:79], v[112:115]
	v_mfma_f32_16x16x32_bf16 v[112:115], v[230:233], v[80:83], v[112:115]
	v_mfma_f32_16x16x32_bf16 v[112:115], v[226:229], v[84:87], v[112:115]
	v_mfma_f32_16x16x32_bf16 v[112:115], v[222:225], v[88:91], v[112:115]
	v_mfma_f32_16x16x32_bf16 v[112:115], v[218:221], v[92:95], v[112:115]
	v_mfma_f32_16x16x32_bf16 v[112:115], v[212:215], v[96:99], v[112:115]
	ds_read_b128 v[208:211], v118 offset:256
	ds_read_b128 v[212:215], v119 offset:256
	ds_read_b128 v[218:221], v204 offset:256
	ds_read_b128 v[222:225], v205 offset:256
	ds_read_b128 v[226:229], v206
	ds_read_b128 v[204:207], v207
	ds_read_b128 v[230:233], v117
	ds_read_b128 v[116:119], v116
	s_waitcnt lgkmcnt(0)
	v_mfma_f32_16x16x32_bf16 v[116:119], v[116:119], v[68:71], 0
	v_mfma_f32_16x16x32_bf16 v[116:119], v[230:233], v[72:75], v[116:119]
	v_mfma_f32_16x16x32_bf16 v[116:119], v[204:207], v[76:79], v[116:119]
	v_mfma_f32_16x16x32_bf16 v[116:119], v[226:229], v[80:83], v[116:119]
	v_mfma_f32_16x16x32_bf16 v[116:119], v[222:225], v[84:87], v[116:119]
	v_mfma_f32_16x16x32_bf16 v[116:119], v[218:221], v[88:91], v[116:119]
	v_mfma_f32_16x16x32_bf16 v[116:119], v[212:215], v[92:95], v[116:119]
	v_mfma_f32_16x16x32_bf16 v[116:119], v[208:211], v[96:99], v[116:119]
	ds_read_b128 v[204:207], v122 offset:256
	ds_read_b128 v[208:211], v123 offset:256
	ds_read_b128 v[212:215], v200 offset:256
	ds_read_b128 v[218:221], v201 offset:256
	ds_read_b128 v[222:225], v202
	ds_read_b128 v[200:203], v203
	ds_read_b128 v[226:229], v121
	ds_read_b128 v[120:123], v120
	s_waitcnt lgkmcnt(0)
	v_mfma_f32_16x16x32_bf16 v[120:123], v[120:123], v[68:71], 0
	v_mfma_f32_16x16x32_bf16 v[120:123], v[226:229], v[72:75], v[120:123]
	v_mfma_f32_16x16x32_bf16 v[120:123], v[200:203], v[76:79], v[120:123]
	v_mfma_f32_16x16x32_bf16 v[120:123], v[222:225], v[80:83], v[120:123]
	v_mfma_f32_16x16x32_bf16 v[120:123], v[218:221], v[84:87], v[120:123]
	v_mfma_f32_16x16x32_bf16 v[120:123], v[212:215], v[88:91], v[120:123]
	v_mfma_f32_16x16x32_bf16 v[120:123], v[208:211], v[92:95], v[120:123]
	v_mfma_f32_16x16x32_bf16 v[120:123], v[204:207], v[96:99], v[120:123]
	ds_read_b128 v[200:203], v125 offset:256
	ds_read_b128 v[204:207], v126 offset:256
	ds_read_b128 v[208:211], v124 offset:256
	ds_read_b128 v[124:127], v127 offset:256
	ds_read_b128 v[212:215], v196
	ds_read_b128 v[218:221], v199
	ds_read_b128 v[222:225], v197
	ds_read_b128 v[196:199], v198
	s_waitcnt lgkmcnt(0)
	v_mfma_f32_16x16x32_bf16 v[196:199], v[196:199], v[68:71], 0
	v_mfma_f32_16x16x32_bf16 v[196:199], v[222:225], v[72:75], v[196:199]
	v_mfma_f32_16x16x32_bf16 v[196:199], v[218:221], v[76:79], v[196:199]
	v_mfma_f32_16x16x32_bf16 v[196:199], v[212:215], v[80:83], v[196:199]
	v_mfma_f32_16x16x32_bf16 v[124:127], v[124:127], v[84:87], v[196:199]
	v_mfma_f32_16x16x32_bf16 v[124:127], v[208:211], v[88:91], v[124:127]
	v_mfma_f32_16x16x32_bf16 v[124:127], v[204:207], v[92:95], v[124:127]
	v_mfma_f32_16x16x32_bf16 v[124:127], v[200:203], v[96:99], v[124:127]
	s_nop 3
	ds_read_b128 v[196:199], v189 offset:256
	ds_read_b128 v[200:203], v191 offset:256
	ds_read_b128 v[204:207], v135 offset:256
	ds_read_b128 v[208:211], v190 offset:256
	ds_read_b128 v[212:215], v192
	ds_read_b128 v[190:193], v193
	ds_read_b128 v[218:221], v194
	ds_read_b128 v[222:225], v195
	s_waitcnt vmcnt(0)
	s_waitcnt lgkmcnt(0)
	s_waitcnt lgkmcnt(0)
	v_mfma_f32_16x16x32_bf16 v[68:71], v[222:225], v[68:71], 0
	s_barrier
	buffer_load_dwordx4 v140, s[8:11], s49 offen lds
	v_mfma_f32_16x16x32_bf16 v[68:71], v[218:221], v[72:75], v[68:71]
	v_max_f32_e32 v72, v45, v45
	v_max_f32_e32 v73, v44, v44
	v_max_f32_e32 v72, v73, v72
	v_max_f32_e32 v73, v47, v47
	v_max_f32_e32 v74, v46, v46
	v_max_f32_e32 v73, v74, v73
	v_max3_f32 v72, v72, s61, v73
	v_max_f32_e32 v73, v61, v61
	v_max_f32_e32 v74, v60, v60
	v_max_f32_e32 v73, v74, v73
	v_max_f32_e32 v74, v63, v63
	v_max_f32_e32 v75, v62, v62
	v_max_f32_e32 v74, v75, v74
	v_max3_f32 v72, v72, v73, v74
	v_max_f32_e32 v73, v37, v37
	v_max_f32_e32 v74, v36, v36
	v_max_f32_e32 v73, v74, v73
	v_max_f32_e32 v74, v39, v39
	v_max_f32_e32 v75, v38, v38
	v_max_f32_e32 v74, v75, v74
	v_max3_f32 v72, v72, v73, v74
	v_max_f32_e32 v73, v53, v53
	v_max_f32_e32 v74, v52, v52
	v_max_f32_e32 v73, v74, v73
	v_max_f32_e32 v74, v55, v55
	v_max_f32_e32 v75, v54, v54
	v_max_f32_e32 v74, v75, v74
	v_max3_f32 v72, v72, v73, v74
	v_max_f32_e32 v73, v41, v41
	v_max_f32_e32 v74, v40, v40
	v_max_f32_e32 v73, v74, v73
	v_max_f32_e32 v74, v43, v43
	v_max_f32_e32 v75, v42, v42
	v_max_f32_e32 v74, v75, v74
	v_max3_f32 v72, v72, v73, v74
	v_max_f32_e32 v73, v57, v57
	v_max_f32_e32 v74, v56, v56
	v_max_f32_e32 v73, v74, v73
	v_max_f32_e32 v74, v59, v59
	v_max_f32_e32 v75, v58, v58
	v_max_f32_e32 v74, v75, v74
	v_max3_f32 v72, v72, v73, v74
	v_max_f32_e32 v73, v49, v49
	v_max_f32_e32 v74, v48, v48
	v_max_f32_e32 v73, v74, v73
	v_max_f32_e32 v74, v51, v51
	v_max_f32_e32 v75, v50, v50
	v_max_f32_e32 v74, v75, v74
	v_mfma_f32_16x16x32_bf16 v[68:71], v[190:193], v[76:79], v[68:71]
	v_max3_f32 v72, v72, v73, v74
	v_max_f32_e32 v73, v65, v65
	v_max_f32_e32 v74, v64, v64
	v_max_f32_e32 v73, v74, v73
	v_max_f32_e32 v74, v67, v67
	v_max_f32_e32 v75, v66, v66
	v_max_f32_e32 v74, v75, v74
	v_max3_f32 v72, v72, v73, v74
	v_max_f32_e32 v73, v101, v101
	v_max_f32_e32 v74, v100, v100
	v_mfma_f32_16x16x32_bf16 v[68:71], v[212:215], v[80:83], v[68:71]
	v_max_f32_e32 v73, v74, v73
	v_max_f32_e32 v74, v103, v103
	v_max_f32_e32 v75, v102, v102
	v_max_f32_e32 v74, v75, v74
	v_max3_f32 v72, v72, v73, v74
	v_max_f32_e32 v73, v105, v105
	v_max_f32_e32 v74, v104, v104
	v_max_f32_e32 v73, v74, v73
	v_max_f32_e32 v74, v107, v107
	v_max_f32_e32 v75, v106, v106
	v_mfma_f32_16x16x32_bf16 v[68:71], v[208:211], v[84:87], v[68:71]
	v_max_f32_e32 v74, v75, v74
	v_max3_f32 v72, v72, v73, v74
	v_max_f32_e32 v73, v109, v109
	v_max_f32_e32 v74, v108, v108
	v_max_f32_e32 v73, v74, v73
	v_max_f32_e32 v74, v111, v111
	v_max_f32_e32 v75, v110, v110
	v_max_f32_e32 v74, v75, v74
	v_mfma_f32_16x16x32_bf16 v[68:71], v[204:207], v[88:91], v[68:71]
	v_max3_f32 v72, v72, v73, v74
	v_max_f32_e32 v73, v113, v113
	v_max_f32_e32 v74, v112, v112
	v_max_f32_e32 v73, v74, v73
	v_max_f32_e32 v74, v115, v115
	v_max_f32_e32 v75, v114, v114
	v_max_f32_e32 v74, v75, v74
	v_max3_f32 v72, v72, v73, v74
	v_max_f32_e32 v73, v117, v117
	v_max_f32_e32 v74, v116, v116
	v_mfma_f32_16x16x32_bf16 v[68:71], v[200:203], v[92:95], v[68:71]
	v_max_f32_e32 v73, v74, v73
	v_max_f32_e32 v74, v119, v119
	v_max_f32_e32 v75, v118, v118
	v_max_f32_e32 v74, v75, v74
	v_max3_f32 v72, v72, v73, v74
	v_max_f32_e32 v73, v121, v121
	v_max_f32_e32 v74, v120, v120
	v_max_f32_e32 v73, v74, v73
	v_max_f32_e32 v74, v123, v123
	v_max_f32_e32 v75, v122, v122
	v_mfma_f32_16x16x32_bf16 v[68:71], v[196:199], v[96:99], v[68:71]
	v_max_f32_e32 v74, v75, v74
	v_max3_f32 v72, v72, v73, v74
	v_max_f32_e32 v73, v125, v125
	v_max_f32_e32 v74, v124, v124
	v_max_f32_e32 v73, v74, v73
	v_max_f32_e32 v74, v127, v127
	v_max_f32_e32 v75, v126, v126
	v_max_f32_e32 v74, v75, v74
	v_max3_f32 v72, v72, v73, v74
	v_max_f32_e32 v73, v69, v69
	v_max_f32_e32 v74, v68, v68
	v_max_f32_e32 v73, v74, v73
	v_max_f32_e32 v74, v71, v71
	v_max_f32_e32 v75, v70, v70
	v_max_f32_e32 v74, v75, v74
	v_max3_f32 v72, v72, v73, v74
	ds_bpermute_b32 v73, v148, v72
	s_mov_b32 m0, s51
	v_mov_b32_e32 v135, v130
	buffer_load_dwordx4 v141, s[8:11], s49 offen lds
	s_mov_b32 m0, s52
	s_waitcnt lgkmcnt(0)
	v_max_f32_e32 v73, v73, v73
	v_max_f32_e32 v72, v72, v73
	ds_bpermute_b32 v73, v149, v72
	buffer_load_dwordx4 v142, s[8:11], s49 offen lds
	s_mov_b32 m0, s53
	s_waitcnt lgkmcnt(0)
	v_max_f32_e32 v73, v73, v73
	v_max_f32_e32 v72, v72, v73
	v_sub_f32_e32 v44, v44, v72
	v_sub_f32_e32 v40, v40, v72
	v_exp_f32_e32 v74, v44
	v_sub_f32_e32 v44, v60, v72
	v_exp_f32_e32 v98, v40
	v_sub_f32_e32 v40, v56, v72
	v_exp_f32_e32 v75, v44
	v_sub_f32_e32 v44, v45, v72
	v_exp_f32_e32 v99, v40
	v_sub_f32_e32 v40, v41, v72
	v_exp_f32_e32 v76, v44
	v_sub_f32_e32 v44, v61, v72
	v_sub_f32_e32 v36, v36, v72
	v_exp_f32_e32 v189, v40
	v_sub_f32_e32 v40, v57, v72
	v_exp_f32_e32 v77, v44
	v_sub_f32_e32 v44, v46, v72
	v_exp_f32_e32 v60, v36
	v_sub_f32_e32 v36, v52, v72
	v_exp_f32_e32 v190, v40
	v_sub_f32_e32 v40, v42, v72
	v_exp_f32_e32 v78, v44
	v_sub_f32_e32 v44, v62, v72
	v_exp_f32_e32 v62, v36
	v_sub_f32_e32 v36, v37, v72
	v_exp_f32_e32 v191, v40
	v_sub_f32_e32 v40, v58, v72
	v_exp_f32_e32 v84, v36
	v_sub_f32_e32 v36, v53, v72
	v_exp_f32_e32 v192, v40
	v_sub_f32_e32 v40, v43, v72
	v_exp_f32_e32 v82, v36
	v_sub_f32_e32 v36, v38, v72
	v_exp_f32_e32 v193, v40
	v_sub_f32_e32 v40, v59, v72
	v_exp_f32_e32 v79, v44
	v_sub_f32_e32 v44, v47, v72
	v_exp_f32_e32 v61, v36
	v_sub_f32_e32 v36, v54, v72
	v_exp_f32_e32 v194, v40
	v_sub_f32_e32 v40, v48, v72
	v_exp_f32_e32 v80, v44
	v_sub_f32_e32 v44, v63, v72
	v_exp_f32_e32 v63, v36
	v_sub_f32_e32 v36, v39, v72
	v_exp_f32_e32 v195, v40
	v_sub_f32_e32 v40, v64, v72
	v_exp_f32_e32 v85, v36
	v_sub_f32_e32 v36, v55, v72
	v_exp_f32_e32 v55, v40
	v_sub_f32_e32 v40, v49, v72
	v_exp_f32_e32 v131, v40
	v_sub_f32_e32 v40, v65, v72
	v_exp_f32_e32 v81, v44
	v_exp_f32_e32 v59, v40
	v_sub_f32_e32 v40, v50, v72
	v_exp_f32_e32 v83, v36
	v_exp_f32_e32 v196, v40
	v_sub_f32_e32 v40, v66, v72
	v_exp_f32_e32 v57, v40
	v_sub_f32_e32 v40, v51, v72
	v_exp_f32_e32 v197, v40
	v_pk_add_f32 v[44:45], v[74:75], v[76:77]
	v_pk_add_f32 v[46:47], v[78:79], v[80:81]
	v_sub_f32_e32 v40, v67, v72
	v_pk_add_f32 v[44:45], v[44:45], v[46:47]
	v_pk_add_f32 v[36:37], v[60:61], v[84:85]
	v_pk_add_f32 v[38:39], v[62:63], v[82:83]
	v_exp_f32_e32 v87, v40
	v_pk_add_f32 v[40:41], v[44:45], v[44:45] op_sel:[0,1] op_sel_hi:[1,0]
	v_pk_add_f32 v[36:37], v[36:37], v[36:37] op_sel:[0,1] op_sel_hi:[1,0]
	v_pk_add_f32 v[38:39], v[38:39], v[38:39] op_sel:[0,1] op_sel_hi:[1,0]
	v_mov_b32_e32 v41, v195
	v_mov_b32_e32 v37, v196
	v_mov_b32_e32 v39, v197
	v_add_f32_e32 v54, v98, v189
	v_add_f32_e32 v58, v191, v193
	v_add_f32_e32 v56, v99, v190
	v_add_f32_e32 v86, v192, v194
	v_pk_add_f32 v[40:41], v[40:41], v[130:131]
	v_pk_add_f32 v[36:37], v[36:37], v[38:39]
	v_pk_add_f32 v[38:39], v[54:55], v[58:59]
	v_pk_add_f32 v[36:37], v[40:41], v[36:37]
	v_pk_add_f32 v[40:41], v[56:57], v[86:87]
	buffer_load_dwordx4 v143, s[8:11], s49 offen lds
	v_pk_add_f32 v[38:39], v[38:39], v[40:41]
	s_mov_b32 m0, s54
	v_pk_add_f32 v[36:37], v[36:37], v[38:39]
	v_sub_f32_e32 v38, v100, v72
	v_exp_f32_e32 v50, v38
	v_sub_f32_e32 v38, v104, v72
	v_exp_f32_e32 v51, v38
	v_sub_f32_e32 v38, v101, v72
	v_exp_f32_e32 v52, v38
	v_sub_f32_e32 v38, v105, v72
	v_exp_f32_e32 v53, v38
	v_sub_f32_e32 v38, v102, v72
	v_exp_f32_e32 v64, v38
	v_sub_f32_e32 v38, v106, v72
	v_exp_f32_e32 v65, v38
	v_sub_f32_e32 v38, v103, v72
	v_exp_f32_e32 v66, v38
	v_sub_f32_e32 v38, v107, v72
	v_exp_f32_e32 v67, v38
	v_pk_add_f32 v[38:39], v[50:51], v[52:53]
	buffer_load_dwordx4 v144, s[8:11], s49 offen lds
	s_mov_b32 m0, s55
	v_pk_add_f32 v[40:41], v[64:65], v[66:67]
	buffer_load_dwordx4 v145, s[8:11], s49 offen lds
	v_pk_add_f32 v[38:39], v[38:39], v[40:41]
	v_sub_f32_e32 v40, v108, v72
	v_exp_f32_e32 v44, v40
	v_sub_f32_e32 v40, v112, v72
	v_exp_f32_e32 v46, v40
	v_sub_f32_e32 v40, v109, v72
	v_exp_f32_e32 v48, v40
	v_sub_f32_e32 v40, v113, v72
	v_exp_f32_e32 v88, v40
	v_sub_f32_e32 v40, v110, v72
	v_exp_f32_e32 v45, v40
	v_sub_f32_e32 v40, v114, v72
	v_exp_f32_e32 v47, v40
	v_sub_f32_e32 v40, v111, v72
	v_exp_f32_e32 v49, v40
	v_sub_f32_e32 v40, v115, v72
	v_exp_f32_e32 v89, v40
	s_mov_b32 m0, s56
	v_pk_add_f32 v[40:41], v[44:45], v[48:49]
	v_cvt_pk_bf16_f32 v44, v44, v48
	v_cvt_pk_bf16_f32 v45, v45, v49
	v_cvt_pk_bf16_f32 v48, v50, v52
	v_cvt_pk_bf16_f32 v49, v64, v66
	v_cvt_pk_bf16_f32 v50, v51, v53
	v_cvt_pk_bf16_f32 v51, v65, v67
	v_cvt_pk_bf16_f32 v64, v74, v76
	v_cvt_pk_bf16_f32 v65, v78, v80
	v_cvt_pk_bf16_f32 v66, v75, v77
	v_cvt_pk_bf16_f32 v67, v79, v81
	v_mov_b64_e32 v[76:77], v[2:3]
	v_mov_b64_e32 v[80:81], v[2:3]
	buffer_load_dwordx4 v146, s[8:11], s49 offen lds
	s_mov_b32 m0, s57
	v_mov_b64_e32 v[74:75], v[0:1]
	v_mov_b64_e32 v[78:79], v[0:1]
	buffer_load_dwordx4 v147, s[8:11], s49 offen lds
	v_cvt_pk_bf16_f32 v60, v60, v84
	v_cvt_pk_bf16_f32 v61, v61, v85
	v_cvt_pk_bf16_f32 v62, v62, v82
	v_cvt_pk_bf16_f32 v63, v63, v83
	ds_read_b128 v[82:85], v188
	s_waitcnt lgkmcnt(0)
	v_mfma_f32_16x16x32_bf16 v[74:77], v[82:85], v[4:7], v[74:77]
	v_sub_f32_e32 v73, v121, v72
	v_exp_f32_e32 v86, v73
	v_sub_f32_e32 v73, v118, v72
	v_mfma_f32_16x16x32_bf16 v[78:81], v[82:85], v[64:67], v[78:81]
	ds_read_b128 v[82:85], v187
	v_exp_f32_e32 v100, v73
	v_sub_f32_e32 v73, v122, v72
	v_sub_f32_e32 v68, v68, v72
	v_exp_f32_e32 v101, v73
	v_sub_f32_e32 v73, v119, v72
	v_exp_f32_e32 v91, v68
	v_sub_f32_e32 v68, v125, v72
	v_exp_f32_e32 v102, v73
	v_sub_f32_e32 v73, v123, v72
	v_exp_f32_e32 v105, v68
	v_sub_f32_e32 v68, v69, v72
	v_exp_f32_e32 v103, v73
	v_sub_f32_e32 v73, v124, v72
	v_exp_f32_e32 v93, v68
	v_sub_f32_e32 v68, v126, v72
	v_exp_f32_e32 v104, v73
	v_exp_f32_e32 v69, v68
	v_sub_f32_e32 v68, v70, v72
	v_exp_f32_e32 v95, v68
	v_sub_f32_e32 v68, v127, v72
	s_waitcnt lgkmcnt(0)
	v_mfma_f32_16x16x32_bf16 v[74:77], v[82:85], v[8:11], v[74:77]
	v_sub_f32_e32 v54, v116, v72
	v_sub_f32_e32 v56, v120, v72
	v_sub_f32_e32 v58, v117, v72
	v_mfma_f32_16x16x32_bf16 v[78:81], v[82:85], v[60:63], v[78:81]
	ds_read_b128 v[82:85], v186
	v_exp_f32_e32 v106, v68
	v_exp_f32_e32 v54, v54
	v_exp_f32_e32 v56, v56
	v_exp_f32_e32 v58, v58
	v_sub_f32_e32 v68, v71, v72
	v_pk_add_f32 v[36:37], v[36:37], v[36:37] op_sel:[0,1] op_sel_hi:[1,0]
	v_pk_add_f32 v[38:39], v[38:39], v[38:39] op_sel:[0,1] op_sel_hi:[1,0]
	v_pk_add_f32 v[42:43], v[46:47], v[88:89]
	v_exp_f32_e32 v97, v68
	v_mov_b32_e32 v37, v104
	v_mov_b32_e32 v39, v105
	v_pk_add_f32 v[36:37], v[36:37], v[38:39]
	v_pk_add_f32 v[38:39], v[40:41], v[40:41] op_sel:[0,1] op_sel_hi:[1,0]
	v_pk_add_f32 v[40:41], v[42:43], v[42:43] op_sel:[0,1] op_sel_hi:[1,0]
	v_mov_b32_e32 v39, v69
	v_mov_b32_e32 v41, v106
	v_add_f32_e32 v90, v54, v58
	v_add_f32_e32 v92, v100, v102
	v_add_f32_e32 v94, v56, v86
	v_add_f32_e32 v96, v101, v103
	v_pk_add_f32 v[38:39], v[38:39], v[40:41]
	v_pk_add_f32 v[40:41], v[94:95], v[96:97]
	v_pk_add_f32 v[36:37], v[36:37], v[38:39]
	v_pk_add_f32 v[38:39], v[90:91], v[92:93]
	v_cvt_pk_bf16_f32 v42, v56, v86
	v_pk_add_f32 v[38:39], v[38:39], v[40:41]
	v_cvt_pk_bf16_f32 v40, v54, v58
	v_cvt_pk_bf16_f32 v54, v55, v59
	v_cvt_pk_bf16_f32 v55, v57, v87
	v_cvt_pk_bf16_f32 v56, v98, v189
	v_cvt_pk_bf16_f32 v57, v191, v193
	v_cvt_pk_bf16_f32 v58, v99, v190
	v_cvt_pk_bf16_f32 v59, v192, v194
	s_waitcnt lgkmcnt(0)
	v_mfma_f32_16x16x32_bf16 v[74:77], v[82:85], v[12:15], v[74:77]
	v_cvt_pk_bf16_f32 v52, v195, v131
	v_cvt_pk_bf16_f32 v53, v196, v197
	v_cvt_pk_bf16_f32 v46, v46, v88
	v_mfma_f32_16x16x32_bf16 v[78:81], v[82:85], v[56:59], v[78:81]
	ds_read_b128 v[82:85], v137
	v_cvt_pk_bf16_f32 v47, v47, v89
	v_pk_add_f32 v[36:37], v[36:37], v[38:39]
	s_waitcnt lgkmcnt(0)
	v_mfma_f32_16x16x32_bf16 v[74:77], v[82:85], v[16:19], v[74:77]
	v_add_f32_e32 v36, v36, v37
	ds_bpermute_b32 v37, v148, v36
	v_cvt_pk_bf16_f32 v41, v100, v102
	v_mfma_f32_16x16x32_bf16 v[78:81], v[82:85], v[52:55], v[78:81]
	ds_read_b128 v[82:85], v188 offset:256
	v_cvt_pk_bf16_f32 v43, v101, v103
	s_waitcnt lgkmcnt(1)
	v_add_f32_e32 v36, v36, v37
	s_waitcnt lgkmcnt(0)
	v_mfma_f32_16x16x32_bf16 v[74:77], v[82:85], v[20:23], v[74:77]
	ds_bpermute_b32 v37, v149, v36
	v_cvt_pk_bf16_f32 v38, v91, v93
	v_cvt_pk_bf16_f32 v39, v95, v97
	v_mfma_f32_16x16x32_bf16 v[78:81], v[82:85], v[48:51], v[78:81]
	ds_read_b128 v[82:85], v187 offset:256
	s_waitcnt lgkmcnt(1)
	v_add_f32_e32 v36, v36, v37
	v_rcp_f32_e32 v68, v36
	s_waitcnt lgkmcnt(0)
	v_mfma_f32_16x16x32_bf16 v[74:77], v[82:85], v[24:27], v[74:77]
	v_lshl_add_u64 v[36:37], s[24:25], 0, v[138:139]
	v_lshl_add_u64 v[36:37], v[36:37], 0, s[2:3]
	v_lshl_add_u64 v[70:71], v[36:37], 0, v[134:135]
	v_mfma_f32_16x16x32_bf16 v[78:81], v[82:85], v[44:47], v[78:81]
	ds_read_b128 v[82:85], v186 offset:256
	v_cvt_pk_bf16_f32 v36, v104, v105
	v_cvt_pk_bf16_f32 v37, v69, v106
	s_waitcnt lgkmcnt(0)
	v_mfma_f32_16x16x32_bf16 v[74:77], v[82:85], v[28:31], v[74:77]
	v_lshl_add_u64 v[72:73], v[70:71], 0, s[26:27]
	s_bfe_i32 s8, s0, 0x80000
	s_bfe_u32 s8, s8, 0x5000a
	v_mfma_f32_16x16x32_bf16 v[78:81], v[82:85], v[40:43], v[78:81]
	ds_read_b128 v[82:85], v137 offset:256
	s_add_i32 s0, s0, s8
	s_bfe_i32 s0, s0, 0x80000
	s_waitcnt lgkmcnt(0)
	v_mfma_f32_16x16x32_bf16 v[74:77], v[82:85], v[32:35], v[74:77]
	s_sext_i32_i16 s0, s0
	s_ashr_i32 s0, s0, 5
	s_cmpk_lt_i32 s20, 0x200
	v_mfma_f32_16x16x32_bf16 v[78:81], v[82:85], v[36:39], v[78:81]
	s_nop 3
	v_mul_f32_e64 v74, v74, v136
	v_mul_f32_e64 v75, v75, v136
	v_pk_mul_f32 v[76:77], v[76:77], v[136:137] op_sel_hi:[1,0]
	v_cvt_pk_bf16_f32 v74, v74, v75
	v_cvt_pk_bf16_f32 v75, v76, v77
	global_store_dwordx2 v[70:71], v[74:75], off
	v_pk_mul_f32 v[76:77], v[78:79], v[68:69] op_sel_hi:[1,0]
	v_pk_mul_f32 v[78:79], v[80:81], v[68:69] op_sel_hi:[1,0]
	v_add_co_u32_e64 v74, s[2:3], s60, v70
	v_cvt_pk_bf16_f32 v76, v76, v77
	v_cvt_pk_bf16_f32 v77, v78, v79
	v_addc_co_u32_e64 v75, s[2:3], 0, v71, s[2:3]
	global_store_dwordx2 v[74:75], v[76:77], off
	v_mov_b64_e32 v[76:77], v[2:3]
	v_mov_b64_e32 v[80:81], v[2:3]
	v_mov_b64_e32 v[74:75], v[0:1]
	v_mov_b64_e32 v[78:79], v[0:1]
	ds_read_b128 v[82:85], v188 offset:8192
	s_waitcnt lgkmcnt(0)
	v_mfma_f32_16x16x32_bf16 v[74:77], v[82:85], v[4:7], v[74:77]
	s_cselect_b64 s[8:9], -1, 0
	s_and_b64 vcc, s[8:9], exec
	s_cselect_b32 s0, s0, s13
	v_mfma_f32_16x16x32_bf16 v[78:81], v[82:85], v[64:67], v[78:81]
	ds_read_b128 v[82:85], v187 offset:8192
	s_cselect_b32 s1, s1, s12
	s_lshl_b32 s0, s0, 2
	s_waitcnt lgkmcnt(0)
	v_mfma_f32_16x16x32_bf16 v[74:77], v[82:85], v[8:11], v[74:77]
	s_add_i32 s0, s0, s1
	s_ashr_i32 s1, s0, 31
	s_lshl_b64 s[0:1], s[0:1], 17
	v_mfma_f32_16x16x32_bf16 v[78:81], v[82:85], v[60:63], v[78:81]
	ds_read_b128 v[82:85], v186 offset:8192
	s_add_u32 s12, s7, s0
	s_addc_u32 s0, s28, s1
	s_waitcnt lgkmcnt(0)
	v_mfma_f32_16x16x32_bf16 v[74:77], v[82:85], v[12:15], v[74:77]
	s_and_b32 s13, s0, 0xffff
	v_mfma_f32_16x16x32_bf16 v[78:81], v[82:85], v[56:59], v[78:81]
	ds_read_b128 v[82:85], v137 offset:8192
	s_waitcnt lgkmcnt(0)
	v_mfma_f32_16x16x32_bf16 v[74:77], v[82:85], v[16:19], v[74:77]
	v_mfma_f32_16x16x32_bf16 v[78:81], v[82:85], v[52:55], v[78:81]
	ds_read_b128 v[82:85], v188 offset:8448
	s_waitcnt lgkmcnt(0)
	v_mfma_f32_16x16x32_bf16 v[74:77], v[82:85], v[20:23], v[74:77]
	v_mfma_f32_16x16x32_bf16 v[78:81], v[82:85], v[48:51], v[78:81]
	ds_read_b128 v[82:85], v187 offset:8448
	s_waitcnt lgkmcnt(0)
	v_mfma_f32_16x16x32_bf16 v[74:77], v[82:85], v[24:27], v[74:77]
	v_mfma_f32_16x16x32_bf16 v[78:81], v[82:85], v[44:47], v[78:81]
	ds_read_b128 v[82:85], v186 offset:8448
	s_waitcnt lgkmcnt(0)
	v_mfma_f32_16x16x32_bf16 v[74:77], v[82:85], v[28:31], v[74:77]
	v_mfma_f32_16x16x32_bf16 v[78:81], v[82:85], v[40:43], v[78:81]
	ds_read_b128 v[82:85], v137 offset:8448
	s_waitcnt lgkmcnt(0)
	v_mfma_f32_16x16x32_bf16 v[74:77], v[82:85], v[32:35], v[74:77]
	s_nop 7
	v_pk_mul_f32 v[74:75], v[74:75], v[136:137] op_sel_hi:[1,0]
	v_mfma_f32_16x16x32_bf16 v[78:81], v[82:85], v[36:39], v[78:81]
	v_mul_f32_e64 v76, v76, v136
	v_mul_f32_e64 v77, v77, v136
	v_cvt_pk_bf16_f32 v74, v74, v75
	v_cvt_pk_bf16_f32 v75, v76, v77
	s_nop 3
	v_pk_mul_f32 v[76:77], v[78:79], v[68:69] op_sel_hi:[1,0]
	v_pk_mul_f32 v[78:79], v[80:81], v[68:69] op_sel_hi:[1,0]
	v_cvt_pk_bf16_f32 v76, v76, v77
	v_cvt_pk_bf16_f32 v77, v78, v79
	global_store_dwordx2 v[70:71], v[74:75], off offset:32
	global_store_dwordx2 v[72:73], v[76:77], off offset:32
	v_mov_b64_e32 v[76:77], v[2:3]
	v_mov_b64_e32 v[80:81], v[2:3]
	v_mov_b64_e32 v[74:75], v[0:1]
	v_mov_b64_e32 v[78:79], v[0:1]
	ds_read_b128 v[82:85], v188 offset:16384
	s_waitcnt lgkmcnt(0)
	v_mfma_f32_16x16x32_bf16 v[74:77], v[82:85], v[4:7], v[74:77]
	v_mfma_f32_16x16x32_bf16 v[78:81], v[82:85], v[64:67], v[78:81]
	ds_read_b128 v[82:85], v187 offset:16384
	s_waitcnt lgkmcnt(0)
	v_mfma_f32_16x16x32_bf16 v[74:77], v[82:85], v[8:11], v[74:77]
	v_mfma_f32_16x16x32_bf16 v[78:81], v[82:85], v[60:63], v[78:81]
	ds_read_b128 v[82:85], v186 offset:16384
	s_waitcnt lgkmcnt(0)
	v_mfma_f32_16x16x32_bf16 v[74:77], v[82:85], v[12:15], v[74:77]
	v_mfma_f32_16x16x32_bf16 v[78:81], v[82:85], v[56:59], v[78:81]
	ds_read_b128 v[82:85], v137 offset:16384
	s_waitcnt lgkmcnt(0)
	v_mfma_f32_16x16x32_bf16 v[74:77], v[82:85], v[16:19], v[74:77]
	v_mfma_f32_16x16x32_bf16 v[78:81], v[82:85], v[52:55], v[78:81]
	ds_read_b128 v[82:85], v188 offset:16640
	s_waitcnt lgkmcnt(0)
	v_mfma_f32_16x16x32_bf16 v[74:77], v[82:85], v[20:23], v[74:77]
	v_mfma_f32_16x16x32_bf16 v[78:81], v[82:85], v[48:51], v[78:81]
	ds_read_b128 v[82:85], v187 offset:16640
	s_waitcnt lgkmcnt(0)
	v_mfma_f32_16x16x32_bf16 v[74:77], v[82:85], v[24:27], v[74:77]
	v_mfma_f32_16x16x32_bf16 v[78:81], v[82:85], v[44:47], v[78:81]
	ds_read_b128 v[82:85], v186 offset:16640
	s_waitcnt lgkmcnt(0)
	v_mfma_f32_16x16x32_bf16 v[74:77], v[82:85], v[28:31], v[74:77]
	v_mfma_f32_16x16x32_bf16 v[78:81], v[82:85], v[40:43], v[78:81]
	ds_read_b128 v[82:85], v137 offset:16640
	s_waitcnt lgkmcnt(0)
	v_mfma_f32_16x16x32_bf16 v[74:77], v[82:85], v[32:35], v[74:77]
	s_nop 7
	v_pk_mul_f32 v[74:75], v[74:75], v[136:137] op_sel_hi:[1,0]
	v_mfma_f32_16x16x32_bf16 v[78:81], v[82:85], v[36:39], v[78:81]
	v_mul_f32_e64 v76, v76, v136
	v_mul_f32_e64 v77, v77, v136
	v_cvt_pk_bf16_f32 v74, v74, v75
	v_cvt_pk_bf16_f32 v75, v76, v77
	s_nop 3
	v_pk_mul_f32 v[76:77], v[78:79], v[68:69] op_sel_hi:[1,0]
	v_pk_mul_f32 v[78:79], v[80:81], v[68:69] op_sel_hi:[1,0]
	v_cvt_pk_bf16_f32 v76, v76, v77
	v_cvt_pk_bf16_f32 v77, v78, v79
	global_store_dwordx2 v[70:71], v[74:75], off offset:64
	global_store_dwordx2 v[72:73], v[76:77], off offset:64
	v_mov_b64_e32 v[76:77], v[2:3]
	v_mov_b64_e32 v[80:81], v[2:3]
	v_mov_b64_e32 v[74:75], v[0:1]
	v_mov_b64_e32 v[78:79], v[0:1]
	ds_read_b128 v[82:85], v188 offset:24576
	s_waitcnt lgkmcnt(0)
	v_mfma_f32_16x16x32_bf16 v[74:77], v[82:85], v[4:7], v[74:77]
	v_mfma_f32_16x16x32_bf16 v[78:81], v[82:85], v[64:67], v[78:81]
	ds_read_b128 v[82:85], v187 offset:24576
	s_waitcnt lgkmcnt(0)
	v_mfma_f32_16x16x32_bf16 v[74:77], v[82:85], v[8:11], v[74:77]
	v_mfma_f32_16x16x32_bf16 v[78:81], v[82:85], v[60:63], v[78:81]
	ds_read_b128 v[82:85], v186 offset:24576
	s_waitcnt lgkmcnt(0)
	v_mfma_f32_16x16x32_bf16 v[74:77], v[82:85], v[12:15], v[74:77]
	v_mfma_f32_16x16x32_bf16 v[78:81], v[82:85], v[56:59], v[78:81]
	ds_read_b128 v[82:85], v137 offset:24576
	s_waitcnt lgkmcnt(0)
	v_mfma_f32_16x16x32_bf16 v[74:77], v[82:85], v[16:19], v[74:77]
	v_mfma_f32_16x16x32_bf16 v[78:81], v[82:85], v[52:55], v[78:81]
	ds_read_b128 v[82:85], v188 offset:24832
	s_waitcnt lgkmcnt(0)
	v_mfma_f32_16x16x32_bf16 v[74:77], v[82:85], v[20:23], v[74:77]
	v_mfma_f32_16x16x32_bf16 v[78:81], v[82:85], v[48:51], v[78:81]
	ds_read_b128 v[82:85], v187 offset:24832
	s_waitcnt lgkmcnt(0)
	v_mfma_f32_16x16x32_bf16 v[74:77], v[82:85], v[24:27], v[74:77]
	v_mfma_f32_16x16x32_bf16 v[78:81], v[82:85], v[44:47], v[78:81]
	ds_read_b128 v[82:85], v186 offset:24832
	s_waitcnt lgkmcnt(0)
	v_mfma_f32_16x16x32_bf16 v[74:77], v[82:85], v[28:31], v[74:77]
	v_mfma_f32_16x16x32_bf16 v[78:81], v[82:85], v[40:43], v[78:81]
	ds_read_b128 v[82:85], v137 offset:24832
	s_waitcnt lgkmcnt(0)
	v_mfma_f32_16x16x32_bf16 v[74:77], v[82:85], v[32:35], v[74:77]
	s_nop 7
	v_pk_mul_f32 v[74:75], v[74:75], v[136:137] op_sel_hi:[1,0]
	v_mfma_f32_16x16x32_bf16 v[78:81], v[82:85], v[36:39], v[78:81]
	v_mul_f32_e64 v76, v76, v136
	v_mul_f32_e64 v77, v77, v136
	v_cvt_pk_bf16_f32 v74, v74, v75
	v_cvt_pk_bf16_f32 v75, v76, v77
	s_nop 3
	v_pk_mul_f32 v[76:77], v[78:79], v[68:69] op_sel_hi:[1,0]
	v_pk_mul_f32 v[78:79], v[80:81], v[68:69] op_sel_hi:[1,0]
	v_cvt_pk_bf16_f32 v76, v76, v77
	v_cvt_pk_bf16_f32 v77, v78, v79
	global_store_dwordx2 v[70:71], v[74:75], off offset:96
	global_store_dwordx2 v[72:73], v[76:77], off offset:96
	v_mov_b64_e32 v[76:77], v[2:3]
	v_mov_b64_e32 v[80:81], v[2:3]
	v_mov_b64_e32 v[74:75], v[0:1]
	v_mov_b64_e32 v[78:79], v[0:1]
	ds_read_b128 v[82:85], v188 offset:32768
	s_waitcnt lgkmcnt(0)
	v_mfma_f32_16x16x32_bf16 v[74:77], v[82:85], v[4:7], v[74:77]
	v_mfma_f32_16x16x32_bf16 v[78:81], v[82:85], v[64:67], v[78:81]
	ds_read_b128 v[82:85], v187 offset:32768
	s_waitcnt lgkmcnt(0)
	v_mfma_f32_16x16x32_bf16 v[74:77], v[82:85], v[8:11], v[74:77]
	v_mfma_f32_16x16x32_bf16 v[78:81], v[82:85], v[60:63], v[78:81]
	ds_read_b128 v[82:85], v186 offset:32768
	s_waitcnt lgkmcnt(0)
	v_mfma_f32_16x16x32_bf16 v[74:77], v[82:85], v[12:15], v[74:77]
	v_mfma_f32_16x16x32_bf16 v[78:81], v[82:85], v[56:59], v[78:81]
	ds_read_b128 v[82:85], v137 offset:32768
	s_waitcnt lgkmcnt(0)
	v_mfma_f32_16x16x32_bf16 v[74:77], v[82:85], v[16:19], v[74:77]
	v_mfma_f32_16x16x32_bf16 v[78:81], v[82:85], v[52:55], v[78:81]
	ds_read_b128 v[82:85], v188 offset:33024
	s_waitcnt lgkmcnt(0)
	v_mfma_f32_16x16x32_bf16 v[74:77], v[82:85], v[20:23], v[74:77]
	v_mfma_f32_16x16x32_bf16 v[78:81], v[82:85], v[48:51], v[78:81]
	ds_read_b128 v[82:85], v187 offset:33024
	s_waitcnt lgkmcnt(0)
	v_mfma_f32_16x16x32_bf16 v[74:77], v[82:85], v[24:27], v[74:77]
	v_mfma_f32_16x16x32_bf16 v[78:81], v[82:85], v[44:47], v[78:81]
	ds_read_b128 v[82:85], v186 offset:33024
	s_waitcnt lgkmcnt(0)
	v_mfma_f32_16x16x32_bf16 v[74:77], v[82:85], v[28:31], v[74:77]
	v_mfma_f32_16x16x32_bf16 v[78:81], v[82:85], v[40:43], v[78:81]
	ds_read_b128 v[82:85], v137 offset:33024
	s_waitcnt lgkmcnt(0)
	v_mfma_f32_16x16x32_bf16 v[74:77], v[82:85], v[32:35], v[74:77]
	s_nop 7
	v_pk_mul_f32 v[74:75], v[74:75], v[136:137] op_sel_hi:[1,0]
	v_mfma_f32_16x16x32_bf16 v[78:81], v[82:85], v[36:39], v[78:81]
	v_mul_f32_e64 v76, v76, v136
	v_mul_f32_e64 v77, v77, v136
	v_cvt_pk_bf16_f32 v74, v74, v75
	v_cvt_pk_bf16_f32 v75, v76, v77
	s_nop 3
	v_pk_mul_f32 v[76:77], v[78:79], v[68:69] op_sel_hi:[1,0]
	v_pk_mul_f32 v[78:79], v[80:81], v[68:69] op_sel_hi:[1,0]
	v_cvt_pk_bf16_f32 v76, v76, v77
	v_cvt_pk_bf16_f32 v77, v78, v79
	global_store_dwordx2 v[70:71], v[74:75], off offset:128
	global_store_dwordx2 v[72:73], v[76:77], off offset:128
	v_mov_b64_e32 v[76:77], v[2:3]
	v_mov_b64_e32 v[80:81], v[2:3]
	v_mov_b64_e32 v[74:75], v[0:1]
	v_mov_b64_e32 v[78:79], v[0:1]
	ds_read_b128 v[82:85], v188 offset:40960
	s_waitcnt lgkmcnt(0)
	v_mfma_f32_16x16x32_bf16 v[74:77], v[82:85], v[4:7], v[74:77]
	v_mfma_f32_16x16x32_bf16 v[78:81], v[82:85], v[64:67], v[78:81]
	ds_read_b128 v[82:85], v187 offset:40960
	s_waitcnt lgkmcnt(0)
	v_mfma_f32_16x16x32_bf16 v[74:77], v[82:85], v[8:11], v[74:77]
	v_mfma_f32_16x16x32_bf16 v[78:81], v[82:85], v[60:63], v[78:81]
	ds_read_b128 v[82:85], v186 offset:40960
	s_waitcnt lgkmcnt(0)
	v_mfma_f32_16x16x32_bf16 v[74:77], v[82:85], v[12:15], v[74:77]
	v_mfma_f32_16x16x32_bf16 v[78:81], v[82:85], v[56:59], v[78:81]
	ds_read_b128 v[82:85], v137 offset:40960
	s_waitcnt lgkmcnt(0)
	v_mfma_f32_16x16x32_bf16 v[74:77], v[82:85], v[16:19], v[74:77]
	v_mfma_f32_16x16x32_bf16 v[78:81], v[82:85], v[52:55], v[78:81]
	ds_read_b128 v[82:85], v188 offset:41216
	s_waitcnt lgkmcnt(0)
	v_mfma_f32_16x16x32_bf16 v[74:77], v[82:85], v[20:23], v[74:77]
	v_mfma_f32_16x16x32_bf16 v[78:81], v[82:85], v[48:51], v[78:81]
	ds_read_b128 v[82:85], v187 offset:41216
	s_waitcnt lgkmcnt(0)
	v_mfma_f32_16x16x32_bf16 v[74:77], v[82:85], v[24:27], v[74:77]
	v_mfma_f32_16x16x32_bf16 v[78:81], v[82:85], v[44:47], v[78:81]
	ds_read_b128 v[82:85], v186 offset:41216
	s_waitcnt lgkmcnt(0)
	v_mfma_f32_16x16x32_bf16 v[74:77], v[82:85], v[28:31], v[74:77]
	v_mfma_f32_16x16x32_bf16 v[78:81], v[82:85], v[40:43], v[78:81]
	ds_read_b128 v[82:85], v137 offset:41216
	s_waitcnt lgkmcnt(0)
	v_mfma_f32_16x16x32_bf16 v[74:77], v[82:85], v[32:35], v[74:77]
	s_nop 7
	v_pk_mul_f32 v[74:75], v[74:75], v[136:137] op_sel_hi:[1,0]
	v_mfma_f32_16x16x32_bf16 v[78:81], v[82:85], v[36:39], v[78:81]
	v_mul_f32_e64 v76, v76, v136
	v_mul_f32_e64 v77, v77, v136
	v_cvt_pk_bf16_f32 v74, v74, v75
	v_cvt_pk_bf16_f32 v75, v76, v77
	s_nop 3
	v_pk_mul_f32 v[76:77], v[78:79], v[68:69] op_sel_hi:[1,0]
	v_pk_mul_f32 v[78:79], v[80:81], v[68:69] op_sel_hi:[1,0]
	v_cvt_pk_bf16_f32 v76, v76, v77
	v_cvt_pk_bf16_f32 v77, v78, v79
	global_store_dwordx2 v[70:71], v[74:75], off offset:160
	global_store_dwordx2 v[72:73], v[76:77], off offset:160
	v_mov_b64_e32 v[76:77], v[2:3]
	v_mov_b64_e32 v[80:81], v[2:3]
	v_mov_b64_e32 v[74:75], v[0:1]
	v_mov_b64_e32 v[78:79], v[0:1]
	ds_read_b128 v[82:85], v188 offset:49152
	s_waitcnt lgkmcnt(0)
	v_mfma_f32_16x16x32_bf16 v[74:77], v[82:85], v[4:7], v[74:77]
	v_mfma_f32_16x16x32_bf16 v[78:81], v[82:85], v[64:67], v[78:81]
	ds_read_b128 v[82:85], v187 offset:49152
	s_waitcnt lgkmcnt(0)
	v_mfma_f32_16x16x32_bf16 v[74:77], v[82:85], v[8:11], v[74:77]
	v_mfma_f32_16x16x32_bf16 v[78:81], v[82:85], v[60:63], v[78:81]
	ds_read_b128 v[82:85], v186 offset:49152
	s_waitcnt lgkmcnt(0)
	v_mfma_f32_16x16x32_bf16 v[74:77], v[82:85], v[12:15], v[74:77]
	v_mfma_f32_16x16x32_bf16 v[78:81], v[82:85], v[56:59], v[78:81]
	ds_read_b128 v[82:85], v137 offset:49152
	s_waitcnt lgkmcnt(0)
	v_mfma_f32_16x16x32_bf16 v[74:77], v[82:85], v[16:19], v[74:77]
	v_mfma_f32_16x16x32_bf16 v[78:81], v[82:85], v[52:55], v[78:81]
	ds_read_b128 v[82:85], v188 offset:49408
	s_waitcnt lgkmcnt(0)
	v_mfma_f32_16x16x32_bf16 v[74:77], v[82:85], v[20:23], v[74:77]
	v_mfma_f32_16x16x32_bf16 v[78:81], v[82:85], v[48:51], v[78:81]
	ds_read_b128 v[82:85], v187 offset:49408
	s_waitcnt lgkmcnt(0)
	v_mfma_f32_16x16x32_bf16 v[74:77], v[82:85], v[24:27], v[74:77]
	v_mfma_f32_16x16x32_bf16 v[78:81], v[82:85], v[44:47], v[78:81]
	ds_read_b128 v[82:85], v186 offset:49408
	s_waitcnt lgkmcnt(0)
	v_mfma_f32_16x16x32_bf16 v[74:77], v[82:85], v[28:31], v[74:77]
	v_mfma_f32_16x16x32_bf16 v[78:81], v[82:85], v[40:43], v[78:81]
	ds_read_b128 v[82:85], v137 offset:49408
	s_waitcnt lgkmcnt(0)
	v_mfma_f32_16x16x32_bf16 v[74:77], v[82:85], v[32:35], v[74:77]
	s_nop 7
	v_pk_mul_f32 v[74:75], v[74:75], v[136:137] op_sel_hi:[1,0]
	v_mfma_f32_16x16x32_bf16 v[78:81], v[82:85], v[36:39], v[78:81]
	v_mul_f32_e64 v76, v76, v136
	v_mul_f32_e64 v77, v77, v136
	v_cvt_pk_bf16_f32 v74, v74, v75
	v_cvt_pk_bf16_f32 v75, v76, v77
	s_nop 3
	v_pk_mul_f32 v[76:77], v[78:79], v[68:69] op_sel_hi:[1,0]
	v_pk_mul_f32 v[78:79], v[80:81], v[68:69] op_sel_hi:[1,0]
	v_cvt_pk_bf16_f32 v76, v76, v77
	v_cvt_pk_bf16_f32 v77, v78, v79
	global_store_dwordx2 v[70:71], v[74:75], off offset:192
	global_store_dwordx2 v[72:73], v[76:77], off offset:192
	v_mov_b64_e32 v[76:77], v[2:3]
	v_mov_b64_e32 v[80:81], v[2:3]
	v_mov_b64_e32 v[74:75], v[0:1]
	v_mov_b64_e32 v[78:79], v[0:1]
	ds_read_b128 v[82:85], v188 offset:57344
	s_waitcnt lgkmcnt(0)
	v_mfma_f32_16x16x32_bf16 v[74:77], v[82:85], v[4:7], v[74:77]
	v_mfma_f32_16x16x32_bf16 v[78:81], v[82:85], v[64:67], v[78:81]
	ds_read_b128 v[82:85], v187 offset:57344
	s_waitcnt lgkmcnt(0)
	v_mfma_f32_16x16x32_bf16 v[74:77], v[82:85], v[8:11], v[74:77]
	v_mfma_f32_16x16x32_bf16 v[78:81], v[82:85], v[60:63], v[78:81]
	ds_read_b128 v[82:85], v186 offset:57344
	s_waitcnt lgkmcnt(0)
	v_mfma_f32_16x16x32_bf16 v[74:77], v[82:85], v[12:15], v[74:77]
	v_mfma_f32_16x16x32_bf16 v[78:81], v[82:85], v[56:59], v[78:81]
	ds_read_b128 v[82:85], v137 offset:57344
	s_waitcnt lgkmcnt(0)
	v_mfma_f32_16x16x32_bf16 v[74:77], v[82:85], v[16:19], v[74:77]
	v_mfma_f32_16x16x32_bf16 v[78:81], v[82:85], v[52:55], v[78:81]
	ds_read_b128 v[82:85], v188 offset:57600
	s_waitcnt lgkmcnt(0)
	v_mfma_f32_16x16x32_bf16 v[74:77], v[82:85], v[20:23], v[74:77]
	v_mfma_f32_16x16x32_bf16 v[78:81], v[82:85], v[48:51], v[78:81]
	ds_read_b128 v[82:85], v187 offset:57600
	s_waitcnt lgkmcnt(0)
	v_mfma_f32_16x16x32_bf16 v[74:77], v[82:85], v[24:27], v[74:77]
	v_mfma_f32_16x16x32_bf16 v[78:81], v[82:85], v[44:47], v[78:81]
	ds_read_b128 v[82:85], v186 offset:57600
	s_waitcnt lgkmcnt(0)
	v_mfma_f32_16x16x32_bf16 v[74:77], v[82:85], v[28:31], v[74:77]
	v_mfma_f32_16x16x32_bf16 v[78:81], v[82:85], v[40:43], v[78:81]
	ds_read_b128 v[82:85], v137 offset:57600
	s_waitcnt lgkmcnt(0)
	v_mfma_f32_16x16x32_bf16 v[74:77], v[82:85], v[32:35], v[74:77]
	s_nop 7
	v_pk_mul_f32 v[74:75], v[74:75], v[136:137] op_sel_hi:[1,0]
	v_mfma_f32_16x16x32_bf16 v[78:81], v[82:85], v[36:39], v[78:81]
	v_mul_f32_e64 v76, v76, v136
	v_mul_f32_e64 v77, v77, v136
	v_cvt_pk_bf16_f32 v74, v74, v75
	v_cvt_pk_bf16_f32 v75, v76, v77
	s_nop 3
	v_pk_mul_f32 v[76:77], v[78:79], v[68:69] op_sel_hi:[1,0]
	v_pk_mul_f32 v[78:79], v[80:81], v[68:69] op_sel_hi:[1,0]
	v_cvt_pk_bf16_f32 v76, v76, v77
	v_cvt_pk_bf16_f32 v77, v78, v79
	global_store_dwordx2 v[70:71], v[74:75], off offset:224
	global_store_dwordx2 v[72:73], v[76:77], off offset:224
	s_waitcnt vmcnt(0)
	s_waitcnt lgkmcnt(0)
	s_barrier
	s_cbranch_vccz .LBB0_1069
	s_mov_b32 m0, s29
	s_nop 0
	buffer_load_dwordx4 v140, s[12:15], 0 offen lds
	s_mov_b32 m0, s30
	s_nop 0
	buffer_load_dwordx4 v141, s[12:15], 0 offen lds
	s_mov_b32 m0, s31
	s_nop 0
	buffer_load_dwordx4 v142, s[12:15], 0 offen lds
	s_mov_b32 m0, s35
	s_nop 0
	buffer_load_dwordx4 v143, s[12:15], 0 offen lds
	s_mov_b32 m0, s37
	s_nop 0
	buffer_load_dwordx4 v144, s[12:15], 0 offen lds
	s_mov_b32 m0, s39
	s_nop 0
	buffer_load_dwordx4 v145, s[12:15], 0 offen lds
	s_mov_b32 m0, s41
	s_nop 0
	buffer_load_dwordx4 v146, s[12:15], 0 offen lds
	s_mov_b32 m0, s48
	s_nop 0
	buffer_load_dwordx4 v147, s[12:15], 0 offen lds

.LBB0_1072:
	s_cmp_eq_u32 s100, 1
	s_cbranch_scc1 .Lqs7
	s_cmp_gt_i32 s91, 8
	s_cselect_b64 s[2:3], -1, 0
	s_and_b64 s[0:1], s[4:5], s[2:3]
	s_andn2_b64 vcc, exec, s[0:1]
	s_cbranch_vccnz .LBB0_1128
	s_cmp_gt_u32 s80, 63
	s_waitcnt lgkmcnt(0)
	s_mov_b64 s[8:9], 0
	s_cbranch_scc1 .LBB0_1075
	v_mbcnt_hi_u32_b32 v0, -1, v217
	v_cmp_eq_u32_e32 vcc, 0, v0
	s_and_b64 s[8:9], vcc, exec

.LBB0_1135:
	s_cmp_eq_u32 s100, 1
	s_cbranch_scc0 .Lqo_p5i
	s_lshl_b32 s55, s98, 1
	s_mov_b32 s54, s99

.LBB0_1147:
	s_cmp_eq_u32 s100, 1
	s_cbranch_scc0 .Lqo_p5n
	s_lshl_b32 s51, s98, 1
	s_add_i32 s51, s51, s39
	s_mov_b32 s43, s99

.LBB0_1151:
	s_lshl_b32 s14, s55, 8
	s_add_i32 s14, s14, s48
	s_lshl_b32 s15, s54, 8
	s_or_b32 s15, s15, s50
	v_and_b32_e32 v219, 15, v136
	v_or_b32_e32 v219, s14, v219
	v_and_b32_e32 v218, 48, v136
	v_add_u32_e32 v218, s15, v218
	v_lshl_add_u32 v141, v219, 10, v218
	v_lshlrev_b32_e32 v141, 1, v141
	v_add_lshl_u32 v237, v136, s14, 2
	v_add_u32_e32 v142, 0x8000, v141
	v_add_u32_e32 v146, 0x10000, v141
	v_add_u32_e32 v147, 0x18000, v141
	v_add_u32_e32 v216, 0x40000, v141
	v_add_u32_e32 v234, 0x48000, v141
	v_add_u32_e32 v235, 0x50000, v141
	v_add_u32_e32 v236, 0x58000, v141
	global_load_dwordx4 v[132:135], v141, s[22:23]
	global_load_dwordx4 v[148:151], v141, s[22:23] offset:16
	global_load_dwordx4 v[152:155], v142, s[22:23]
	global_load_dwordx4 v[156:159], v142, s[22:23] offset:16
	global_load_dwordx4 v[160:163], v146, s[22:23]
	global_load_dwordx4 v[164:167], v146, s[22:23] offset:16
	global_load_dwordx4 v[168:171], v147, s[22:23]
	global_load_dwordx4 v[172:175], v147, s[22:23] offset:16
	global_load_dwordx4 v[176:179], v216, s[22:23]
	global_load_dwordx4 v[180:183], v216, s[22:23] offset:16
	global_load_dwordx4 v[184:187], v234, s[22:23]
	global_load_dwordx4 v[188:191], v234, s[22:23] offset:16
	global_load_dwordx4 v[192:195], v235, s[22:23]
	global_load_dwordx4 v[196:199], v235, s[22:23] offset:16
	global_load_dwordx4 v[200:203], v236, s[22:23]
	global_load_dwordx4 v[204:207], v236, s[22:23] offset:16
	s_waitcnt vmcnt(14)
	v_lshlrev_b32_e32 v218, 16, v132
	v_and_b32_e32 v219, 0xffff0000, v132
	v_lshlrev_b32_e32 v220, 16, v133
	v_and_b32_e32 v221, 0xffff0000, v133
	v_lshlrev_b32_e32 v222, 16, v134
	v_and_b32_e32 v223, 0xffff0000, v134
	v_lshlrev_b32_e32 v224, 16, v135
	v_and_b32_e32 v225, 0xffff0000, v135
	v_lshlrev_b32_e32 v226, 16, v148
	v_and_b32_e32 v227, 0xffff0000, v148
	v_lshlrev_b32_e32 v228, 16, v149
	v_and_b32_e32 v229, 0xffff0000, v149
	v_lshlrev_b32_e32 v230, 16, v150
	v_and_b32_e32 v231, 0xffff0000, v150
	v_lshlrev_b32_e32 v232, 16, v151
	v_and_b32_e32 v233, 0xffff0000, v151
	v_pk_add_f32 v[112:113], v[112:113], v[218:219]
	v_pk_add_f32 v[114:115], v[114:115], v[220:221]
	v_pk_add_f32 v[116:117], v[116:117], v[222:223]
	v_pk_add_f32 v[118:119], v[118:119], v[224:225]
	v_pk_add_f32 v[124:125], v[124:125], v[226:227]
	v_pk_add_f32 v[126:127], v[126:127], v[228:229]
	v_pk_add_f32 v[120:121], v[120:121], v[230:231]
	v_pk_add_f32 v[122:123], v[122:123], v[232:233]
	v_mul_f32_e32 v132, v112, v112
	v_fmac_f32_e32 v132, v113, v113
	v_mul_f32_e32 v219, v114, v114
	v_fmac_f32_e32 v219, v115, v115
	v_mul_f32_e32 v220, v116, v116
	v_fmac_f32_e32 v220, v117, v117
	v_mul_f32_e32 v218, v118, v118
	v_fmac_f32_e32 v218, v119, v119
	v_fmac_f32_e32 v132, v124, v124
	v_fmac_f32_e32 v132, v125, v125
	v_fmac_f32_e32 v219, v126, v126
	v_fmac_f32_e32 v219, v127, v127
	v_fmac_f32_e32 v220, v120, v120
	v_fmac_f32_e32 v220, v121, v121
	v_fmac_f32_e32 v218, v122, v122
	v_fmac_f32_e32 v218, v123, v123
	v_add_f32_e32 v132, v132, v219
	v_add_f32_e32 v220, v220, v218
	v_add_f32_e32 v132, v132, v220
	v_cvt_pk_bf16_f32 v208, v112, v113
	v_cvt_pk_bf16_f32 v209, v114, v115
	v_cvt_pk_bf16_f32 v210, v116, v117
	v_cvt_pk_bf16_f32 v211, v118, v119
	v_cvt_pk_bf16_f32 v212, v124, v125
	v_cvt_pk_bf16_f32 v213, v126, v127
	v_cvt_pk_bf16_f32 v214, v120, v121
	v_cvt_pk_bf16_f32 v215, v122, v123
	global_store_dwordx4 v141, v[208:211], s[22:23]
	global_store_dwordx4 v141, v[212:215], s[22:23] offset:16
	s_waitcnt vmcnt(14)
	v_lshlrev_b32_e32 v218, 16, v152
	v_and_b32_e32 v219, 0xffff0000, v152
	v_lshlrev_b32_e32 v220, 16, v153
	v_and_b32_e32 v221, 0xffff0000, v153
	v_lshlrev_b32_e32 v222, 16, v154
	v_and_b32_e32 v223, 0xffff0000, v154
	v_lshlrev_b32_e32 v224, 16, v155
	v_and_b32_e32 v225, 0xffff0000, v155
	v_lshlrev_b32_e32 v226, 16, v156
	v_and_b32_e32 v227, 0xffff0000, v156
	v_lshlrev_b32_e32 v228, 16, v157
	v_and_b32_e32 v229, 0xffff0000, v157
	v_lshlrev_b32_e32 v230, 16, v158
	v_and_b32_e32 v231, 0xffff0000, v158
	v_lshlrev_b32_e32 v232, 16, v159
	v_and_b32_e32 v233, 0xffff0000, v159
	v_pk_add_f32 v[96:97], v[96:97], v[218:219]
	v_pk_add_f32 v[98:99], v[98:99], v[220:221]
	v_pk_add_f32 v[100:101], v[100:101], v[222:223]
	v_pk_add_f32 v[102:103], v[102:103], v[224:225]
	v_pk_add_f32 v[108:109], v[108:109], v[226:227]
	v_pk_add_f32 v[110:111], v[110:111], v[228:229]
	v_pk_add_f32 v[104:105], v[104:105], v[230:231]
	v_pk_add_f32 v[106:107], v[106:107], v[232:233]
	v_mul_f32_e32 v152, v96, v96
	v_fmac_f32_e32 v152, v97, v97
	v_mul_f32_e32 v219, v98, v98
	v_fmac_f32_e32 v219, v99, v99
	v_mul_f32_e32 v220, v100, v100
	v_fmac_f32_e32 v220, v101, v101
	v_mul_f32_e32 v218, v102, v102
	v_fmac_f32_e32 v218, v103, v103
	v_fmac_f32_e32 v152, v108, v108
	v_fmac_f32_e32 v152, v109, v109
	v_fmac_f32_e32 v219, v110, v110
	v_fmac_f32_e32 v219, v111, v111
	v_fmac_f32_e32 v220, v104, v104
	v_fmac_f32_e32 v220, v105, v105
	v_fmac_f32_e32 v218, v106, v106
	v_fmac_f32_e32 v218, v107, v107
	v_add_f32_e32 v152, v152, v219
	v_add_f32_e32 v220, v220, v218
	v_add_f32_e32 v152, v152, v220
	v_cvt_pk_bf16_f32 v208, v96, v97
	v_cvt_pk_bf16_f32 v209, v98, v99
	v_cvt_pk_bf16_f32 v210, v100, v101
	v_cvt_pk_bf16_f32 v211, v102, v103
	v_cvt_pk_bf16_f32 v212, v108, v109
	v_cvt_pk_bf16_f32 v213, v110, v111
	v_cvt_pk_bf16_f32 v214, v104, v105
	v_cvt_pk_bf16_f32 v215, v106, v107
	global_store_dwordx4 v142, v[208:211], s[22:23]
	global_store_dwordx4 v142, v[212:215], s[22:23] offset:16
	s_waitcnt vmcnt(14)
	v_lshlrev_b32_e32 v218, 16, v160
	v_and_b32_e32 v219, 0xffff0000, v160
	v_lshlrev_b32_e32 v220, 16, v161
	v_and_b32_e32 v221, 0xffff0000, v161
	v_lshlrev_b32_e32 v222, 16, v162
	v_and_b32_e32 v223, 0xffff0000, v162
	v_lshlrev_b32_e32 v224, 16, v163
	v_and_b32_e32 v225, 0xffff0000, v163
	v_lshlrev_b32_e32 v226, 16, v164
	v_and_b32_e32 v227, 0xffff0000, v164
	v_lshlrev_b32_e32 v228, 16, v165
	v_and_b32_e32 v229, 0xffff0000, v165
	v_lshlrev_b32_e32 v230, 16, v166
	v_and_b32_e32 v231, 0xffff0000, v166
	v_lshlrev_b32_e32 v232, 16, v167
	v_and_b32_e32 v233, 0xffff0000, v167
	v_pk_add_f32 v[80:81], v[80:81], v[218:219]
	v_pk_add_f32 v[82:83], v[82:83], v[220:221]
	v_pk_add_f32 v[84:85], v[84:85], v[222:223]
	v_pk_add_f32 v[86:87], v[86:87], v[224:225]
	v_pk_add_f32 v[92:93], v[92:93], v[226:227]
	v_pk_add_f32 v[94:95], v[94:95], v[228:229]
	v_pk_add_f32 v[88:89], v[88:89], v[230:231]
	v_pk_add_f32 v[90:91], v[90:91], v[232:233]
	v_mul_f32_e32 v160, v80, v80
	v_fmac_f32_e32 v160, v81, v81
	v_mul_f32_e32 v219, v82, v82
	v_fmac_f32_e32 v219, v83, v83
	v_mul_f32_e32 v220, v84, v84
	v_fmac_f32_e32 v220, v85, v85
	v_mul_f32_e32 v218, v86, v86
	v_fmac_f32_e32 v218, v87, v87
	v_fmac_f32_e32 v160, v92, v92
	v_fmac_f32_e32 v160, v93, v93
	v_fmac_f32_e32 v219, v94, v94
	v_fmac_f32_e32 v219, v95, v95
	v_fmac_f32_e32 v220, v88, v88
	v_fmac_f32_e32 v220, v89, v89
	v_fmac_f32_e32 v218, v90, v90
	v_fmac_f32_e32 v218, v91, v91
	v_add_f32_e32 v160, v160, v219
	v_add_f32_e32 v220, v220, v218
	v_add_f32_e32 v160, v160, v220
	v_cvt_pk_bf16_f32 v208, v80, v81
	v_cvt_pk_bf16_f32 v209, v82, v83
	v_cvt_pk_bf16_f32 v210, v84, v85
	v_cvt_pk_bf16_f32 v211, v86, v87
	v_cvt_pk_bf16_f32 v212, v92, v93
	v_cvt_pk_bf16_f32 v213, v94, v95
	v_cvt_pk_bf16_f32 v214, v88, v89
	v_cvt_pk_bf16_f32 v215, v90, v91
	global_store_dwordx4 v146, v[208:211], s[22:23]
	global_store_dwordx4 v146, v[212:215], s[22:23] offset:16
	s_waitcnt vmcnt(14)
	v_lshlrev_b32_e32 v218, 16, v168
	v_and_b32_e32 v219, 0xffff0000, v168
	v_lshlrev_b32_e32 v220, 16, v169
	v_and_b32_e32 v221, 0xffff0000, v169
	v_lshlrev_b32_e32 v222, 16, v170
	v_and_b32_e32 v223, 0xffff0000, v170
	v_lshlrev_b32_e32 v224, 16, v171
	v_and_b32_e32 v225, 0xffff0000, v171
	v_lshlrev_b32_e32 v226, 16, v172
	v_and_b32_e32 v227, 0xffff0000, v172
	v_lshlrev_b32_e32 v228, 16, v173
	v_and_b32_e32 v229, 0xffff0000, v173
	v_lshlrev_b32_e32 v230, 16, v174
	v_and_b32_e32 v231, 0xffff0000, v174
	v_lshlrev_b32_e32 v232, 16, v175
	v_and_b32_e32 v233, 0xffff0000, v175
	v_pk_add_f32 v[64:65], v[64:65], v[218:219]
	v_pk_add_f32 v[66:67], v[66:67], v[220:221]
	v_pk_add_f32 v[68:69], v[68:69], v[222:223]
	v_pk_add_f32 v[70:71], v[70:71], v[224:225]
	v_pk_add_f32 v[76:77], v[76:77], v[226:227]
	v_pk_add_f32 v[78:79], v[78:79], v[228:229]
	v_pk_add_f32 v[72:73], v[72:73], v[230:231]
	v_pk_add_f32 v[74:75], v[74:75], v[232:233]
	v_mul_f32_e32 v168, v64, v64
	v_fmac_f32_e32 v168, v65, v65
	v_mul_f32_e32 v219, v66, v66
	v_fmac_f32_e32 v219, v67, v67
	v_mul_f32_e32 v220, v68, v68
	v_fmac_f32_e32 v220, v69, v69
	v_mul_f32_e32 v218, v70, v70
	v_fmac_f32_e32 v218, v71, v71
	v_fmac_f32_e32 v168, v76, v76
	v_fmac_f32_e32 v168, v77, v77
	v_fmac_f32_e32 v219, v78, v78
	v_fmac_f32_e32 v219, v79, v79
	v_fmac_f32_e32 v220, v72, v72
	v_fmac_f32_e32 v220, v73, v73
	v_fmac_f32_e32 v218, v74, v74
	v_fmac_f32_e32 v218, v75, v75
	v_add_f32_e32 v168, v168, v219
	v_add_f32_e32 v220, v220, v218
	v_add_f32_e32 v168, v168, v220
	v_cvt_pk_bf16_f32 v208, v64, v65
	v_cvt_pk_bf16_f32 v209, v66, v67
	v_cvt_pk_bf16_f32 v210, v68, v69
	v_cvt_pk_bf16_f32 v211, v70, v71
	v_cvt_pk_bf16_f32 v212, v76, v77
	v_cvt_pk_bf16_f32 v213, v78, v79
	v_cvt_pk_bf16_f32 v214, v72, v73
	v_cvt_pk_bf16_f32 v215, v74, v75
	global_store_dwordx4 v147, v[208:211], s[22:23]
	global_store_dwordx4 v147, v[212:215], s[22:23] offset:16
	s_waitcnt vmcnt(14)
	v_lshlrev_b32_e32 v218, 16, v176
	v_and_b32_e32 v219, 0xffff0000, v176
	v_lshlrev_b32_e32 v220, 16, v177
	v_and_b32_e32 v221, 0xffff0000, v177
	v_lshlrev_b32_e32 v222, 16, v178
	v_and_b32_e32 v223, 0xffff0000, v178
	v_lshlrev_b32_e32 v224, 16, v179
	v_and_b32_e32 v225, 0xffff0000, v179
	v_lshlrev_b32_e32 v226, 16, v180
	v_and_b32_e32 v227, 0xffff0000, v180
	v_lshlrev_b32_e32 v228, 16, v181
	v_and_b32_e32 v229, 0xffff0000, v181
	v_lshlrev_b32_e32 v230, 16, v182
	v_and_b32_e32 v231, 0xffff0000, v182
	v_lshlrev_b32_e32 v232, 16, v183
	v_and_b32_e32 v233, 0xffff0000, v183
	v_pk_add_f32 v[48:49], v[48:49], v[218:219]
	v_pk_add_f32 v[50:51], v[50:51], v[220:221]
	v_pk_add_f32 v[52:53], v[52:53], v[222:223]
	v_pk_add_f32 v[54:55], v[54:55], v[224:225]
	v_pk_add_f32 v[60:61], v[60:61], v[226:227]
	v_pk_add_f32 v[62:63], v[62:63], v[228:229]
	v_pk_add_f32 v[56:57], v[56:57], v[230:231]
	v_pk_add_f32 v[58:59], v[58:59], v[232:233]
	v_mul_f32_e32 v176, v48, v48
	v_fmac_f32_e32 v176, v49, v49
	v_mul_f32_e32 v219, v50, v50
	v_fmac_f32_e32 v219, v51, v51
	v_mul_f32_e32 v220, v52, v52
	v_fmac_f32_e32 v220, v53, v53
	v_mul_f32_e32 v218, v54, v54
	v_fmac_f32_e32 v218, v55, v55
	v_fmac_f32_e32 v176, v60, v60
	v_fmac_f32_e32 v176, v61, v61
	v_fmac_f32_e32 v219, v62, v62
	v_fmac_f32_e32 v219, v63, v63
	v_fmac_f32_e32 v220, v56, v56
	v_fmac_f32_e32 v220, v57, v57
	v_fmac_f32_e32 v218, v58, v58
	v_fmac_f32_e32 v218, v59, v59
	v_add_f32_e32 v176, v176, v219
	v_add_f32_e32 v220, v220, v218
	v_add_f32_e32 v176, v176, v220
	v_cvt_pk_bf16_f32 v208, v48, v49
	v_cvt_pk_bf16_f32 v209, v50, v51
	v_cvt_pk_bf16_f32 v210, v52, v53
	v_cvt_pk_bf16_f32 v211, v54, v55
	v_cvt_pk_bf16_f32 v212, v60, v61
	v_cvt_pk_bf16_f32 v213, v62, v63
	v_cvt_pk_bf16_f32 v214, v56, v57
	v_cvt_pk_bf16_f32 v215, v58, v59
	global_store_dwordx4 v216, v[208:211], s[22:23]
	global_store_dwordx4 v216, v[212:215], s[22:23] offset:16
	s_waitcnt vmcnt(14)
	v_lshlrev_b32_e32 v218, 16, v184
	v_and_b32_e32 v219, 0xffff0000, v184
	v_lshlrev_b32_e32 v220, 16, v185
	v_and_b32_e32 v221, 0xffff0000, v185
	v_lshlrev_b32_e32 v222, 16, v186
	v_and_b32_e32 v223, 0xffff0000, v186
	v_lshlrev_b32_e32 v224, 16, v187
	v_and_b32_e32 v225, 0xffff0000, v187
	v_lshlrev_b32_e32 v226, 16, v188
	v_and_b32_e32 v227, 0xffff0000, v188
	v_lshlrev_b32_e32 v228, 16, v189
	v_and_b32_e32 v229, 0xffff0000, v189
	v_lshlrev_b32_e32 v230, 16, v190
	v_and_b32_e32 v231, 0xffff0000, v190
	v_lshlrev_b32_e32 v232, 16, v191
	v_and_b32_e32 v233, 0xffff0000, v191
	v_pk_add_f32 v[32:33], v[32:33], v[218:219]
	v_pk_add_f32 v[34:35], v[34:35], v[220:221]
	v_pk_add_f32 v[36:37], v[36:37], v[222:223]
	v_pk_add_f32 v[38:39], v[38:39], v[224:225]
	v_pk_add_f32 v[44:45], v[44:45], v[226:227]
	v_pk_add_f32 v[46:47], v[46:47], v[228:229]
	v_pk_add_f32 v[40:41], v[40:41], v[230:231]
	v_pk_add_f32 v[42:43], v[42:43], v[232:233]
	v_mul_f32_e32 v184, v32, v32
	v_fmac_f32_e32 v184, v33, v33
	v_mul_f32_e32 v219, v34, v34
	v_fmac_f32_e32 v219, v35, v35
	v_mul_f32_e32 v220, v36, v36
	v_fmac_f32_e32 v220, v37, v37
	v_mul_f32_e32 v218, v38, v38
	v_fmac_f32_e32 v218, v39, v39
	v_fmac_f32_e32 v184, v44, v44
	v_fmac_f32_e32 v184, v45, v45
	v_fmac_f32_e32 v219, v46, v46
	v_fmac_f32_e32 v219, v47, v47
	v_fmac_f32_e32 v220, v40, v40
	v_fmac_f32_e32 v220, v41, v41
	v_fmac_f32_e32 v218, v42, v42
	v_fmac_f32_e32 v218, v43, v43
	v_add_f32_e32 v184, v184, v219
	v_add_f32_e32 v220, v220, v218
	v_add_f32_e32 v184, v184, v220
	v_cvt_pk_bf16_f32 v208, v32, v33
	v_cvt_pk_bf16_f32 v209, v34, v35
	v_cvt_pk_bf16_f32 v210, v36, v37
	v_cvt_pk_bf16_f32 v211, v38, v39
	v_cvt_pk_bf16_f32 v212, v44, v45
	v_cvt_pk_bf16_f32 v213, v46, v47
	v_cvt_pk_bf16_f32 v214, v40, v41
	v_cvt_pk_bf16_f32 v215, v42, v43
	global_store_dwordx4 v234, v[208:211], s[22:23]
	global_store_dwordx4 v234, v[212:215], s[22:23] offset:16
	s_waitcnt vmcnt(14)
	v_lshlrev_b32_e32 v218, 16, v192
	v_and_b32_e32 v219, 0xffff0000, v192
	v_lshlrev_b32_e32 v220, 16, v193
	v_and_b32_e32 v221, 0xffff0000, v193
	v_lshlrev_b32_e32 v222, 16, v194
	v_and_b32_e32 v223, 0xffff0000, v194
	v_lshlrev_b32_e32 v224, 16, v195
	v_and_b32_e32 v225, 0xffff0000, v195
	v_lshlrev_b32_e32 v226, 16, v196
	v_and_b32_e32 v227, 0xffff0000, v196
	v_lshlrev_b32_e32 v228, 16, v197
	v_and_b32_e32 v229, 0xffff0000, v197
	v_lshlrev_b32_e32 v230, 16, v198
	v_and_b32_e32 v231, 0xffff0000, v198
	v_lshlrev_b32_e32 v232, 16, v199
	v_and_b32_e32 v233, 0xffff0000, v199
	v_pk_add_f32 v[16:17], v[16:17], v[218:219]
	v_pk_add_f32 v[18:19], v[18:19], v[220:221]
	v_pk_add_f32 v[20:21], v[20:21], v[222:223]
	v_pk_add_f32 v[22:23], v[22:23], v[224:225]
	v_pk_add_f32 v[28:29], v[28:29], v[226:227]
	v_pk_add_f32 v[30:31], v[30:31], v[228:229]
	v_pk_add_f32 v[24:25], v[24:25], v[230:231]
	v_pk_add_f32 v[26:27], v[26:27], v[232:233]
	v_mul_f32_e32 v192, v16, v16
	v_fmac_f32_e32 v192, v17, v17
	v_mul_f32_e32 v219, v18, v18
	v_fmac_f32_e32 v219, v19, v19
	v_mul_f32_e32 v220, v20, v20
	v_fmac_f32_e32 v220, v21, v21
	v_mul_f32_e32 v218, v22, v22
	v_fmac_f32_e32 v218, v23, v23
	v_fmac_f32_e32 v192, v28, v28
	v_fmac_f32_e32 v192, v29, v29
	v_fmac_f32_e32 v219, v30, v30
	v_fmac_f32_e32 v219, v31, v31
	v_fmac_f32_e32 v220, v24, v24
	v_fmac_f32_e32 v220, v25, v25
	v_fmac_f32_e32 v218, v26, v26
	v_fmac_f32_e32 v218, v27, v27
	v_add_f32_e32 v192, v192, v219
	v_add_f32_e32 v220, v220, v218
	v_add_f32_e32 v192, v192, v220
	v_cvt_pk_bf16_f32 v208, v16, v17
	v_cvt_pk_bf16_f32 v209, v18, v19
	v_cvt_pk_bf16_f32 v210, v20, v21
	v_cvt_pk_bf16_f32 v211, v22, v23
	v_cvt_pk_bf16_f32 v212, v28, v29
	v_cvt_pk_bf16_f32 v213, v30, v31
	v_cvt_pk_bf16_f32 v214, v24, v25
	v_cvt_pk_bf16_f32 v215, v26, v27
	global_store_dwordx4 v235, v[208:211], s[22:23]
	global_store_dwordx4 v235, v[212:215], s[22:23] offset:16
	s_waitcnt vmcnt(14)
	v_lshlrev_b32_e32 v218, 16, v200
	v_and_b32_e32 v219, 0xffff0000, v200
	v_lshlrev_b32_e32 v220, 16, v201
	v_and_b32_e32 v221, 0xffff0000, v201
	v_lshlrev_b32_e32 v222, 16, v202
	v_and_b32_e32 v223, 0xffff0000, v202
	v_lshlrev_b32_e32 v224, 16, v203
	v_and_b32_e32 v225, 0xffff0000, v203
	v_lshlrev_b32_e32 v226, 16, v204
	v_and_b32_e32 v227, 0xffff0000, v204
	v_lshlrev_b32_e32 v228, 16, v205
	v_and_b32_e32 v229, 0xffff0000, v205
	v_lshlrev_b32_e32 v230, 16, v206
	v_and_b32_e32 v231, 0xffff0000, v206
	v_lshlrev_b32_e32 v232, 16, v207
	v_and_b32_e32 v233, 0xffff0000, v207
	v_pk_add_f32 v[0:1], v[0:1], v[218:219]
	v_pk_add_f32 v[2:3], v[2:3], v[220:221]
	v_pk_add_f32 v[4:5], v[4:5], v[222:223]
	v_pk_add_f32 v[6:7], v[6:7], v[224:225]
	v_pk_add_f32 v[12:13], v[12:13], v[226:227]
	v_pk_add_f32 v[14:15], v[14:15], v[228:229]
	v_pk_add_f32 v[8:9], v[8:9], v[230:231]
	v_pk_add_f32 v[10:11], v[10:11], v[232:233]
	v_mul_f32_e32 v200, v0, v0
	v_fmac_f32_e32 v200, v1, v1
	v_mul_f32_e32 v219, v2, v2
	v_fmac_f32_e32 v219, v3, v3
	v_mul_f32_e32 v220, v4, v4
	v_fmac_f32_e32 v220, v5, v5
	v_mul_f32_e32 v218, v6, v6
	v_fmac_f32_e32 v218, v7, v7
	v_fmac_f32_e32 v200, v12, v12
	v_fmac_f32_e32 v200, v13, v13
	v_fmac_f32_e32 v219, v14, v14
	v_fmac_f32_e32 v219, v15, v15
	v_fmac_f32_e32 v220, v8, v8
	v_fmac_f32_e32 v220, v9, v9
	v_fmac_f32_e32 v218, v10, v10
	v_fmac_f32_e32 v218, v11, v11
	v_add_f32_e32 v200, v200, v219
	v_add_f32_e32 v220, v220, v218
	v_add_f32_e32 v200, v200, v220
	v_cvt_pk_bf16_f32 v208, v0, v1
	v_cvt_pk_bf16_f32 v209, v2, v3
	v_cvt_pk_bf16_f32 v210, v4, v5
	v_cvt_pk_bf16_f32 v211, v6, v7
	v_cvt_pk_bf16_f32 v212, v12, v13
	v_cvt_pk_bf16_f32 v213, v14, v15
	v_cvt_pk_bf16_f32 v214, v8, v9
	v_cvt_pk_bf16_f32 v215, v10, v11
	global_store_dwordx4 v236, v[208:211], s[22:23]
	global_store_dwordx4 v236, v[212:215], s[22:23] offset:16
	s_nop 1
	v_permlane32_swap_b32_e32 v132, v160
	v_permlane32_swap_b32_e32 v152, v168
	v_add_f32_e32 v132, v132, v160
	v_add_f32_e32 v152, v152, v168
	s_nop 1
	v_permlane16_swap_b32_e32 v132, v152
	v_add_f32_e32 v132, v132, v152
	global_atomic_add_f32 v237, v132, s[24:25]
	s_nop 1
	v_permlane32_swap_b32_e32 v176, v192
	v_permlane32_swap_b32_e32 v184, v200
	v_add_f32_e32 v176, v176, v192
	v_add_f32_e32 v184, v184, v200
	s_nop 1
	v_permlane16_swap_b32_e32 v176, v184
	v_add_f32_e32 v176, v176, v184
	global_atomic_add_f32 v237, v176, s[24:25] offset:512
	s_andn2_b64 vcc, exec, s[2:3]
	s_mov_b64 s[2:3], -1
	s_cbranch_vccnz .LBB0_1140
	v_mov_b32_e32 v8, 0
	s_andn2_b64 vcc, exec, s[20:21]
	s_nop 0
	v_mfma_f32_4x4x1_16b_f32 v[112:115], v8, v8, 0
	s_nop 0
	v_mfma_f32_4x4x1_16b_f32 v[116:119], v8, v8, 0
	s_nop 0
	v_mfma_f32_4x4x1_16b_f32 v[96:99], v8, v8, 0
	s_nop 0
	v_mfma_f32_4x4x1_16b_f32 v[100:103], v8, v8, 0
	s_nop 0
	v_mfma_f32_4x4x1_16b_f32 v[80:83], v8, v8, 0
	s_nop 0
	v_mfma_f32_4x4x1_16b_f32 v[84:87], v8, v8, 0
	s_nop 0
	v_mfma_f32_4x4x1_16b_f32 v[64:67], v8, v8, 0
	s_nop 0
	v_mfma_f32_4x4x1_16b_f32 v[68:71], v8, v8, 0
	s_nop 0
	v_mfma_f32_4x4x1_16b_f32 v[124:127], v8, v8, 0
	s_nop 0
	v_mfma_f32_4x4x1_16b_f32 v[120:123], v8, v8, 0
	s_nop 0
	v_mfma_f32_4x4x1_16b_f32 v[108:111], v8, v8, 0
	s_nop 0
	v_mfma_f32_4x4x1_16b_f32 v[104:107], v8, v8, 0
	s_nop 0
	v_mfma_f32_4x4x1_16b_f32 v[92:95], v8, v8, 0
	s_nop 0
	v_mfma_f32_4x4x1_16b_f32 v[88:91], v8, v8, 0
	s_nop 0
	v_mfma_f32_4x4x1_16b_f32 v[76:79], v8, v8, 0
	s_nop 0
	v_mfma_f32_4x4x1_16b_f32 v[72:75], v8, v8, 0
	s_nop 0
	v_mfma_f32_4x4x1_16b_f32 v[48:51], v8, v8, 0
	s_nop 0
	v_mfma_f32_4x4x1_16b_f32 v[52:55], v8, v8, 0
	s_nop 0
	v_mfma_f32_4x4x1_16b_f32 v[32:35], v8, v8, 0
	s_nop 0
	v_mfma_f32_4x4x1_16b_f32 v[36:39], v8, v8, 0
	s_nop 0
	v_mfma_f32_4x4x1_16b_f32 v[16:19], v8, v8, 0
	s_nop 0
	v_mfma_f32_4x4x1_16b_f32 v[20:23], v8, v8, 0
	s_waitcnt lgkmcnt(0)
	v_mfma_f32_4x4x1_16b_f32 v[0:3], v8, v8, 0
	s_nop 0
	v_mfma_f32_4x4x1_16b_f32 v[4:7], v8, v8, 0
	s_nop 0
	v_mfma_f32_4x4x1_16b_f32 v[60:63], v8, v8, 0
	s_nop 0
	v_mfma_f32_4x4x1_16b_f32 v[56:59], v8, v8, 0
	s_nop 0
	v_mfma_f32_4x4x1_16b_f32 v[44:47], v8, v8, 0
	s_nop 0
	v_mfma_f32_4x4x1_16b_f32 v[40:43], v8, v8, 0
	s_nop 0
	v_mfma_f32_4x4x1_16b_f32 v[28:31], v8, v8, 0
	s_nop 0
	v_mfma_f32_4x4x1_16b_f32 v[24:27], v8, v8, 0
	s_nop 0
	v_mfma_f32_4x4x1_16b_f32 v[12:15], v8, v8, 0
	s_nop 0
	v_mfma_f32_4x4x1_16b_f32 v[8:11], v8, v8, 0
	s_cbranch_vccnz .LBB0_1139
	s_barrier
	s_branch .LBB0_1139

.Lqs7:
	s_waitcnt vmcnt(0) lgkmcnt(0)
	s_barrier
	s_cmp_gt_u32 s80, 63
	s_cbranch_scc1 .Lqs7_wait
	s_add_u32 s8, s18, 0xc0000
	s_addc_u32 s9, s19, 0
	s_mov_b64 s[10:11], exec
	s_mov_b64 exec, 1
	s_lshl_b32 s0, s98, 8
	s_add_i32 s0, s0, 224
	v_mov_b32_e32 v0, s0
	v_mov_b32_e32 v1, 1
	global_atomic_add v0, v1, s[8:9]
	buffer_inv sc1
	s_mov_b32 s1, 0
.Lqs7_spin:
	global_load_dword v2, v0, s[8:9] sc1
	s_waitcnt vmcnt(0)
	v_readfirstlane_b32 s0, v2
	s_nop 3
	s_cmp_ge_u32 s0, 4
	s_cbranch_scc1 .Lqs7_done
	s_sleep 1
	s_add_u32 s1, s1, 1
	s_cmp_lt_u32 s1, 0x4000
	s_cbranch_scc1 .Lqs7_spin
.Lqs7_done:
	s_waitcnt vmcnt(0)
	s_mov_b64 exec, s[10:11]
.Lqs7_wait:
	s_barrier
	s_mov_b64 s[2:3], -1
	s_branch .LBB0_1128
.Lqs6:
	s_waitcnt vmcnt(0) lgkmcnt(0)
	s_barrier
	buffer_inv sc1
	s_waitcnt vmcnt(0)
	s_barrier
	s_mov_b64 s[2:3], -1
	s_branch .LBB0_1063
.Lqs5:
	s_waitcnt vmcnt(0) lgkmcnt(0)
	s_barrier
	s_cmp_gt_u32 s80, 63
	s_cbranch_scc1 .Lqs5_wait
	s_add_u32 s8, s18, 0xc0000
	s_addc_u32 s9, s19, 0
	s_mov_b64 s[10:11], exec
	s_mov_b64 exec, 1
	s_lshl_b32 s0, s98, 8
	s_add_i32 s0, s0, 160
	v_mov_b32_e32 v0, s0
	v_mov_b32_e32 v1, 1
	global_atomic_add v0, v1, s[8:9]
	buffer_inv sc1
	s_mov_b32 s1, 0

	.amdhsa_kernel _Z9hymba_fwd4Args
		.amdhsa_group_segment_fixed_size 0
		.amdhsa_private_segment_fixed_size 0
		.amdhsa_kernarg_size 560
		.amdhsa_user_sgpr_count 2
		.amdhsa_user_sgpr_dispatch_ptr 0
		.amdhsa_user_sgpr_queue_ptr 0
		.amdhsa_user_sgpr_kernarg_segment_ptr 1
		.amdhsa_user_sgpr_dispatch_id 0
		.amdhsa_user_sgpr_kernarg_preload_length 0
		.amdhsa_user_sgpr_kernarg_preload_offset 0
		.amdhsa_user_sgpr_private_segment_size 0
		.amdhsa_uses_dynamic_stack 0
		.amdhsa_enable_private_segment 0
		.amdhsa_system_sgpr_workgroup_id_x 1
		.amdhsa_system_sgpr_workgroup_id_y 0
		.amdhsa_system_sgpr_workgroup_id_z 0
		.amdhsa_system_sgpr_workgroup_info 0
		.amdhsa_system_vgpr_workitem_id 0
		.amdhsa_next_free_vgpr 255
		.amdhsa_next_free_sgpr 101
		.amdhsa_accum_offset 256
		.amdhsa_reserve_vcc 1
		.amdhsa_float_round_mode_32 0
		.amdhsa_float_round_mode_16_64 0
		.amdhsa_float_denorm_mode_32 3
		.amdhsa_float_denorm_mode_16_64 3
		.amdhsa_dx10_clamp 1
		.amdhsa_ieee_mode 1
		.amdhsa_fp16_overflow 0
		.amdhsa_tg_split 0
		.amdhsa_exception_fp_ieee_invalid_op 0
		.amdhsa_exception_fp_denorm_src 0
		.amdhsa_exception_fp_ieee_div_zero 0
		.amdhsa_exception_fp_ieee_overflow 0
		.amdhsa_exception_fp_ieee_underflow 0
		.amdhsa_exception_fp_ieee_inexact 0
		.amdhsa_exception_int_div_zero 0
	.end_amdhsa_kernel

amdhsa.kernels:
  - .agpr_count:     0
    .args:
      - .offset:         0
        .size:           304
        .value_kind:     by_value
      - .offset:         304
        .size:           4
        .value_kind:     hidden_block_count_x
      - .offset:         308
        .size:           4
        .value_kind:     hidden_block_count_y
      - .offset:         312
        .size:           4
        .value_kind:     hidden_block_count_z
      - .offset:         316
        .size:           2
        .value_kind:     hidden_group_size_x
      - .offset:         318
        .size:           2
        .value_kind:     hidden_group_size_y
      - .offset:         320
        .size:           2
        .value_kind:     hidden_group_size_z
      - .offset:         322
        .size:           2
        .value_kind:     hidden_remainder_x
      - .offset:         324
        .size:           2
        .value_kind:     hidden_remainder_y
      - .offset:         326
        .size:           2
        .value_kind:     hidden_remainder_z
      - .offset:         344
        .size:           8
        .value_kind:     hidden_global_offset_x
      - .offset:         352
        .size:           8
        .value_kind:     hidden_global_offset_y
      - .offset:         360
        .size:           8
        .value_kind:     hidden_global_offset_z
      - .offset:         368
        .size:           2
        .value_kind:     hidden_grid_dims
      - .offset:         424
        .size:           4
        .value_kind:     hidden_dynamic_lds_size
    .group_segment_fixed_size: 0
    .kernarg_segment_align: 8
    .kernarg_segment_size: 560
    .language:       OpenCL C
    .language_version:
      - 2
      - 0
    .max_flat_workgroup_size: 512
    .name:           _Z9hymba_fwd4Args
    .private_segment_fixed_size: 0
    .sgpr_count:     107
    .sgpr_spill_count: 18
    .symbol:         _Z9hymba_fwd4Args.kd
    .uniform_work_group_size: 1
    .uses_dynamic_stack: false
    .vgpr_count:     255
    .vgpr_spill_count: 0
    .wavefront_size: 64
